# v44 + lever 9 (7.12 chain shortening): 57 canonicalising v_max_f32 d,x,x removed from the serial row-max chains of the P3 attention loops (exact no-ops under ieee=1/denorm=3)
# speedup vs baseline: 1.0019x; 1.0004x over previous
; #define LAS __attribute__((address_space(3)))
; __device__ __forceinline__ int v_st(int k, int c) { const int kk = (k & ~0xC) | ((k & 4) << 1) | ((k & 8) >> 1); return ((kk >> 3) * 4 + (c >> 5)) * 512 + ((kk & 7) * 32 + (c & 31)) * 2; }
; template <int MODE>
; __device__ __forceinline__ void attn_pass(const bf16_t* __restrict__ Qb, const bf16_t* __restrict__ Kh, const bf16_t* __restrict__ Vh, const int NT, const int kr0, const int g4, const int map,
;                                           LAS unsigned char* lds, f32x16 (&o)[4]) {
;     ...
;     const bf16_t* Qw = Qb + (long)(wid * QBLK + r32) * LDK + hi * 8;
;     LAS unsigned char* Qs = lds + OFF_Q + wid * (QBLK * 256);
; #pragma unroll
;     for (int d0 = 0; d0 < ND; ++d0) { qr[d0] = *(const bf16x8*)(Qw + d0 * 16); if constexpr (MODE == 0) *(LAS bf16x8*)(Qs + KSWZ(r32, (d0 * 16 + hi * 8) * 2)) = qr[d0]; }
;     const int cbase = MODE == 1 ? map * 128 : 0;
;     const int sr = tid >> 4, sc = (tid & 15) * 8, vst0 = v_st(sr, sc), vst1 = v_st(32 + sr, sc);
;     const int vb0 = (int)(uintptr_t)V_lds + v_rd_base(lane);
;     const int qR = g4 * 4 + (wid >> 1), qc = 32 * (wid & 1) + r32, cs = qc < 8 ? 0 : (qc > 56 ? 48 : qc - 8);
;     const int r0w = qR < 4 ? 0 : (qR > 60 ? 56 : qR - 4);
;     struct { bf16x8 vs0, vs1, ks0, ks1; } sr_[2];
;     ...
;     const int kr1 = tid >> 3, kc1 = map * 64 + (tid & 7) * 8;
;     ...
;     f32x16 pA0, pA1, pB0, pB1; float mnA, mnB, alA, alB; bf16x8 pa0, pa1, pa2, pa3;
;     constexpr int SE = 0, SO = 1;
;     SLOAD(SE, 0); asm volatile("s_waitcnt vmcnt(0)" ::: "memory"); SWRITE(0, SE); __syncthreads();
; __device__ __forceinline__ void p3_attention(Frame& F) {
;     ...
;     { float d1 = 0.f, d2 = 0.f;
;       for (int i = 0; i < 64; ++i) { d1 += F.in[I_LQ1][i] * F.in[I_LK1][i]; d2 += F.in[I_LQ2][i] * F.in[I_LK2][i]; }
;       lam = expf(d1) - expf(d2) + LAM_INIT; }
;     {
;         const bf16_t* Kh = KV + 2 * (KV_STRIDE / 2) + (size_t)b * RPB * 1024 + h * 128;
;         const bf16_t* Vh = KV + 3 * (KV_STRIDE / 2) + (size_t)b * RPB * 1024 + h * 128;
;         const bf16_t* Qb = (const bf16_t*)(F.ws + WS_QDF) + (size_t)(b * SEQ + qb * 256) * 1024 + h * 128;
;         LAS u32x4* o1l = (LAS u32x4*)(F.lds + attn::OFF_Q) + tid;
;         attn::attn_pass<1>(Qb, Kh, Vh, RPB / 64, 0, 0, 0, F.lds, o);
.LBB0_410:
	s_add_u32 s4, s52, s0
	s_addc_u32 s5, s53, s1
	global_load_dwordx4 v[2:5], v1, s[4:5]
	global_load_dwordx4 v[6:9], v1, s[4:5] offset:16
	s_add_u32 s4, s54, s0
	s_addc_u32 s5, s55, s1
	global_load_dwordx4 v[10:13], v1, s[4:5]
	global_load_dwordx4 v[14:17], v1, s[4:5] offset:16
	s_add_u32 s4, s56, s0
	s_addc_u32 s5, s57, s1
	global_load_dwordx4 v[18:21], v1, s[4:5]
	global_load_dwordx4 v[22:25], v1, s[4:5] offset:16
	s_add_u32 s4, s58, s0
	s_addc_u32 s5, s59, s1
	global_load_dwordx4 v[26:29], v1, s[4:5]
	global_load_dwordx4 v[30:33], v1, s[4:5] offset:16
	s_add_u32 s0, s0, 32
	s_addc_u32 s1, s1, 0
	s_cmpk_eq_i32 s0, 0x100
	s_waitcnt vmcnt(0)
	v_mov_b32_e32 v34, v2
	v_mov_b32_e32 v2, v4
	v_mov_b32_e32 v4, v6
	v_mov_b32_e32 v6, v8
	v_mov_b32_e32 v8, v10
	v_mov_b32_e32 v10, v12
	v_mov_b32_e32 v35, v18
	v_mov_b32_e32 v18, v3
	v_mov_b32_e32 v3, v20
	v_mov_b32_e32 v20, v5
	v_mov_b32_e32 v5, v22
	v_mov_b32_e32 v22, v7
	v_mov_b32_e32 v7, v24
	v_mov_b32_e32 v24, v9
	v_mov_b32_e32 v9, v26
	v_mov_b32_e32 v26, v11
	v_pk_fma_f32 v[8:9], v[34:35], v[8:9], v[194:195]
	v_mov_b32_e32 v11, v28
	v_pk_fma_f32 v[8:9], v[18:19], v[26:27], v[8:9]
	v_mov_b32_e32 v28, v13
	v_pk_fma_f32 v[2:3], v[2:3], v[10:11], v[8:9]
	v_mov_b32_e32 v12, v14
	v_mov_b32_e32 v13, v30
	v_pk_fma_f32 v[2:3], v[20:21], v[28:29], v[2:3]
	v_mov_b32_e32 v30, v15
	v_pk_fma_f32 v[2:3], v[4:5], v[12:13], v[2:3]
	v_mov_b32_e32 v14, v16
	v_mov_b32_e32 v15, v32
	v_pk_fma_f32 v[2:3], v[22:23], v[30:31], v[2:3]
	v_mov_b32_e32 v32, v17
	v_pk_fma_f32 v[2:3], v[6:7], v[14:15], v[2:3]
	s_nop 0
	v_pk_fma_f32 v[194:195], v[24:25], v[32:33], v[2:3]
	s_cbranch_scc0 .LBB0_410
	s_lshl_b32 s3, s2, 1
	s_and_b32 s0, s3, 14
	s_ashr_i32 s5, s2, 7
	s_add_i32 s0, s0, s5
	s_ashr_i32 s4, s0, 3
	s_and_b32 s54, s0, 7
	s_mul_hi_i32 s1, s4, 0x440000
	s_mul_i32 s0, s4, 0x440000
	s_bfe_u32 s55, s2, 0x40003
	s_lshl_b64 s[24:25], s[0:1], 1
	s_lshl_b32 s38, s54, 7
	s_lshl_b32 s20, s54, 8
	s_add_u32 s0, s82, s24
	s_addc_u32 s1, s83, s25
	s_add_u32 s0, s0, s20
	v_mov_b32_e32 v167, 0
	v_lshrrev_b32_e32 v174, 4, v0
	v_lshlrev_b32_e32 v62, 3, v0
	s_addc_u32 s1, s1, 0
	v_and_b32_e32 v156, 0x78, v62
	v_lshlrev_b32_e32 v50, 11, v174
	v_mov_b32_e32 v51, v167
	v_lshl_add_u64 v[2:3], s[0:1], 0, v[50:51]
	v_lshlrev_b32_e32 v4, 1, v156
	v_mov_b32_e32 v5, v167
	v_lshl_add_u64 v[54:55], v[2:3], 0, v[4:5]
	s_mov_b32 s21, 0x39500000
	v_lshrrev_b32_e32 v1, 3, v0
	v_add_co_u32_e32 v2, vcc, s21, v54
	v_and_b32_e32 v217, 56, v62
	s_nop 0
	v_addc_co_u32_e32 v3, vcc, 0, v55, vcc
	s_mov_b32 s21, 0x39510000
	v_lshlrev_b32_e32 v52, 11, v1
	v_mov_b32_e32 v53, v167
	s_lshl_b32 s6, s4, 12
	s_lshl_b32 s7, s55, 8
	v_add_co_u32_e32 v6, vcc, s21, v54
	v_lshl_add_u64 v[58:59], s[0:1], 0, v[52:53]
	v_lshlrev_b32_e32 v60, 1, v217
	v_mov_b32_e32 v61, v167
	s_or_b32 s42, s6, s7
	v_addc_co_u32_e32 v7, vcc, 0, v55, vcc
	v_lshl_add_u64 v[56:57], v[58:59], 0, v[60:61]
	s_mov_b32 s0, 0x38400000
	s_ashr_i32 s43, s42, 31
	v_add_co_u32_e32 v10, vcc, s0, v56
	s_lshl_b64 s[40:41], s[42:43], 10
	s_lshl_b64 s[6:7], s[42:43], 11
	v_addc_co_u32_e32 v11, vcc, 0, v57, vcc
	s_add_u32 s6, s82, s6
	global_load_dwordx4 v[2:5], v[2:3], off
	s_nop 0
	global_load_dwordx4 v[6:9], v[6:7], off
	v_and_b32_e32 v172, 31, v0
	global_load_dwordx4 v[10:13], v[10:11], off
	s_addc_u32 s7, s83, s7
	s_add_u32 s0, s6, s20
	v_lshlrev_b32_e32 v14, 9, v0
	v_lshlrev_b32_e32 v214, 10, v172
	s_mov_b32 s6, 0x38000
	v_and_or_b32 v14, v14, s6, v214
	s_addc_u32 s1, s7, 0
	v_lshrrev_b32_e32 v208, 5, v170
	v_lshlrev_b32_e32 v166, 1, v14
	v_lshl_add_u64 v[14:15], s[0:1], 0, v[166:167]
	v_lshlrev_b32_e32 v166, 4, v208
	v_lshl_add_u64 v[14:15], v[14:15], 0, v[166:167]
	s_mov_b32 s0, 0x3b600000
	v_add_co_u32_e32 v16, vcc, s0, v14
	s_mov_b64 s[0:1], 0x3b600000
	s_nop 0
	v_addc_co_u32_e32 v17, vcc, 0, v15, vcc
	global_load_dwordx4 v[110:113], v[16:17], off
	v_lshl_add_u64 v[178:179], v[14:15], 0, s[0:1]
	global_load_dwordx4 v[106:109], v[178:179], off offset:32
	global_load_dwordx4 v[102:105], v[178:179], off offset:64
	global_load_dwordx4 v[98:101], v[178:179], off offset:96
	v_mul_f32_e32 v14, 0x3fb8aa3b, v195
	s_mov_b32 s0, 0x3fb8aa3b
	v_rndne_f32_e32 v15, v14
	v_sub_f32_e32 v16, v14, v15
	v_fma_f32 v14, v195, s0, -v14
	v_fmamk_f32 v14, v195, 0x32a5705f, v14
	v_add_f32_e32 v14, v16, v14
	v_and_b32_e32 v16, 8, v1
	v_or_b32_e32 v176, 32, v174
	v_and_or_b32 v17, v174, 16, v16
	v_lshrrev_b32_e32 v154, 5, v0
	v_bfe_u32 v19, v0, 4, 2
	v_and_or_b32 v16, v176, 48, v16
	v_lshrrev_b32_e32 v17, 1, v17
	v_bfe_u32 v18, v62, 5, 2
	v_and_or_b32 v19, v154, 4, v19
	v_lshrrev_b32_e32 v16, 1, v16
	v_or_b32_e32 v17, v17, v18
	v_lshlrev_b32_e32 v19, 6, v19
	v_lshlrev_b32_e32 v51, 4, v0
	v_or_b32_e32 v16, v16, v18
	v_lshlrev_b32_e32 v53, 1, v0
	v_and_b32_e32 v20, 48, v51
	v_lshl_or_b32 v161, v17, 9, v19
	v_lshl_or_b32 v210, v16, 9, v19
	v_lshlrev_b32_e32 v220, 8, v1
	s_movk_i32 s0, 0x70
	v_and_b32_e32 v221, 0x70, v53
	v_lshlrev_b32_e32 v157, 8, v172
	v_or_b32_e32 v17, v161, v20
	v_or_b32_e32 v16, v210, v20
	v_bitop3_b32 v1, v60, v220, v221 bitop3:0xde
	v_add_u32_e32 v218, 0, v157
	v_bitop3_b32 v213, v166, v51, s0 bitop3:0x78
	v_add_u32_e32 v215, 0, v17
	v_add_u32_e32 v216, 0, v16
	v_add_u32_e32 v222, 0, v1
	v_add_u32_e32 v204, v218, v213
	s_waitcnt vmcnt(0)
	v_exp_f32_e32 v14, v14
	v_cvt_i32_f32_e32 v15, v15
	s_mov_b32 s0, 0xc2ce8ed0
	v_and_b32_e32 v219, 0x70, v51
	v_cmp_ngt_f32_e32 vcc, s0, v195
	v_ldexp_f32 v1, v14, v15
	s_mov_b32 s0, 0x42b17218
	v_bitop3_b32 v209, v166, v219, 32 bitop3:0x36
	v_cndmask_b32_e32 v1, 0, v1, vcc
	v_cmp_nlt_f32_e32 vcc, s0, v195
	v_add_u32_e32 v195, v218, v209
	v_bitop3_b32 v211, v166, v219, 64 bitop3:0x36
	v_add_u32_e32 v205, v218, v211
	s_add_i32 s0, 0, 0x10000
	s_mov_b32 s7, 0x42800000
	s_waitcnt vmcnt(6)
	ds_write_b128 v215, v[2:5]
	s_waitcnt vmcnt(5)
	ds_write_b128 v216, v[6:9]
	s_mul_i32 s56, s4, 0x880000
	s_waitcnt vmcnt(4)
	ds_write_b128 v222, v[10:13] offset:32768
	s_waitcnt lgkmcnt(0)
	s_barrier
; #define LAS __attribute__((address_space(3)))
; template <int MODE>
; __device__ __forceinline__ void partialSM(f32x16& p0, f32x16& p1, float& m_reg, float& mn, float& alpha) {
;     constexpr float SCALE = Cfg<MODE>::SCALE, C = SCALE * 1.4426950408889634f;
;     float pmax = p0[0];
; #pragma unroll
;     for (int r = 1; r < 16; ++r) pmax = fmaxf(pmax, p0[r]);
; #pragma unroll
;     for (int r = 0; r < 16; ++r) pmax = fmaxf(pmax, p1[r]);
;     { auto rr = __builtin_amdgcn_permlane32_swap(__float_as_uint(pmax), __float_as_uint(pmax), false, false);
;       pmax = fmaxf(__uint_as_float(rr[0]), __uint_as_float(rr[1])); }
;     if (__builtin_expect(__all(pmax - m_reg <= THR / SCALE), 1)) { mn = m_reg; alpha = 1.f; }
;     else { mn = fmaxf(m_reg, pmax); alpha = __builtin_amdgcn_exp2f((m_reg - mn) * C); m_reg = mn; }
;     const float mnC = -mn * C;
; #pragma unroll
;     for (int r = 0; r < 16; ++r) p0[r] = fmaf(p0[r], C, mnC);
; #pragma unroll
;     for (int r = 0; r < 16; ++r) p1[r] = fmaf(p1[r], C, mnC);
; #pragma unroll
;     for (int r = 0; r < 16; ++r) p0[r] = __builtin_amdgcn_exp2f(p0[r]);
; }
; template <int MODE>
; __device__ __forceinline__ void qkt(f32x16& p0, f32x16& p1, const LAS unsigned char* Ks, const bf16x8* qr, const LAS unsigned char* Qs, int r32, int hi, int cbase) {
;     p0 = f32x16{}; p1 = f32x16{};
; #pragma unroll
;     for (int d0 = 0; d0 < Cfg<MODE>::ND; ++d0) { const int cb = cbase + (d0 * 16 + hi * 8) * 2;
;         const bf16x8 b0 = *(const LAS bf16x8*)(Ks + KSWZ(r32, cb));
;         const bf16x8 b1 = *(const LAS bf16x8*)(Ks + KSWZ(32 + r32, cb));
;         bf16x8 q; if constexpr (MODE == 0) q = *(const LAS bf16x8*)(Qs + KSWZ(r32, cb)); else q = qr[d0];
;         p0 = __builtin_amdgcn_mfma_f32_32x32x16_bf16(b0, q, p0, 0, 0, 0);
;         p1 = __builtin_amdgcn_mfma_f32_32x32x16_bf16(b1, q, p1, 0, 0, 0); }
; template <int MODE>
; __device__ __forceinline__ void attn_pass(const bf16_t* __restrict__ Qb, const bf16_t* __restrict__ Kh, const bf16_t* __restrict__ Vh, const int NT, const int kr0, const int g4, const int map,
;                                           LAS unsigned char* lds, f32x16 (&o)[4]) {
;     ...
;     qkt<MODE>(pA0, pA1, K_lds, qr, Qs, r32, hi, cbase); MASK(pA0, pA1, 0); partialSM<MODE>(pA0, pA1, m_reg, mnA, alA);
;     SLOAD(SO, 1); if (2 < NT) SLOAD(SE, 2);
;     SWAIT(); SWRITE(1, SO); __syncthreads();
	ds_read_b128 v[2:5], v204 offset:32768
	ds_read_b128 v[6:9], v204 offset:40960
	s_waitcnt vmcnt(3) lgkmcnt(1)
	v_mfma_f32_32x32x16_bf16 v[18:33], v[2:5], v[110:113], 0
	v_mov_b32_e32 v2, 0x7f800000
	v_cndmask_b32_e32 v177, v2, v1, vcc
	ds_read_b128 v[2:5], v195 offset:32768
	v_and_b32_e32 v10, 0xc0, v51
	v_and_b32_e32 v11, 32, v53
	v_and_b32_e32 v1, 0x1c0, v0
	v_lshl_add_u32 v1, v1, 2, s0
	s_waitcnt lgkmcnt(1)
	v_mfma_f32_32x32x16_bf16 v[34:49], v[6:9], v[110:113], 0
	ds_read_b128 v[6:9], v195 offset:40960
	s_mov_b64 s[0:1], 0x39500000
	v_lshl_add_u64 v[182:183], v[54:55], 0, s[0:1]
	s_mov_b64 s[0:1], 0x39510000
	v_lshl_add_u64 v[184:185], v[54:55], 0, s[0:1]
	s_mov_b64 s[0:1], 0x38400000
	v_lshl_add_u64 v[168:169], v[56:57], 0, s[0:1]
	s_waitcnt vmcnt(2) lgkmcnt(1)
	v_mfma_f32_32x32x16_bf16 v[18:33], v[2:5], v[106:109], v[18:33]
	v_and_b32_e32 v2, 0x118, v62
	v_or3_b32 v51, v11, v10, v2
	ds_read_b128 v[2:5], v205 offset:32768
	s_movk_i32 s0, 0x60
	v_bitop3_b32 v212, v166, v219, s0 bitop3:0x36
	v_add_u32_e32 v206, v218, v212
	ds_read_b128 v[62:65], v206 offset:40960
	s_waitcnt lgkmcnt(2)
	v_mfma_f32_32x32x16_bf16 v[34:49], v[6:9], v[106:109], v[34:49]
	ds_read_b128 v[6:9], v205 offset:40960
	s_mov_b32 s0, 0x39520000
	s_mov_b32 s39, 0
	s_mov_b32 s64, s39
	s_mov_b32 s65, s39
	s_mov_b32 s66, s39
	s_mov_b32 s67, s39
	s_waitcnt vmcnt(1) lgkmcnt(2)
	v_mfma_f32_32x32x16_bf16 v[18:33], v[2:5], v[102:105], v[18:33]
	ds_read_b128 v[2:5], v206 offset:32768
	s_mov_b32 s68, s39
	s_mov_b32 s69, s39
	s_mov_b32 s70, s39
	s_mov_b32 s71, s39
	s_mov_b32 s72, s39
	s_mov_b32 s73, s39
	s_waitcnt lgkmcnt(1)
	v_mfma_f32_32x32x16_bf16 v[34:49], v[6:9], v[102:105], v[34:49]
	s_mov_b32 s74, s39
	s_mov_b32 s75, s39
	s_mov_b32 s76, s39
	s_mov_b32 s77, s39
	s_mov_b32 s78, s39
	s_mov_b32 s79, s39
	s_mov_b32 s44, 0x3e38aa3b
	s_waitcnt vmcnt(0) lgkmcnt(0)
	v_mfma_f32_32x32x16_bf16 v[18:33], v[2:5], v[98:101], v[18:33]
	v_mov_b64_e32 v[2:3], s[64:65]
	v_mov_b64_e32 v[16:17], s[78:79]
	v_add_u32_e32 v175, 0, v51
	v_mov_b64_e32 v[4:5], s[66:67]
	v_mov_b64_e32 v[6:7], s[68:69]
	v_mov_b64_e32 v[8:9], s[70:71]
	v_mov_b64_e32 v[10:11], s[72:73]
	v_mfma_f32_32x32x16_bf16 v[34:49], v[62:65], v[98:101], v[34:49]
	s_nop 3
	v_max_f32_e32 v53, v18, v19
	v_max3_f32 v53, v53, v20, v21
	v_max3_f32 v53, v53, v22, v23
	v_max3_f32 v53, v53, v24, v25
	v_max3_f32 v53, v53, v26, v27
	v_max3_f32 v53, v53, v28, v29
	v_max3_f32 v53, v53, v30, v31
	v_max3_f32 v53, v53, v32, v33
	v_max3_f32 v53, v53, v34, v35
	v_max3_f32 v53, v53, v36, v37
	v_max3_f32 v53, v53, v38, v39
	v_max3_f32 v53, v53, v40, v41
	v_max3_f32 v53, v53, v42, v43
	v_max3_f32 v53, v53, v44, v45
	v_max3_f32 v53, v53, v46, v47
	v_max3_f32 v53, v53, v48, v49
	v_mov_b32_e32 v62, v53
	s_nop 1
	v_permlane32_swap_b32_e32 v53, v62
	v_max_f32_e32 v53, v53, v62
	v_add_f32_e32 v62, 0x7149f2ca, v53
	v_max_f32_e32 v53, 0xf149f2ca, v53
	v_cmp_ge_f32_e32 vcc, s7, v62
	v_sub_f32_e32 v62, 0xf149f2ca, v53
	v_mul_f32_e32 v62, 0x3e38aa3b, v62
	s_cmp_eq_u64 vcc, exec
	v_exp_f32_e32 v72, v62
	v_add_co_u32_e32 v62, vcc, s0, v54
	s_mov_b32 s0, 0x39530000
	s_nop 0
	v_addc_co_u32_e32 v63, vcc, 0, v55, vcc
	v_add_co_u32_e32 v66, vcc, s0, v54
	s_mov_b64 s[0:1], 0x38420000
	s_nop 0
	v_addc_co_u32_e32 v67, vcc, 0, v55, vcc
	global_load_dwordx4 v[62:65], v[62:63], off
	s_nop 0
	global_load_dwordx4 v[68:71], v[66:67], off
	v_mov_b32_e32 v66, 0xf149f2ca
	s_cselect_b64 vcc, -1, 0
	v_cndmask_b32_e32 v140, v53, v66, vcc
	v_lshl_add_u64 v[180:181], v[58:59], 0, s[0:1]
	v_cndmask_b32_e64 v223, v72, 1.0, vcc
	v_mul_f32_e32 v72, 0xbe38aa3b, v140
	s_mov_b32 s0, 0x38440000
	v_fmamk_f32 v53, v18, 0x3e38aa3b, v72
	v_add_co_u32_e32 v18, vcc, s0, v56
	v_lshl_add_u64 v[58:59], v[180:181], 0, v[60:61]
	v_fmamk_f32 v73, v19, 0x3e38aa3b, v72
	v_addc_co_u32_e32 v19, vcc, 0, v57, vcc
	s_mov_b32 s0, 0x39550000
	global_load_dwordx4 v[58:61], v[58:59], off
	v_fmamk_f32 v74, v20, 0x3e38aa3b, v72
	global_load_dwordx4 v[114:117], v[18:19], off
	v_add_co_u32_e32 v18, vcc, s0, v54
	s_mov_b32 s0, 0x39540000
	s_nop 0
	v_addc_co_u32_e32 v19, vcc, 0, v55, vcc
	v_add_co_u32_e32 v20, vcc, s0, v54
	v_fmamk_f32 v75, v21, 0x3e38aa3b, v72
	s_nop 0
	v_addc_co_u32_e32 v21, vcc, 0, v55, vcc
	global_load_dwordx4 v[122:125], v[18:19], off
	global_load_dwordx4 v[118:121], v[20:21], off
	v_fmamk_f32 v18, v30, 0x3e38aa3b, v72
	s_add_i32 s3, s3, s5
	v_exp_f32_e32 v143, v18
	s_add_i32 s20, 0, 0x4000
	s_and_b32 s3, s3, 7
	v_and_b32_e32 v18, 7, v0
	v_fmamk_f32 v19, v31, 0x3e38aa3b, v72
	v_add_u32_e32 v173, s20, v51
	s_lshl_b32 s20, s3, 8
	s_mul_hi_i32 s3, s4, 0x880000
	v_lshlrev_b32_e32 v18, 4, v18
	v_exp_f32_e32 v146, v19
	s_mov_b64 s[0:1], 0x39520000
	v_or3_b32 v18, s56, v52, v18
	v_mov_b32_e32 v19, s3
	v_lshl_add_u64 v[190:191], v[54:55], 0, s[0:1]
	s_mov_b64 s[0:1], 0x39530000
	v_lshl_add_u64 v[162:163], s[82:83], 0, v[18:19]
	v_and_b32_e32 v18, 15, v0
	v_mov_b32_e32 v21, v72
	v_lshl_add_u64 v[192:193], v[54:55], 0, s[0:1]
	s_mov_b64 s[0:1], 0x39550000
	s_waitcnt vmcnt(3)
	v_lshlrev_b32_e32 v158, 4, v18
	v_fmamk_f32 v22, v22, 0x3e38aa3b, v72
	v_fmamk_f32 v23, v23, 0x3e38aa3b, v72
	v_fmamk_f32 v24, v24, 0x3e38aa3b, v72
	v_fmamk_f32 v25, v25, 0x3e38aa3b, v72
	v_fmamk_f32 v26, v26, 0x3e38aa3b, v72
	v_fmamk_f32 v27, v27, 0x3e38aa3b, v72
	v_fmamk_f32 v28, v28, 0x3e38aa3b, v72
	v_fmamk_f32 v29, v29, 0x3e38aa3b, v72
	v_fmamk_f32 v20, v32, 0x3e38aa3b, v72
	v_fmac_f32_e32 v21, 0x3e38aa3b, v33
	v_lshl_add_u64 v[186:187], v[54:55], 0, s[0:1]
	s_mov_b64 s[0:1], 0x39540000
	v_or3_b32 v18, s56, v50, v158
	v_mov_b64_e32 v[12:13], s[74:75]
	v_mov_b64_e32 v[14:15], s[76:77]
	v_pk_fma_f32 v[134:135], v[48:49], s[44:45], v[72:73] op_sel_hi:[1,0,0]
	v_pk_fma_f32 v[136:137], v[46:47], s[44:45], v[72:73] op_sel_hi:[1,0,0]
	v_pk_fma_f32 v[138:139], v[44:45], s[44:45], v[72:73] op_sel_hi:[1,0,0]
	v_pk_fma_f32 v[126:127], v[42:43], s[44:45], v[72:73] op_sel_hi:[1,0,0]
	v_pk_fma_f32 v[128:129], v[40:41], s[44:45], v[72:73] op_sel_hi:[1,0,0]
	v_pk_fma_f32 v[130:131], v[38:39], s[44:45], v[72:73] op_sel_hi:[1,0,0]
	v_pk_fma_f32 v[66:67], v[36:37], s[44:45], v[72:73] op_sel_hi:[1,0,0]
	v_pk_fma_f32 v[132:133], v[34:35], s[44:45], v[72:73] op_sel_hi:[1,0,0]
	v_exp_f32_e32 v201, v53
	v_exp_f32_e32 v151, v22
	v_exp_f32_e32 v200, v23
	v_exp_f32_e32 v150, v24
	v_exp_f32_e32 v152, v25
	v_exp_f32_e32 v147, v26
	v_exp_f32_e32 v149, v27
	v_exp_f32_e32 v145, v28
	v_exp_f32_e32 v148, v29
	v_exp_f32_e32 v142, v20
	v_exp_f32_e32 v144, v21
	v_lshl_add_u64 v[188:189], v[54:55], 0, s[0:1]
	s_waitcnt vmcnt(5)
	ds_write_b128 v215, v[62:65] offset:16384
	s_waitcnt vmcnt(4)
	ds_write_b128 v216, v[68:71] offset:16384
	s_waitcnt vmcnt(3)
	ds_write_b128 v222, v[58:61] offset:49152
	v_lshl_add_u64 v[164:165], s[82:83], 0, v[18:19]
	v_mov_b64_e32 v[64:65], v[16:17]
	v_mov_b64_e32 v[48:49], v[16:17]
	v_mov_b64_e32 v[32:33], v[16:17]
	s_mov_b32 s6, 1
	v_lshlrev_b32_e32 v160, 3, v208
	v_mov_b32_e32 v155, v167
	v_exp_f32_e32 v203, v73
	v_exp_f32_e32 v153, v74
	v_exp_f32_e32 v202, v75
	s_waitcnt lgkmcnt(0)
	s_barrier
; #define LAS __attribute__((address_space(3)))
; #define SBAR() __builtin_amdgcn_sched_barrier(0)
; __device__ __forceinline__ void finishSM(f32x16& p0, f32x16& p1, float alpha, float& l_reg, bf16x8& pa0, bf16x8& pa1, bf16x8& pa2, bf16x8& pa3) {
; #pragma unroll
;     for (int r = 0; r < 16; ++r) p1[r] = __builtin_amdgcn_exp2f(p1[r]);
;     float ps = 0;
; #pragma unroll
;     for (int r = 0; r < 16; ++r) ps += p0[r];
; #pragma unroll
;     for (int r = 0; r < 16; ++r) ps += p1[r];
;     { auto rr = __builtin_amdgcn_permlane32_swap(__float_as_uint(ps), __float_as_uint(ps), false, false);
;       ps = __uint_as_float(rr[0]) + __uint_as_float(rr[1]); }
;     l_reg = l_reg * alpha + ps;
;     ...
;     PK4(p0, 0, pa0); PK4(p0, 8, pa1); PK4(p1, 0, pa2); PK4(p1, 8, pa3);
;     ...
; }
; template <int MODE>
; __device__ __forceinline__ void qkt(f32x16& p0, f32x16& p1, const LAS unsigned char* Ks, const bf16x8* qr, const LAS unsigned char* Qs, int r32, int hi, int cbase) {
;     p0 = f32x16{}; p1 = f32x16{};
; #pragma unroll
;     for (int d0 = 0; d0 < Cfg<MODE>::ND; ++d0) { const int cb = cbase + (d0 * 16 + hi * 8) * 2;
;         const bf16x8 b0 = *(const LAS bf16x8*)(Ks + KSWZ(r32, cb));
;         const bf16x8 b1 = *(const LAS bf16x8*)(Ks + KSWZ(32 + r32, cb));
;         bf16x8 q; if constexpr (MODE == 0) q = *(const LAS bf16x8*)(Qs + KSWZ(r32, cb)); else q = qr[d0];
;         p0 = __builtin_amdgcn_mfma_f32_32x32x16_bf16(b0, q, p0, 0, 0, 0);
;         p1 = __builtin_amdgcn_mfma_f32_32x32x16_bf16(b1, q, p1, 0, 0, 0); }
; template <int MODE>
; __device__ __forceinline__ void attn_pass(const bf16_t* __restrict__ Qb, const bf16_t* __restrict__ Kh, const bf16_t* __restrict__ Vh, const int NT, const int kr0, const int g4, const int map,
;                                           LAS unsigned char* lds, f32x16 (&o)[4]) {
;     ...
;         SBAR(); qkt<MODE>(pB0, pB1, K_lds + SHM_K, qr, Qs, r32, hi, cbase); MASK(pB0, pB1, j);
;         finishSM(pA0, pA1, alA, l_reg, pa0, pa1, pa2, pa3); SBAR();
;         SLOAD(SO, j + 2 < NT ? j + 2 : NT - 1); SBAR();
;         pv_d0(o, vb0, pa0, pa1, pa2, pa3); partialSM<MODE>(pB0, pB1, m_reg, mnB, alB);
	v_cmp_gt_u32_e64 s[0:1], 32, v170
	v_lshl_add_u32 v171, v172, 2, v1
	v_add_u32_e32 v207, v1, v166
	s_mov_b32 s21, s39
	v_mov_b32_e32 v159, v167
	s_mov_b32 s43, 0x39560000
	s_mov_b32 s45, 0x39570000
	s_mov_b32 s57, 0x38460000
	s_mov_b64 s[46:47], 0x40000
	v_mov_b64_e32 v[196:197], v[164:165]
	v_mov_b64_e32 v[198:199], v[162:163]
	v_mov_b64_e32 v[62:63], v[14:15]
	v_mov_b64_e32 v[60:61], v[12:13]
	v_mov_b64_e32 v[58:59], v[10:11]
	v_mov_b64_e32 v[56:57], v[8:9]
	v_mov_b64_e32 v[54:55], v[6:7]
	v_mov_b64_e32 v[52:53], v[4:5]
	v_mov_b64_e32 v[50:51], v[2:3]
	v_mov_b64_e32 v[46:47], v[14:15]
	v_mov_b64_e32 v[44:45], v[12:13]
	v_mov_b64_e32 v[42:43], v[10:11]
	v_mov_b64_e32 v[40:41], v[8:9]
	v_mov_b64_e32 v[38:39], v[6:7]
	v_mov_b64_e32 v[36:37], v[4:5]
	v_mov_b64_e32 v[34:35], v[2:3]
	v_mov_b64_e32 v[30:31], v[14:15]
	v_mov_b64_e32 v[28:29], v[12:13]
	v_mov_b64_e32 v[26:27], v[10:11]
	v_mov_b64_e32 v[24:25], v[8:9]
	v_mov_b64_e32 v[22:23], v[6:7]
	v_mov_b64_e32 v[20:21], v[4:5]
	v_mov_b64_e32 v[18:19], v[2:3]
.LBB0_412:
	ds_read_b128 v[68:71], v204 offset:49152
	ds_read_b128 v[72:75], v204 offset:57344
	ds_read_b128 v[224:227], v195 offset:49152
	ds_read_b128 v[228:231], v195 offset:57344
	ds_read_b128 v[232:235], v205 offset:49152
	ds_read_b128 v[236:239], v205 offset:57344
	s_waitcnt lgkmcnt(5)
	v_mfma_f32_32x32x16_bf16 v[82:97], v[68:71], v[110:113], 0
	v_exp_f32_e32 v141, v66
	v_exp_f32_e32 v248, v67
	v_exp_f32_e32 v132, v132
	v_exp_f32_e32 v133, v133
	v_exp_f32_e32 v130, v130
	v_exp_f32_e32 v131, v131
	v_exp_f32_e32 v128, v128
	s_waitcnt lgkmcnt(3)
	v_mfma_f32_32x32x16_bf16 v[82:97], v[224:227], v[106:109], v[82:97]
	v_add_f32_e32 v224, 0, v201
	v_add_f32_e32 v224, v203, v224
	v_add_f32_e32 v224, v153, v224
	v_add_f32_e32 v224, v202, v224
	v_add_f32_e32 v224, v151, v224
	v_add_f32_e32 v224, v200, v224
	v_add_f32_e32 v224, v150, v224
	v_mfma_f32_32x32x16_bf16 v[66:81], v[72:75], v[110:113], 0
	v_add_f32_e32 v224, v152, v224
	v_add_f32_e32 v224, v147, v224
	v_add_f32_e32 v224, v149, v224
	v_add_f32_e32 v224, v145, v224
	v_add_f32_e32 v224, v148, v224
	v_add_f32_e32 v224, v143, v224
	v_add_f32_e32 v224, v146, v224
	s_waitcnt lgkmcnt(2)
	v_mfma_f32_32x32x16_bf16 v[66:81], v[228:231], v[106:109], v[66:81]
	v_add_f32_e32 v224, v142, v224
	v_add_f32_e32 v224, v144, v224
	v_add_f32_e32 v224, v132, v224
	v_add_f32_e32 v224, v133, v224
	v_add_f32_e32 v224, v141, v224
	v_exp_f32_e32 v129, v129
	v_add_f32_e32 v224, v248, v224
	s_waitcnt lgkmcnt(1)
	v_mfma_f32_32x32x16_bf16 v[82:97], v[232:235], v[102:105], v[82:97]
	v_exp_f32_e32 v126, v126
	v_add_f32_e32 v224, v130, v224
	ds_read_b128 v[240:243], v206 offset:49152
	ds_read_b128 v[244:247], v206 offset:57344
	v_exp_f32_e32 v127, v127
	v_add_f32_e32 v224, v131, v224
	v_exp_f32_e32 v138, v138
	v_add_f32_e32 v224, v128, v224
	s_waitcnt lgkmcnt(2)
	v_mfma_f32_32x32x16_bf16 v[66:81], v[236:239], v[102:105], v[66:81]
	v_exp_f32_e32 v139, v139
	v_add_f32_e32 v224, v129, v224
	v_exp_f32_e32 v136, v136
	v_add_f32_e32 v224, v126, v224
	v_exp_f32_e32 v137, v137
	v_add_f32_e32 v224, v127, v224
	v_exp_f32_e32 v134, v134
	s_waitcnt lgkmcnt(1)
	v_mfma_f32_32x32x16_bf16 v[82:97], v[240:243], v[98:101], v[82:97]
	v_add_f32_e32 v224, v138, v224
	v_exp_f32_e32 v135, v135
	v_add_f32_e32 v224, v139, v224
	v_add_f32_e32 v224, v136, v224
	v_add_f32_e32 v224, v137, v224
	v_add_f32_e32 v224, v134, v224
	v_add_f32_e32 v224, v135, v224
	s_waitcnt lgkmcnt(0)
	v_mfma_f32_32x32x16_bf16 v[66:81], v[244:247], v[98:101], v[66:81]
	v_mov_b32_e32 v225, v224
	v_cvt_pk_bf16_f32 v226, v201, v203
	v_cvt_pk_bf16_f32 v227, v153, v202
	v_cvt_pk_bf16_f32 v228, v151, v200
	s_nop 1
	v_permlane32_swap_b32_e32 v224, v225
	v_cvt_pk_bf16_f32 v229, v150, v152
	v_permlane32_swap_b32_e32 v226, v228
	v_cvt_pk_bf16_f32 v150, v147, v149
	v_cvt_pk_bf16_f32 v151, v145, v148
	v_cvt_pk_bf16_f32 v152, v143, v146
	v_cvt_pk_bf16_f32 v153, v142, v144
	v_cvt_pk_bf16_f32 v142, v132, v133
	v_cvt_pk_bf16_f32 v143, v141, v248
	v_cvt_pk_bf16_f32 v144, v130, v131
	v_cvt_pk_bf16_f32 v145, v128, v129
	v_cvt_pk_bf16_f32 v146, v126, v127
	v_cvt_pk_bf16_f32 v147, v138, v139
	v_cvt_pk_bf16_f32 v148, v136, v137
	v_cvt_pk_bf16_f32 v149, v134, v135
	v_permlane32_swap_b32_e32 v227, v229
	v_permlane32_swap_b32_e32 v150, v152
	v_permlane32_swap_b32_e32 v151, v153
	v_permlane32_swap_b32_e32 v142, v144
	v_permlane32_swap_b32_e32 v143, v145
	v_permlane32_swap_b32_e32 v146, v148
	v_permlane32_swap_b32_e32 v147, v149
	v_lshl_add_u64 v[200:201], v[196:197], 0, s[20:21]
	v_add_co_u32_e32 v126, vcc, s43, v200
	v_lshl_add_u64 v[202:203], v[198:199], 0, s[20:21]
	s_nop 0
	v_addc_co_u32_e32 v127, vcc, 0, v201, vcc
	v_add_co_u32_e32 v130, vcc, s45, v200
	s_nop 1
	v_addc_co_u32_e32 v131, vcc, 0, v201, vcc
	v_add_co_u32_e32 v134, vcc, s57, v202
	global_load_dwordx4 v[126:129], v[126:127], off
	s_nop 0
	global_load_dwordx4 v[130:133], v[130:131], off
	v_addc_co_u32_e32 v135, vcc, 0, v203, vcc
	global_load_dwordx4 v[134:137], v[134:135], off
	ds_read_b64_tr_b16 v[230:231], v175 offset:0
	ds_read_b64_tr_b16 v[232:233], v175 offset:0x800
	ds_read_b64_tr_b16 v[234:235], v175 offset:0x1000
	ds_read_b64_tr_b16 v[236:237], v175 offset:0x1800
	ds_read_b64_tr_b16 v[238:239], v175 offset:0x2000
	ds_read_b64_tr_b16 v[240:241], v175 offset:0x2800
	ds_read_b64_tr_b16 v[242:243], v175 offset:0x3000
	ds_read_b64_tr_b16 v[244:245], v175 offset:0x3800
	s_waitcnt lgkmcnt(0)
; #define SWAIT() do { if constexpr (MODE == 1) asm volatile("s_waitcnt vmcnt(3)" ::: "memory"); else asm volatile("s_waitcnt vmcnt(4)" ::: "memory"); } while (0)
; #define RESC(a) do { if (__any((a) < 1.f)) { if (hi == 0) al_l[r32] = (a); asm volatile("s_waitcnt lgkmcnt(0)" ::: "memory"); \
;     _Pragma("unroll") for (int d = 0; d < 4; ++d) _Pragma("unroll") for (int r = 0; r < 16; ++r) o[d][r] *= al_l[crow(r, hi)]; } } while (0)
; template <int MODE>
; __device__ __forceinline__ void partialSM(f32x16& p0, f32x16& p1, float& m_reg, float& mn, float& alpha) {
;     constexpr float SCALE = Cfg<MODE>::SCALE, C = SCALE * 1.4426950408889634f;
;     float pmax = p0[0];
; #pragma unroll
;     for (int r = 1; r < 16; ++r) pmax = fmaxf(pmax, p0[r]);
; #pragma unroll
;     for (int r = 0; r < 16; ++r) pmax = fmaxf(pmax, p1[r]);
;     { auto rr = __builtin_amdgcn_permlane32_swap(__float_as_uint(pmax), __float_as_uint(pmax), false, false);
;       pmax = fmaxf(__uint_as_float(rr[0]), __uint_as_float(rr[1])); }
;     if (__builtin_expect(__all(pmax - m_reg <= THR / SCALE), 1)) { mn = m_reg; alpha = 1.f; }
;     else { mn = fmaxf(m_reg, pmax); alpha = __builtin_amdgcn_exp2f((m_reg - mn) * C); m_reg = mn; }
; template <int MODE>
; __device__ __forceinline__ void attn_pass(const bf16_t* __restrict__ Qb, const bf16_t* __restrict__ Kh, const bf16_t* __restrict__ Vh, const int NT, const int kr0, const int g4, const int map,
;                                           LAS unsigned char* lds, f32x16 (&o)[4]) {
;     ...
;         pv_d0(o, vb0, pa0, pa1, pa2, pa3); partialSM<MODE>(pB0, pB1, m_reg, mnB, alB);
;         __syncthreads(); SWAIT(); SWRITE(0, SE);
;         RESC(alB); __syncthreads();
	s_nop 0
	v_mfma_f32_32x32x16_bf16 v[2:17], v[226:229], v[230:233], v[2:17]
	ds_read_b64_tr_b16 v[230:231], v175 offset:0x200
	ds_read_b64_tr_b16 v[232:233], v175 offset:0xa00
	v_mfma_f32_32x32x16_bf16 v[2:17], v[150:153], v[234:237], v[2:17]
	ds_read_b64_tr_b16 v[234:235], v175 offset:0x1200
	ds_read_b64_tr_b16 v[236:237], v175 offset:0x1a00
	v_mfma_f32_32x32x16_bf16 v[2:17], v[142:145], v[238:241], v[2:17]
	ds_read_b64_tr_b16 v[238:239], v175 offset:0x2200
	ds_read_b64_tr_b16 v[240:241], v175 offset:0x2a00
	ds_read_b64_tr_b16 v[246:247], v175 offset:0x3200
	ds_read_b64_tr_b16 v[248:249], v175 offset:0x3a00
	v_mfma_f32_32x32x16_bf16 v[2:17], v[146:149], v[242:245], v[2:17]
	s_waitcnt lgkmcnt(0)
	v_mfma_f32_32x32x16_bf16 v[50:65], v[226:229], v[230:233], v[50:65]
	ds_read_b64_tr_b16 v[230:231], v175 offset:0x400
	ds_read_b64_tr_b16 v[232:233], v175 offset:0xc00
	v_mfma_f32_32x32x16_bf16 v[50:65], v[150:153], v[234:237], v[50:65]
	ds_read_b64_tr_b16 v[234:235], v175 offset:0x1400
	ds_read_b64_tr_b16 v[236:237], v175 offset:0x1c00
	v_mfma_f32_32x32x16_bf16 v[50:65], v[142:145], v[238:241], v[50:65]
	ds_read_b64_tr_b16 v[238:239], v175 offset:0x2400
	ds_read_b64_tr_b16 v[240:241], v175 offset:0x2c00
	ds_read_b64_tr_b16 v[242:243], v175 offset:0x3400
	ds_read_b64_tr_b16 v[244:245], v175 offset:0x3c00
	v_mfma_f32_32x32x16_bf16 v[50:65], v[146:149], v[246:249], v[50:65]
	s_waitcnt lgkmcnt(0)
	v_mfma_f32_32x32x16_bf16 v[34:49], v[226:229], v[230:233], v[34:49]
	ds_read_b64_tr_b16 v[230:231], v175 offset:0x600
	ds_read_b64_tr_b16 v[232:233], v175 offset:0xe00
	v_mfma_f32_32x32x16_bf16 v[34:49], v[150:153], v[234:237], v[34:49]
	ds_read_b64_tr_b16 v[234:235], v175 offset:0x1600
	ds_read_b64_tr_b16 v[236:237], v175 offset:0x1e00
	v_mfma_f32_32x32x16_bf16 v[34:49], v[142:145], v[238:241], v[34:49]
	ds_read_b64_tr_b16 v[238:239], v175 offset:0x2600
	ds_read_b64_tr_b16 v[240:241], v175 offset:0x2e00
	ds_read_b64_tr_b16 v[246:247], v175 offset:0x3600
	ds_read_b64_tr_b16 v[248:249], v175 offset:0x3e00
	v_mfma_f32_32x32x16_bf16 v[34:49], v[146:149], v[242:245], v[34:49]
	s_waitcnt lgkmcnt(0)
	v_mfma_f32_32x32x16_bf16 v[18:33], v[226:229], v[230:233], v[18:33]
	v_max_f32_e32 v138, v82, v83
	v_max3_f32 v138, v138, v84, v85
	v_max3_f32 v138, v138, v86, v87
	v_max3_f32 v138, v138, v88, v89
	v_max3_f32 v138, v138, v90, v91
	v_max3_f32 v138, v138, v92, v93
	v_mfma_f32_32x32x16_bf16 v[18:33], v[150:153], v[234:237], v[18:33]
	v_max3_f32 v138, v138, v94, v95
	v_max3_f32 v138, v138, v96, v97
	v_max3_f32 v138, v138, v66, v67
	v_max3_f32 v138, v138, v68, v69
	v_max3_f32 v138, v138, v70, v71
	v_max3_f32 v138, v138, v72, v73
	v_max3_f32 v138, v138, v74, v75
	v_max3_f32 v138, v138, v76, v77
	v_mfma_f32_32x32x16_bf16 v[18:33], v[142:145], v[238:241], v[18:33]
	v_max3_f32 v138, v138, v78, v79
	v_max3_f32 v138, v138, v80, v81
	v_mov_b32_e32 v139, v138
	s_nop 1
	v_permlane32_swap_b32_e32 v138, v139
	v_max_f32_e32 v138, v138, v139
	v_sub_f32_e32 v139, v138, v140
	v_max_f32_e32 v138, v140, v138
	v_mfma_f32_32x32x16_bf16 v[18:33], v[146:149], v[246:249], v[18:33]
	v_sub_f32_e32 v141, v140, v138
	v_mul_f32_e32 v141, 0x3e38aa3b, v141
	v_exp_f32_e32 v141, v141
	v_cmp_ge_f32_e32 vcc, s7, v139
	s_cmp_eq_u64 vcc, exec
	s_cselect_b64 s[4:5], -1, 0
	s_barrier
	s_waitcnt vmcnt(3)
	v_cndmask_b32_e64 v226, v141, 1.0, s[4:5]
	v_cmp_gt_f32_e32 vcc, 1.0, v226
	s_waitcnt vmcnt(3)
	ds_write_b128 v215, v[118:121]
	ds_write_b128 v216, v[122:125]
	ds_write_b128 v222, v[114:117] offset:32768
	s_cbranch_vccz .LBB0_416
	s_and_saveexec_b64 s[48:49], s[0:1]
	ds_write_b32 v171, v226 offset:128
	s_or_b64 exec, exec, s[48:49]
	s_waitcnt lgkmcnt(0)
	ds_read_b128 v[142:145], v207 offset:224
	ds_read_b128 v[146:149], v207 offset:192
	ds_read_b128 v[150:153], v207 offset:160
	ds_read_b128 v[228:231], v207 offset:128
	s_waitcnt lgkmcnt(3)
	v_pk_mul_f32 v[16:17], v[16:17], v[144:145]
	s_waitcnt lgkmcnt(2)
	v_pk_mul_f32 v[12:13], v[12:13], v[148:149]
	s_waitcnt lgkmcnt(1)
	v_pk_mul_f32 v[8:9], v[8:9], v[152:153]
	s_waitcnt lgkmcnt(0)
	v_pk_mul_f32 v[4:5], v[4:5], v[230:231]
	v_pk_mul_f32 v[14:15], v[14:15], v[142:143]
	v_pk_mul_f32 v[10:11], v[10:11], v[146:147]
	v_pk_mul_f32 v[6:7], v[6:7], v[150:151]
	v_pk_mul_f32 v[2:3], v[2:3], v[228:229]
	v_pk_mul_f32 v[64:65], v[64:65], v[144:145]
	v_pk_mul_f32 v[60:61], v[60:61], v[148:149]
	v_pk_mul_f32 v[56:57], v[56:57], v[152:153]
	v_pk_mul_f32 v[52:53], v[52:53], v[230:231]
	v_pk_mul_f32 v[62:63], v[62:63], v[142:143]
	v_pk_mul_f32 v[58:59], v[58:59], v[146:147]
	v_pk_mul_f32 v[54:55], v[54:55], v[150:151]
	v_pk_mul_f32 v[50:51], v[50:51], v[228:229]
	v_pk_mul_f32 v[48:49], v[48:49], v[144:145]
	v_pk_mul_f32 v[44:45], v[44:45], v[148:149]
	v_pk_mul_f32 v[40:41], v[40:41], v[152:153]
	v_pk_mul_f32 v[36:37], v[36:37], v[230:231]
	v_pk_mul_f32 v[46:47], v[46:47], v[142:143]
	v_pk_mul_f32 v[42:43], v[42:43], v[146:147]
	v_pk_mul_f32 v[38:39], v[38:39], v[150:151]
	v_pk_mul_f32 v[34:35], v[34:35], v[228:229]
	v_pk_mul_f32 v[32:33], v[32:33], v[144:145]
	v_pk_mul_f32 v[28:29], v[28:29], v[148:149]
	v_pk_mul_f32 v[24:25], v[24:25], v[152:153]
	v_pk_mul_f32 v[20:21], v[20:21], v[230:231]
	v_pk_mul_f32 v[30:31], v[30:31], v[142:143]
	v_pk_mul_f32 v[26:27], v[26:27], v[146:147]
	v_pk_mul_f32 v[22:23], v[22:23], v[150:151]
	v_pk_mul_f32 v[18:19], v[18:19], v[228:229]

; #define SWAIT() do { if constexpr (MODE == 1) asm volatile("s_waitcnt vmcnt(3)" ::: "memory"); else asm volatile("s_waitcnt vmcnt(4)" ::: "memory"); } while (0)
; #define RESC(a) do { if (__any((a) < 1.f)) { if (hi == 0) al_l[r32] = (a); asm volatile("s_waitcnt lgkmcnt(0)" ::: "memory"); \
;     _Pragma("unroll") for (int d = 0; d < 4; ++d) _Pragma("unroll") for (int r = 0; r < 16; ++r) o[d][r] *= al_l[crow(r, hi)]; } } while (0)
; template <int MODE>
; __device__ __forceinline__ void partialSM(f32x16& p0, f32x16& p1, float& m_reg, float& mn, float& alpha) {
;     constexpr float SCALE = Cfg<MODE>::SCALE, C = SCALE * 1.4426950408889634f;
;     float pmax = p0[0];
; #pragma unroll
;     for (int r = 1; r < 16; ++r) pmax = fmaxf(pmax, p0[r]);
; #pragma unroll
;     for (int r = 0; r < 16; ++r) pmax = fmaxf(pmax, p1[r]);
;     { auto rr = __builtin_amdgcn_permlane32_swap(__float_as_uint(pmax), __float_as_uint(pmax), false, false);
;       pmax = fmaxf(__uint_as_float(rr[0]), __uint_as_float(rr[1])); }
;     if (__builtin_expect(__all(pmax - m_reg <= THR / SCALE), 1)) { mn = m_reg; alpha = 1.f; }
;     else { mn = fmaxf(m_reg, pmax); alpha = __builtin_amdgcn_exp2f((m_reg - mn) * C); m_reg = mn; }
; template <int MODE>
; __device__ __forceinline__ void attn_pass(const bf16_t* __restrict__ Qb, const bf16_t* __restrict__ Kh, const bf16_t* __restrict__ Vh, const int NT, const int kr0, const int g4, const int map,
;                                           LAS unsigned char* lds, f32x16 (&o)[4]) {
;     ...
;         pv_d0(o, vb0 + SHM_V, pa0, pa1, pa2, pa3); partialSM<MODE>(pA0, pA1, m_reg, mnA, alA);
;         __syncthreads(); SWAIT(); SWRITE(1, SO);
;         RESC(alA); __syncthreads();
.LBB0_418:
	ds_read_b64_tr_b16 v[200:201], v173 offset:0
	ds_read_b64_tr_b16 v[202:203], v173 offset:0x800
	ds_read_b64_tr_b16 v[230:231], v173 offset:0x1000
	ds_read_b64_tr_b16 v[232:233], v173 offset:0x1800
	ds_read_b64_tr_b16 v[234:235], v173 offset:0x2000
	ds_read_b64_tr_b16 v[236:237], v173 offset:0x2800
	ds_read_b64_tr_b16 v[238:239], v173 offset:0x3000
	ds_read_b64_tr_b16 v[240:241], v173 offset:0x3800
	s_waitcnt lgkmcnt(0)
	s_nop 0
	v_mfma_f32_32x32x16_bf16 v[2:17], v[138:141], v[200:203], v[2:17]
	ds_read_b64_tr_b16 v[200:201], v173 offset:0x200
	ds_read_b64_tr_b16 v[202:203], v173 offset:0xa00
	v_mfma_f32_32x32x16_bf16 v[2:17], v[142:145], v[230:233], v[2:17]
	ds_read_b64_tr_b16 v[230:231], v173 offset:0x1200
	ds_read_b64_tr_b16 v[232:233], v173 offset:0x1a00
	v_mfma_f32_32x32x16_bf16 v[2:17], v[150:153], v[234:237], v[2:17]
	ds_read_b64_tr_b16 v[234:235], v173 offset:0x2200
	ds_read_b64_tr_b16 v[236:237], v173 offset:0x2a00
	ds_read_b64_tr_b16 v[242:243], v173 offset:0x3200
	ds_read_b64_tr_b16 v[244:245], v173 offset:0x3a00
	v_mfma_f32_32x32x16_bf16 v[2:17], v[146:149], v[238:241], v[2:17]
	s_waitcnt lgkmcnt(0)
	v_mfma_f32_32x32x16_bf16 v[50:65], v[138:141], v[200:203], v[50:65]
	ds_read_b64_tr_b16 v[200:201], v173 offset:0x400
	ds_read_b64_tr_b16 v[202:203], v173 offset:0xc00
	v_mfma_f32_32x32x16_bf16 v[50:65], v[142:145], v[230:233], v[50:65]
	ds_read_b64_tr_b16 v[230:231], v173 offset:0x1400
	ds_read_b64_tr_b16 v[232:233], v173 offset:0x1c00
	v_mfma_f32_32x32x16_bf16 v[50:65], v[150:153], v[234:237], v[50:65]
	ds_read_b64_tr_b16 v[234:235], v173 offset:0x2400
	ds_read_b64_tr_b16 v[236:237], v173 offset:0x2c00
	ds_read_b64_tr_b16 v[238:239], v173 offset:0x3400
	ds_read_b64_tr_b16 v[240:241], v173 offset:0x3c00
	v_mfma_f32_32x32x16_bf16 v[50:65], v[146:149], v[242:245], v[50:65]
	s_waitcnt lgkmcnt(0)
	v_mfma_f32_32x32x16_bf16 v[34:49], v[138:141], v[200:203], v[34:49]
	ds_read_b64_tr_b16 v[200:201], v173 offset:0x600
	ds_read_b64_tr_b16 v[202:203], v173 offset:0xe00
	v_mfma_f32_32x32x16_bf16 v[34:49], v[142:145], v[230:233], v[34:49]
	ds_read_b64_tr_b16 v[230:231], v173 offset:0x1600
	ds_read_b64_tr_b16 v[232:233], v173 offset:0x1e00
	v_mfma_f32_32x32x16_bf16 v[34:49], v[150:153], v[234:237], v[34:49]
	ds_read_b64_tr_b16 v[234:235], v173 offset:0x2600
	ds_read_b64_tr_b16 v[236:237], v173 offset:0x2e00
	ds_read_b64_tr_b16 v[242:243], v173 offset:0x3600
	ds_read_b64_tr_b16 v[244:245], v173 offset:0x3e00
	v_mfma_f32_32x32x16_bf16 v[34:49], v[146:149], v[238:241], v[34:49]
	s_waitcnt lgkmcnt(0)
	v_mfma_f32_32x32x16_bf16 v[18:33], v[138:141], v[200:203], v[18:33]
	v_max_f32_e32 v238, v82, v83
	v_max3_f32 v238, v238, v84, v85
	v_max3_f32 v238, v238, v86, v87
	v_max3_f32 v138, v238, v88, v89
	v_max3_f32 v138, v138, v90, v91
	v_max3_f32 v138, v138, v92, v93
	v_mfma_f32_32x32x16_bf16 v[18:33], v[142:145], v[230:233], v[18:33]
	v_max3_f32 v138, v138, v94, v95
	v_max3_f32 v138, v138, v96, v97
	v_max3_f32 v138, v138, v66, v67
	v_max3_f32 v138, v138, v68, v69
	v_max3_f32 v138, v138, v70, v71
	v_max3_f32 v138, v138, v72, v73
	v_max3_f32 v138, v138, v74, v75
	v_max3_f32 v138, v138, v76, v77
	v_mfma_f32_32x32x16_bf16 v[18:33], v[150:153], v[234:237], v[18:33]
	v_max3_f32 v138, v138, v78, v79
	v_max3_f32 v138, v138, v80, v81
	v_mov_b32_e32 v139, v138
	s_nop 1
	v_permlane32_swap_b32_e32 v138, v139
	v_max_f32_e32 v138, v138, v139
	v_sub_f32_e32 v139, v138, v227
	v_max_f32_e32 v138, v227, v138
	v_mfma_f32_32x32x16_bf16 v[18:33], v[146:149], v[242:245], v[18:33]
	v_sub_f32_e32 v140, v227, v138
	v_mul_f32_e32 v140, 0x3e38aa3b, v140
	v_exp_f32_e32 v140, v140
	v_cmp_ge_f32_e32 vcc, s7, v139
	s_cmp_eq_u64 vcc, exec
	s_cselect_b64 s[4:5], -1, 0
	s_barrier
	s_waitcnt vmcnt(3)
	v_cndmask_b32_e64 v141, v140, 1.0, s[4:5]
	v_cmp_gt_f32_e32 vcc, 1.0, v141
	s_waitcnt vmcnt(3)
	ds_write_b128 v215, v[126:129] offset:16384
	s_waitcnt vmcnt(3)
	ds_write_b128 v216, v[130:133] offset:16384
	s_waitcnt vmcnt(3)
	ds_write_b128 v222, v[134:137] offset:49152
	s_cbranch_vccz .LBB0_422
	s_and_saveexec_b64 s[52:53], s[0:1]
	ds_write_b32 v171, v141 offset:128
	s_or_b64 exec, exec, s[52:53]
	s_waitcnt lgkmcnt(0)
	ds_read_b128 v[126:129], v207 offset:224
	ds_read_b128 v[130:133], v207 offset:192
	ds_read_b128 v[134:137], v207 offset:160
	ds_read_b128 v[142:145], v207 offset:128
	s_waitcnt lgkmcnt(3)
	v_pk_mul_f32 v[16:17], v[16:17], v[128:129]
	s_waitcnt lgkmcnt(2)
	v_pk_mul_f32 v[12:13], v[12:13], v[132:133]
	s_waitcnt lgkmcnt(1)
	v_pk_mul_f32 v[8:9], v[8:9], v[136:137]
	s_waitcnt lgkmcnt(0)
	v_pk_mul_f32 v[4:5], v[4:5], v[144:145]
	v_pk_mul_f32 v[14:15], v[14:15], v[126:127]
	v_pk_mul_f32 v[10:11], v[10:11], v[130:131]
	v_pk_mul_f32 v[6:7], v[6:7], v[134:135]
	v_pk_mul_f32 v[2:3], v[2:3], v[142:143]
	v_pk_mul_f32 v[64:65], v[64:65], v[128:129]
	v_pk_mul_f32 v[60:61], v[60:61], v[132:133]
	v_pk_mul_f32 v[56:57], v[56:57], v[136:137]
	v_pk_mul_f32 v[52:53], v[52:53], v[144:145]
	v_pk_mul_f32 v[62:63], v[62:63], v[126:127]
	v_pk_mul_f32 v[58:59], v[58:59], v[130:131]
	v_pk_mul_f32 v[54:55], v[54:55], v[134:135]
	v_pk_mul_f32 v[50:51], v[50:51], v[142:143]
	v_pk_mul_f32 v[48:49], v[48:49], v[128:129]
	v_pk_mul_f32 v[44:45], v[44:45], v[132:133]
	v_pk_mul_f32 v[40:41], v[40:41], v[136:137]
	v_pk_mul_f32 v[36:37], v[36:37], v[144:145]
	v_pk_mul_f32 v[46:47], v[46:47], v[126:127]
	v_pk_mul_f32 v[42:43], v[42:43], v[130:131]
	v_pk_mul_f32 v[38:39], v[38:39], v[134:135]
	v_pk_mul_f32 v[34:35], v[34:35], v[142:143]
	v_pk_mul_f32 v[32:33], v[32:33], v[128:129]
	v_pk_mul_f32 v[28:29], v[28:29], v[132:133]
	v_pk_mul_f32 v[24:25], v[24:25], v[136:137]
	v_pk_mul_f32 v[20:21], v[20:21], v[144:145]
	v_pk_mul_f32 v[30:31], v[30:31], v[126:127]
	v_pk_mul_f32 v[26:27], v[26:27], v[130:131]
	v_pk_mul_f32 v[22:23], v[22:23], v[134:135]
	v_pk_mul_f32 v[18:19], v[18:19], v[142:143]

; #define LAS __attribute__((address_space(3)))
; #define SBAR() __builtin_amdgcn_sched_barrier(0)
; #define MASK(P0, P1, jt) do { if (MODE == 0 && (jt) >= 4) { const int kr_ = kr0 + (jt) - 4; const bool rv_ = (kr_ >= r0w) && (kr_ < r0w + 8); int br_ = kr_ - qR + 7; br_ = br_ < 0 ? 0 : (br_ > 14 ? 14 : br_); \
;     na_mask(P0, P1, rv_, biasL + 64 + br_ * 32 + (4 * hi - qc + 15), 4 * hi - cs); } } while (0)
; __device__ __forceinline__ void finishSM(f32x16& p0, f32x16& p1, float alpha, float& l_reg, bf16x8& pa0, bf16x8& pa1, bf16x8& pa2, bf16x8& pa3) {
; #pragma unroll
;     for (int r = 0; r < 16; ++r) p1[r] = __builtin_amdgcn_exp2f(p1[r]);
;     float ps = 0;
; #pragma unroll
;     for (int r = 0; r < 16; ++r) ps += p0[r];
; #pragma unroll
;     for (int r = 0; r < 16; ++r) ps += p1[r];
;     { auto rr = __builtin_amdgcn_permlane32_swap(__float_as_uint(ps), __float_as_uint(ps), false, false);
;       ps = __uint_as_float(rr[0]) + __uint_as_float(rr[1]); }
;     l_reg = l_reg * alpha + ps;
;     ...
;     PK4(p0, 0, pa0); PK4(p0, 8, pa1); PK4(p1, 0, pa2); PK4(p1, 8, pa3);
;     ...
; }
; template <int MODE>
; __device__ __forceinline__ void qkt(f32x16& p0, f32x16& p1, const LAS unsigned char* Ks, const bf16x8* qr, const LAS unsigned char* Qs, int r32, int hi, int cbase) {
;     p0 = f32x16{}; p1 = f32x16{};
; #pragma unroll
;     for (int d0 = 0; d0 < Cfg<MODE>::ND; ++d0) { const int cb = cbase + (d0 * 16 + hi * 8) * 2;
;         const bf16x8 b0 = *(const LAS bf16x8*)(Ks + KSWZ(r32, cb));
;         const bf16x8 b1 = *(const LAS bf16x8*)(Ks + KSWZ(32 + r32, cb));
;         bf16x8 q; if constexpr (MODE == 0) q = *(const LAS bf16x8*)(Qs + KSWZ(r32, cb)); else q = qr[d0];
;         p0 = __builtin_amdgcn_mfma_f32_32x32x16_bf16(b0, q, p0, 0, 0, 0);
;         p1 = __builtin_amdgcn_mfma_f32_32x32x16_bf16(b1, q, p1, 0, 0, 0); }
; template <int MODE>
; __device__ __forceinline__ void attn_pass(const bf16_t* __restrict__ Qb, const bf16_t* __restrict__ Kh, const bf16_t* __restrict__ Vh, const int NT, const int kr0, const int g4, const int map,
;                                           LAS unsigned char* lds, f32x16 (&o)[4]) {
;     ...
;     SBAR(); qkt<MODE>(pB0, pB1, K_lds + SHM_K, qr, Qs, r32, hi, cbase); MASK(pB0, pB1, NT - 1);
;     finishSM(pA0, pA1, alA, l_reg, pa0, pa1, pa2, pa3); SBAR();
;     pv_d0(o, vb0, pa0, pa1, pa2, pa3); partialSM<MODE>(pB0, pB1, m_reg, mnB, alB);
.LBB0_424:
	v_mul_f32_e32 v68, 0x3fb8aa3b, v194
	s_mov_b32 s4, 0x3fb8aa3b
	v_rndne_f32_e32 v69, v68
	v_sub_f32_e32 v70, v68, v69
	v_fma_f32 v68, v194, s4, -v68
	v_fmamk_f32 v68, v194, 0x32a5705f, v68
	v_add_f32_e32 v68, v70, v68
	v_exp_f32_e32 v68, v68
	v_cvt_i32_f32_e32 v69, v69
	s_mov_b32 s4, 0xc2ce8ed0
	v_cmp_ngt_f32_e32 vcc, s4, v194
	s_mov_b32 s4, 0x42b17218
	v_ldexp_f32 v68, v68, v69
	v_cndmask_b32_e32 v114, 0, v68, vcc
	v_cmp_nlt_f32_e64 s[4:5], s4, v194
	v_mov_b32_e32 v115, 0x7f800000
	ds_read_b128 v[68:71], v204 offset:49152
	ds_read_b128 v[72:75], v204 offset:57344
	ds_read_b128 v[116:119], v195 offset:49152
	ds_read_b128 v[120:123], v195 offset:57344
	ds_read_b128 v[196:199], v205 offset:49152
	ds_read_b128 v[222:225], v205 offset:57344
	s_waitcnt lgkmcnt(5)
	v_mfma_f32_32x32x16_bf16 v[82:97], v[68:71], v[110:113], 0
	v_exp_f32_e32 v124, v132
	v_exp_f32_e32 v125, v133
	v_exp_f32_e32 v132, v66
	v_exp_f32_e32 v133, v67
	v_exp_f32_e32 v130, v130
	ds_read_b128 v[226:229], v206 offset:49152
	ds_read_b128 v[230:233], v206 offset:57344
	s_waitcnt lgkmcnt(6)
	v_mfma_f32_32x32x16_bf16 v[66:81], v[72:75], v[110:113], 0
	v_exp_f32_e32 v110, v131
	v_exp_f32_e32 v111, v128
	v_exp_f32_e32 v112, v129
	v_exp_f32_e32 v113, v126
	v_exp_f32_e32 v126, v127
	v_exp_f32_e32 v127, v138
	v_exp_f32_e32 v128, v139
	s_waitcnt lgkmcnt(5)
	v_mfma_f32_32x32x16_bf16 v[82:97], v[116:119], v[106:109], v[82:97]
	v_add_f32_e32 v116, 0, v201
	v_add_f32_e32 v116, v203, v116
	v_add_f32_e32 v116, v153, v116
	v_exp_f32_e32 v118, v136
	v_exp_f32_e32 v119, v137
	v_exp_f32_e32 v129, v134
	v_exp_f32_e32 v131, v135
	s_waitcnt lgkmcnt(4)
	v_mfma_f32_32x32x16_bf16 v[66:81], v[120:123], v[106:109], v[66:81]
	v_add_f32_e32 v106, v202, v116
	v_add_f32_e32 v106, v151, v106
	v_add_f32_e32 v106, v200, v106
	v_add_f32_e32 v106, v150, v106
	v_add_f32_e32 v106, v152, v106
	v_add_f32_e32 v106, v147, v106
	v_add_f32_e32 v106, v149, v106
	v_add_f32_e32 v106, v145, v106
	v_add_f32_e32 v106, v148, v106
	v_add_f32_e32 v106, v143, v106
	v_add_f32_e32 v106, v146, v106
	v_add_f32_e32 v106, v142, v106
	v_add_f32_e32 v106, v144, v106
	v_add_f32_e32 v106, v124, v106
	s_waitcnt lgkmcnt(3)
	v_mfma_f32_32x32x16_bf16 v[82:97], v[196:199], v[102:105], v[82:97]
	s_waitcnt lgkmcnt(2)
	v_mfma_f32_32x32x16_bf16 v[66:81], v[222:225], v[102:105], v[66:81]
	v_add_f32_e32 v102, v125, v106
	v_add_f32_e32 v102, v132, v102
	v_add_f32_e32 v102, v133, v102
	v_add_f32_e32 v102, v130, v102
	v_add_f32_e32 v102, v110, v102
	v_add_f32_e32 v102, v111, v102
	v_add_f32_e32 v102, v112, v102
	v_add_f32_e32 v102, v113, v102
	v_add_f32_e32 v102, v126, v102
	s_waitcnt lgkmcnt(1)
	v_mfma_f32_32x32x16_bf16 v[82:97], v[226:229], v[98:101], v[82:97]
	v_add_f32_e32 v102, v127, v102
	v_add_f32_e32 v102, v128, v102
	v_add_f32_e32 v102, v118, v102
	v_add_f32_e32 v102, v119, v102
	v_add_f32_e32 v102, v129, v102
	s_waitcnt lgkmcnt(0)
	v_mfma_f32_32x32x16_bf16 v[66:81], v[230:233], v[98:101], v[66:81]
	v_add_f32_e32 v98, v131, v102
	v_mov_b32_e32 v99, v98
	v_cvt_pk_bf16_f32 v100, v201, v203
	v_cvt_pk_bf16_f32 v101, v153, v202
	v_cvt_pk_bf16_f32 v102, v151, v200
	v_cvt_pk_bf16_f32 v103, v150, v152
	s_nop 1
	v_permlane32_swap_b32_e32 v98, v99
	v_permlane32_swap_b32_e32 v100, v102
	v_permlane32_swap_b32_e32 v101, v103
	v_cvt_pk_bf16_f32 v104, v147, v149
	v_cvt_pk_bf16_f32 v105, v145, v148
	v_cvt_pk_bf16_f32 v106, v143, v146
	v_cvt_pk_bf16_f32 v107, v142, v144
	v_cvt_pk_bf16_f32 v108, v124, v125
	v_cvt_pk_bf16_f32 v109, v132, v133
	v_cvt_pk_bf16_f32 v110, v130, v110
	v_cvt_pk_bf16_f32 v111, v111, v112
	v_cvt_pk_bf16_f32 v116, v113, v126
	v_cvt_pk_bf16_f32 v117, v127, v128
	v_cvt_pk_bf16_f32 v118, v118, v119
	v_cvt_pk_bf16_f32 v119, v129, v131
	s_nop 0
	v_permlane32_swap_b32_e32 v104, v106
	v_permlane32_swap_b32_e32 v105, v107
	v_permlane32_swap_b32_e32 v108, v110
	v_permlane32_swap_b32_e32 v109, v111
	v_permlane32_swap_b32_e32 v116, v118
	v_permlane32_swap_b32_e32 v117, v119
	ds_read_b64_tr_b16 v[120:121], v175 offset:0
	ds_read_b64_tr_b16 v[122:123], v175 offset:0x800
	ds_read_b64_tr_b16 v[124:125], v175 offset:0x1000
	ds_read_b64_tr_b16 v[126:127], v175 offset:0x1800
	ds_read_b64_tr_b16 v[128:129], v175 offset:0x2000
	ds_read_b64_tr_b16 v[130:131], v175 offset:0x2800
	ds_read_b64_tr_b16 v[132:133], v175 offset:0x3000
	ds_read_b64_tr_b16 v[134:135], v175 offset:0x3800
	s_waitcnt lgkmcnt(0)
	s_nop 0
	v_mfma_f32_32x32x16_bf16 v[2:17], v[100:103], v[120:123], v[2:17]
	ds_read_b64_tr_b16 v[120:121], v175 offset:0x200
	ds_read_b64_tr_b16 v[122:123], v175 offset:0xa00
	v_mfma_f32_32x32x16_bf16 v[2:17], v[104:107], v[124:127], v[2:17]
	ds_read_b64_tr_b16 v[124:125], v175 offset:0x1200
	ds_read_b64_tr_b16 v[126:127], v175 offset:0x1a00
	v_mfma_f32_32x32x16_bf16 v[2:17], v[108:111], v[128:131], v[2:17]
	ds_read_b64_tr_b16 v[128:129], v175 offset:0x2200
	ds_read_b64_tr_b16 v[130:131], v175 offset:0x2a00
	ds_read_b64_tr_b16 v[136:137], v175 offset:0x3200
	ds_read_b64_tr_b16 v[138:139], v175 offset:0x3a00
	v_mfma_f32_32x32x16_bf16 v[2:17], v[116:119], v[132:135], v[2:17]
	s_waitcnt lgkmcnt(0)
	v_mfma_f32_32x32x16_bf16 v[50:65], v[100:103], v[120:123], v[50:65]
	ds_read_b64_tr_b16 v[120:121], v175 offset:0x400
	ds_read_b64_tr_b16 v[122:123], v175 offset:0xc00
	v_mfma_f32_32x32x16_bf16 v[50:65], v[104:107], v[124:127], v[50:65]
	ds_read_b64_tr_b16 v[124:125], v175 offset:0x1400
	ds_read_b64_tr_b16 v[126:127], v175 offset:0x1c00
	v_mfma_f32_32x32x16_bf16 v[50:65], v[108:111], v[128:131], v[50:65]
	ds_read_b64_tr_b16 v[128:129], v175 offset:0x2400
	ds_read_b64_tr_b16 v[130:131], v175 offset:0x2c00
	ds_read_b64_tr_b16 v[132:133], v175 offset:0x3400
	ds_read_b64_tr_b16 v[134:135], v175 offset:0x3c00
	v_mfma_f32_32x32x16_bf16 v[50:65], v[116:119], v[136:139], v[50:65]
	s_waitcnt lgkmcnt(0)
; #define RESC(a) do { if (__any((a) < 1.f)) { if (hi == 0) al_l[r32] = (a); asm volatile("s_waitcnt lgkmcnt(0)" ::: "memory"); \
;     _Pragma("unroll") for (int d = 0; d < 4; ++d) _Pragma("unroll") for (int r = 0; r < 16; ++r) o[d][r] *= al_l[crow(r, hi)]; } } while (0)
; template <int MODE>
; __device__ __forceinline__ void partialSM(f32x16& p0, f32x16& p1, float& m_reg, float& mn, float& alpha) {
;     constexpr float SCALE = Cfg<MODE>::SCALE, C = SCALE * 1.4426950408889634f;
;     float pmax = p0[0];
; #pragma unroll
;     for (int r = 1; r < 16; ++r) pmax = fmaxf(pmax, p0[r]);
; #pragma unroll
;     for (int r = 0; r < 16; ++r) pmax = fmaxf(pmax, p1[r]);
;     { auto rr = __builtin_amdgcn_permlane32_swap(__float_as_uint(pmax), __float_as_uint(pmax), false, false);
;       pmax = fmaxf(__uint_as_float(rr[0]), __uint_as_float(rr[1])); }
;     if (__builtin_expect(__all(pmax - m_reg <= THR / SCALE), 1)) { mn = m_reg; alpha = 1.f; }
;     else { mn = fmaxf(m_reg, pmax); alpha = __builtin_amdgcn_exp2f((m_reg - mn) * C); m_reg = mn; }
;     const float mnC = -mn * C;
; #pragma unroll
;     for (int r = 0; r < 16; ++r) p0[r] = fmaf(p0[r], C, mnC);
; #pragma unroll
;     for (int r = 0; r < 16; ++r) p1[r] = fmaf(p1[r], C, mnC);
; #pragma unroll
;     for (int r = 0; r < 16; ++r) p0[r] = __builtin_amdgcn_exp2f(p0[r]);
; }
; template <int MODE>
; __device__ __forceinline__ void attn_pass(const bf16_t* __restrict__ Qb, const bf16_t* __restrict__ Kh, const bf16_t* __restrict__ Vh, const int NT, const int kr0, const int g4, const int map,
;                                           LAS unsigned char* lds, f32x16 (&o)[4]) {
;     ...
;     pv_d0(o, vb0, pa0, pa1, pa2, pa3); partialSM<MODE>(pB0, pB1, m_reg, mnB, alB);
;     __syncthreads(); RESC(alB);
	v_mfma_f32_32x32x16_bf16 v[34:49], v[100:103], v[120:123], v[34:49]
	ds_read_b64_tr_b16 v[120:121], v175 offset:0x600
	ds_read_b64_tr_b16 v[122:123], v175 offset:0xe00
	v_mfma_f32_32x32x16_bf16 v[34:49], v[104:107], v[124:127], v[34:49]
	ds_read_b64_tr_b16 v[124:125], v175 offset:0x1600
	ds_read_b64_tr_b16 v[126:127], v175 offset:0x1e00
	v_mfma_f32_32x32x16_bf16 v[34:49], v[108:111], v[128:131], v[34:49]
	ds_read_b64_tr_b16 v[128:129], v175 offset:0x2600
	ds_read_b64_tr_b16 v[130:131], v175 offset:0x2e00
	ds_read_b64_tr_b16 v[136:137], v175 offset:0x3600
	ds_read_b64_tr_b16 v[138:139], v175 offset:0x3e00
	v_mfma_f32_32x32x16_bf16 v[34:49], v[116:119], v[132:135], v[34:49]
	s_waitcnt lgkmcnt(0)
	v_mfma_f32_32x32x16_bf16 v[18:33], v[100:103], v[120:123], v[18:33]
	v_max_f32_e32 v112, v82, v83
	v_max3_f32 v112, v112, v84, v85
	v_max3_f32 v112, v112, v86, v87
	v_max3_f32 v100, v112, v88, v89
	v_max3_f32 v100, v100, v90, v91
	v_max3_f32 v100, v100, v92, v93
	v_mfma_f32_32x32x16_bf16 v[18:33], v[104:107], v[124:127], v[18:33]
	v_max3_f32 v100, v100, v94, v95
	v_max3_f32 v100, v100, v96, v97
	v_max3_f32 v100, v100, v66, v67
	v_max3_f32 v100, v100, v68, v69
	v_max3_f32 v100, v100, v70, v71
	v_max3_f32 v100, v100, v72, v73
	v_max3_f32 v100, v100, v74, v75
	v_max3_f32 v100, v100, v76, v77
	v_mfma_f32_32x32x16_bf16 v[18:33], v[108:111], v[128:131], v[18:33]
	v_max3_f32 v100, v100, v78, v79
	v_max3_f32 v100, v100, v80, v81
	v_mov_b32_e32 v101, v100
	s_nop 1
	v_permlane32_swap_b32_e32 v100, v101
	v_max_f32_e32 v100, v100, v101
	v_max_f32_e32 v102, v140, v100
	v_sub_f32_e32 v101, v100, v140
	v_mfma_f32_32x32x16_bf16 v[18:33], v[116:119], v[136:139], v[18:33]
	v_sub_f32_e32 v100, v140, v102
	s_mov_b32 s6, 0x42800000
	v_mul_f32_e32 v100, 0x3e38aa3b, v100
	v_exp_f32_e32 v100, v100
	v_cmp_ge_f32_e32 vcc, s6, v101
	s_cmp_eq_u64 vcc, exec
	s_cselect_b64 vcc, -1, 0
	v_cndmask_b32_e32 v101, v102, v140, vcc
	v_cndmask_b32_e64 v100, v100, 1.0, vcc
	v_mul_f32_e32 v101, 0xbe38aa3b, v101
	v_fmamk_f32 v82, v82, 0x3e38aa3b, v101
	v_fmamk_f32 v83, v83, 0x3e38aa3b, v101
	v_fmamk_f32 v84, v84, 0x3e38aa3b, v101
	v_fmamk_f32 v85, v85, 0x3e38aa3b, v101
	v_fmamk_f32 v86, v86, 0x3e38aa3b, v101
	v_fmamk_f32 v87, v87, 0x3e38aa3b, v101
	v_fmamk_f32 v88, v88, 0x3e38aa3b, v101
	v_fmamk_f32 v89, v89, 0x3e38aa3b, v101
	v_fmamk_f32 v90, v90, 0x3e38aa3b, v101
	v_fmamk_f32 v91, v91, 0x3e38aa3b, v101
	v_fmamk_f32 v92, v92, 0x3e38aa3b, v101
	v_fmamk_f32 v93, v93, 0x3e38aa3b, v101
	v_fmamk_f32 v94, v94, 0x3e38aa3b, v101
	v_fmamk_f32 v95, v95, 0x3e38aa3b, v101
	v_fmamk_f32 v96, v96, 0x3e38aa3b, v101
	v_fmamk_f32 v97, v97, 0x3e38aa3b, v101
	v_cmp_gt_f32_e32 vcc, 1.0, v100
	s_barrier
	s_cbranch_vccz .LBB0_428
	s_and_saveexec_b64 s[44:45], s[0:1]
	ds_write_b32 v171, v100 offset:128
	s_or_b64 exec, exec, s[44:45]
	s_waitcnt lgkmcnt(0)
	ds_read_b128 v[102:105], v207 offset:224
	ds_read_b128 v[106:109], v207 offset:192
	ds_read_b128 v[110:113], v207 offset:160
	ds_read_b128 v[116:119], v207 offset:128
	s_waitcnt lgkmcnt(3)
	v_pk_mul_f32 v[16:17], v[16:17], v[104:105]
	s_waitcnt lgkmcnt(2)
	v_pk_mul_f32 v[12:13], v[12:13], v[108:109]
	s_waitcnt lgkmcnt(1)
	v_pk_mul_f32 v[8:9], v[8:9], v[112:113]
	s_waitcnt lgkmcnt(0)
	v_pk_mul_f32 v[4:5], v[4:5], v[118:119]
	v_pk_mul_f32 v[14:15], v[14:15], v[102:103]
	v_pk_mul_f32 v[10:11], v[10:11], v[106:107]
	v_pk_mul_f32 v[6:7], v[6:7], v[110:111]
	v_pk_mul_f32 v[2:3], v[2:3], v[116:117]
	v_pk_mul_f32 v[64:65], v[64:65], v[104:105]
	v_pk_mul_f32 v[60:61], v[60:61], v[108:109]
	v_pk_mul_f32 v[56:57], v[56:57], v[112:113]
	v_pk_mul_f32 v[52:53], v[52:53], v[118:119]
	v_pk_mul_f32 v[62:63], v[62:63], v[102:103]
	v_pk_mul_f32 v[58:59], v[58:59], v[106:107]
	v_pk_mul_f32 v[54:55], v[54:55], v[110:111]
	v_pk_mul_f32 v[50:51], v[50:51], v[116:117]
	v_pk_mul_f32 v[48:49], v[48:49], v[104:105]
	v_pk_mul_f32 v[44:45], v[44:45], v[108:109]
	v_pk_mul_f32 v[40:41], v[40:41], v[112:113]
	v_pk_mul_f32 v[36:37], v[36:37], v[118:119]
	v_pk_mul_f32 v[46:47], v[46:47], v[102:103]
	v_pk_mul_f32 v[42:43], v[42:43], v[106:107]
	v_pk_mul_f32 v[38:39], v[38:39], v[110:111]
	v_pk_mul_f32 v[34:35], v[34:35], v[116:117]
	v_pk_mul_f32 v[32:33], v[32:33], v[104:105]
	v_pk_mul_f32 v[28:29], v[28:29], v[108:109]
	v_pk_mul_f32 v[24:25], v[24:25], v[112:113]
	v_pk_mul_f32 v[20:21], v[20:21], v[118:119]
	v_pk_mul_f32 v[30:31], v[30:31], v[102:103]
	v_pk_mul_f32 v[26:27], v[26:27], v[106:107]
	v_pk_mul_f32 v[22:23], v[22:23], v[110:111]
	v_pk_mul_f32 v[18:19], v[18:19], v[116:117]
; #define SBAR() __builtin_amdgcn_sched_barrier(0)
; __device__ __forceinline__ void finishSM(f32x16& p0, f32x16& p1, float alpha, float& l_reg, bf16x8& pa0, bf16x8& pa1, bf16x8& pa2, bf16x8& pa3) {
; #pragma unroll
;     for (int r = 0; r < 16; ++r) p1[r] = __builtin_amdgcn_exp2f(p1[r]);
;     float ps = 0;
; #pragma unroll
;     for (int r = 0; r < 16; ++r) ps += p0[r];
; #pragma unroll
;     for (int r = 0; r < 16; ++r) ps += p1[r];
;     { auto rr = __builtin_amdgcn_permlane32_swap(__float_as_uint(ps), __float_as_uint(ps), false, false);
;       ps = __uint_as_float(rr[0]) + __uint_as_float(rr[1]); }
;     l_reg = l_reg * alpha + ps;
;     ...
;     PK4(p0, 0, pa0); PK4(p0, 8, pa1); PK4(p1, 0, pa2); PK4(p1, 8, pa3);
; template <int MODE>
; __device__ __forceinline__ void attn_pass(const bf16_t* __restrict__ Qb, const bf16_t* __restrict__ Kh, const bf16_t* __restrict__ Vh, const int NT, const int kr0, const int g4, const int map,
;                                           LAS unsigned char* lds, f32x16 (&o)[4]) {
;     ...
;     finishSM(pB0, pB1, alB, l_reg, pa0, pa1, pa2, pa3); SBAR();
;     pv_d0(o, vb0 + SHM_V, pa0, pa1, pa2, pa3);
.LBB0_428:
	v_exp_f32_e32 v102, v82
	v_exp_f32_e32 v103, v83
	v_exp_f32_e32 v82, v84
	v_fmamk_f32 v66, v66, 0x3e38aa3b, v101
	v_exp_f32_e32 v84, v85
	v_fmamk_f32 v113, v77, 0x3e38aa3b, v101
	v_exp_f32_e32 v77, v86
	v_exp_f32_e32 v85, v66
	v_add_f32_e32 v66, 0, v102
	v_exp_f32_e32 v83, v87
	v_add_f32_e32 v66, v103, v66
	v_fmamk_f32 v112, v76, 0x3e38aa3b, v101
	v_exp_f32_e32 v76, v88
	v_add_f32_e32 v66, v82, v66
	v_cndmask_b32_e64 v199, v115, v114, s[4:5]
	v_fmamk_f32 v114, v78, 0x3e38aa3b, v101
	v_exp_f32_e32 v78, v89
	v_add_f32_e32 v66, v84, v66
	v_fmamk_f32 v109, v73, 0x3e38aa3b, v101
	v_exp_f32_e32 v73, v90
	v_add_f32_e32 v66, v77, v66
	v_fmamk_f32 v111, v75, 0x3e38aa3b, v101
	v_exp_f32_e32 v75, v91
	v_add_f32_e32 v66, v83, v66
	v_fmamk_f32 v107, v71, 0x3e38aa3b, v101
	v_exp_f32_e32 v71, v92
	v_add_f32_e32 v66, v76, v66
	v_fmamk_f32 v110, v74, 0x3e38aa3b, v101
	v_exp_f32_e32 v74, v93
	v_add_f32_e32 v66, v78, v66
	v_fmamk_f32 v105, v69, 0x3e38aa3b, v101
	v_exp_f32_e32 v69, v94
	v_add_f32_e32 v66, v73, v66
	v_fmamk_f32 v108, v72, 0x3e38aa3b, v101
	v_exp_f32_e32 v72, v95
	v_add_f32_e32 v66, v75, v66
	v_fmamk_f32 v104, v68, 0x3e38aa3b, v101
	v_exp_f32_e32 v68, v96
	v_add_f32_e32 v66, v71, v66
	v_fmamk_f32 v106, v70, 0x3e38aa3b, v101
	v_exp_f32_e32 v70, v97
	v_add_f32_e32 v66, v74, v66
	v_fmamk_f32 v67, v67, 0x3e38aa3b, v101
	v_add_f32_e32 v66, v69, v66
	v_exp_f32_e32 v86, v67
	v_add_f32_e32 v66, v72, v66
	v_exp_f32_e32 v87, v104
	v_add_f32_e32 v66, v68, v66
	v_exp_f32_e32 v88, v105
	v_add_f32_e32 v66, v70, v66
	v_exp_f32_e32 v89, v106
	v_add_f32_e32 v66, v85, v66
	v_exp_f32_e32 v90, v107
	v_add_f32_e32 v66, v86, v66
	v_exp_f32_e32 v91, v108
	v_add_f32_e32 v66, v87, v66
	v_exp_f32_e32 v92, v109
	v_add_f32_e32 v66, v88, v66
	v_exp_f32_e32 v93, v110
	v_add_f32_e32 v66, v89, v66
	v_exp_f32_e32 v94, v111
	v_add_f32_e32 v66, v90, v66
	v_exp_f32_e32 v95, v112
	v_add_f32_e32 v66, v91, v66
	v_exp_f32_e32 v96, v113
	v_add_f32_e32 v66, v92, v66
	v_fmamk_f32 v79, v79, 0x3e38aa3b, v101
	v_exp_f32_e32 v97, v114
	v_add_f32_e32 v66, v93, v66
	v_fmamk_f32 v80, v80, 0x3e38aa3b, v101
	v_exp_f32_e32 v104, v79
	v_add_f32_e32 v66, v94, v66
	v_fmac_f32_e32 v101, 0x3e38aa3b, v81
	v_exp_f32_e32 v105, v80
	v_add_f32_e32 v66, v95, v66
	v_exp_f32_e32 v101, v101
	v_add_f32_e32 v66, v96, v66
	v_add_f32_e32 v66, v97, v66
	v_add_f32_e32 v66, v104, v66
	v_add_f32_e32 v66, v105, v66
	v_add_f32_e32 v66, v101, v66
	v_mov_b32_e32 v67, v66
	s_mov_b32 s64, 0
	s_nop 0
	v_permlane32_swap_b32_e32 v66, v67
	v_cvt_pk_bf16_f32 v80, v102, v103
	v_cvt_pk_bf16_f32 v81, v82, v84
	v_cvt_pk_bf16_f32 v82, v77, v83
	v_cvt_pk_bf16_f32 v83, v76, v78
	v_cvt_pk_bf16_f32 v76, v73, v75
	v_cvt_pk_bf16_f32 v77, v71, v74
	v_cvt_pk_bf16_f32 v78, v69, v72
	v_cvt_pk_bf16_f32 v79, v68, v70
	v_cvt_pk_bf16_f32 v68, v85, v86
	v_cvt_pk_bf16_f32 v69, v87, v88
	v_cvt_pk_bf16_f32 v70, v89, v90
	v_cvt_pk_bf16_f32 v71, v91, v92
	v_cvt_pk_bf16_f32 v72, v93, v94
	v_cvt_pk_bf16_f32 v73, v95, v96
	v_cvt_pk_bf16_f32 v74, v97, v104
	v_cvt_pk_bf16_f32 v75, v105, v101
	s_nop 0
	v_permlane32_swap_b32_e32 v80, v82
	v_permlane32_swap_b32_e32 v81, v83
	v_permlane32_swap_b32_e32 v76, v78
	v_permlane32_swap_b32_e32 v77, v79
	v_permlane32_swap_b32_e32 v68, v70
	v_permlane32_swap_b32_e32 v69, v71
	v_permlane32_swap_b32_e32 v72, v74
	v_permlane32_swap_b32_e32 v73, v75
	ds_read_b64_tr_b16 v[84:85], v173 offset:0
	ds_read_b64_tr_b16 v[86:87], v173 offset:0x800
	ds_read_b64_tr_b16 v[88:89], v173 offset:0x1000
	ds_read_b64_tr_b16 v[90:91], v173 offset:0x1800
	ds_read_b64_tr_b16 v[92:93], v173 offset:0x2000
	ds_read_b64_tr_b16 v[94:95], v173 offset:0x2800
	ds_read_b64_tr_b16 v[102:103], v173 offset:0x3000
	ds_read_b64_tr_b16 v[104:105], v173 offset:0x3800
	s_waitcnt lgkmcnt(0)
	s_nop 0
	v_mfma_f32_32x32x16_bf16 v[2:17], v[80:83], v[84:87], v[2:17]
	ds_read_b64_tr_b16 v[84:85], v173 offset:0x200
	ds_read_b64_tr_b16 v[86:87], v173 offset:0xa00
	v_mfma_f32_32x32x16_bf16 v[2:17], v[76:79], v[88:91], v[2:17]
	ds_read_b64_tr_b16 v[88:89], v173 offset:0x1200
	ds_read_b64_tr_b16 v[90:91], v173 offset:0x1a00
	v_mfma_f32_32x32x16_bf16 v[2:17], v[68:71], v[92:95], v[2:17]
	ds_read_b64_tr_b16 v[92:93], v173 offset:0x2200
	ds_read_b64_tr_b16 v[94:95], v173 offset:0x2a00
	ds_read_b64_tr_b16 v[106:107], v173 offset:0x3200
	ds_read_b64_tr_b16 v[108:109], v173 offset:0x3a00
	v_mfma_f32_32x32x16_bf16 v[2:17], v[72:75], v[102:105], v[2:17]
	s_waitcnt lgkmcnt(0)
	v_mfma_f32_32x32x16_bf16 v[50:65], v[80:83], v[84:87], v[50:65]
	ds_read_b64_tr_b16 v[84:85], v173 offset:0x400
	ds_read_b64_tr_b16 v[86:87], v173 offset:0xc00
	v_mfma_f32_32x32x16_bf16 v[50:65], v[76:79], v[88:91], v[50:65]
	ds_read_b64_tr_b16 v[88:89], v173 offset:0x1400
	ds_read_b64_tr_b16 v[90:91], v173 offset:0x1c00
	v_mfma_f32_32x32x16_bf16 v[50:65], v[68:71], v[92:95], v[50:65]
	ds_read_b64_tr_b16 v[92:93], v173 offset:0x2400
	ds_read_b64_tr_b16 v[94:95], v173 offset:0x2c00
	ds_read_b64_tr_b16 v[102:103], v173 offset:0x3400
	ds_read_b64_tr_b16 v[104:105], v173 offset:0x3c00
	v_mfma_f32_32x32x16_bf16 v[50:65], v[72:75], v[106:109], v[50:65]
	s_waitcnt lgkmcnt(0)
	v_mfma_f32_32x32x16_bf16 v[34:49], v[80:83], v[84:87], v[34:49]
	ds_read_b64_tr_b16 v[84:85], v173 offset:0x600
	ds_read_b64_tr_b16 v[86:87], v173 offset:0xe00
	v_mfma_f32_32x32x16_bf16 v[34:49], v[76:79], v[88:91], v[34:49]
	ds_read_b64_tr_b16 v[88:89], v173 offset:0x1600
	ds_read_b64_tr_b16 v[90:91], v173 offset:0x1e00
	v_mfma_f32_32x32x16_bf16 v[34:49], v[68:71], v[92:95], v[34:49]
	ds_read_b64_tr_b16 v[92:93], v173 offset:0x2600
	ds_read_b64_tr_b16 v[94:95], v173 offset:0x2e00
	ds_read_b64_tr_b16 v[106:107], v173 offset:0x3600
	ds_read_b64_tr_b16 v[108:109], v173 offset:0x3e00
	v_mfma_f32_32x32x16_bf16 v[34:49], v[72:75], v[102:105], v[34:49]
	s_waitcnt lgkmcnt(0)
; __device__ __forceinline__ unsigned cvt_pk_bf16(float lo, float hi) { unsigned r; asm volatile("v_cvt_pk_bf16_f32 %0, %1, %2" : "=v"(r) : "v"(lo), "v"(hi)); return r; }
; __device__ __forceinline__ int crow(int r, int hi) { return (r & 3) + 8 * (r >> 2) + 4 * hi; }
; template <int MODE>
; __device__ __forceinline__ void attn_pass(const bf16_t* __restrict__ Qb, const bf16_t* __restrict__ Kh, const bf16_t* __restrict__ Vh, const int NT, const int kr0, const int g4, const int map,
;                                           LAS unsigned char* lds, f32x16 (&o)[4]) {
;     ...
;     if (hi == 0) li_l[r32] = l_reg; asm volatile("s_waitcnt lgkmcnt(0)" ::: "memory");
; #pragma unroll
;     for (int r = 0; r < 16; ++r) { const float rl = __builtin_amdgcn_rcpf(li_l[crow(r, hi)]);
; #pragma unroll
;         for (int d = 0; d < 4; ++d) o[d][r] *= rl; }
;     __syncthreads();
; __device__ __forceinline__ void p3_attention(Frame& F) {
;     ...
;         attn::attn_pass<1>(Qb, Kh, Vh, RPB / 64, 0, 0, 0, F.lds, o);
; #pragma unroll
;         for (int k = 0; k < 8; ++k) { const int d = k >> 1, r0 = (k & 1) * 8; u32x4 w;
;             w.x = cvt_pk_bf16(o[d][r0], o[d][r0 + 1]); w.y = cvt_pk_bf16(o[d][r0 + 2], o[d][r0 + 3]); w.z = cvt_pk_bf16(o[d][r0 + 4], o[d][r0 + 5]); w.w = cvt_pk_bf16(o[d][r0 + 6], o[d][r0 + 7]);
;             o1l[k * 512] = w; }
;         attn::attn_pass<1>(Qb + 64, Kh, Vh, RPB / 64, 0, 0, 1, F.lds, o);
	v_mfma_f32_32x32x16_bf16 v[18:33], v[80:83], v[84:87], v[18:33]
	v_mfma_f32_32x32x16_bf16 v[18:33], v[76:79], v[88:91], v[18:33]
	v_mfma_f32_32x32x16_bf16 v[18:33], v[68:71], v[92:95], v[18:33]
	v_mfma_f32_32x32x16_bf16 v[18:33], v[72:75], v[106:109], v[18:33]
	s_and_saveexec_b64 s[4:5], s[0:1]
	v_add_f32_e32 v68, v98, v99
	v_fmac_f32_e32 v68, v167, v141
	v_add_f32_e32 v66, v66, v67
	v_fmac_f32_e32 v66, v68, v100
	ds_write_b32 v171, v66
	s_or_b64 exec, exec, s[4:5]
	s_waitcnt lgkmcnt(0)
	ds_read_b128 v[66:69], v207
	ds_read_b128 v[70:73], v207 offset:32
	v_lshl_add_u32 v74, v0, 4, 0
	v_add_u32_e32 v200, 0x11800, v74
	s_movk_i32 s4, 0x80
	s_waitcnt lgkmcnt(1)
	v_rcp_f32_e32 v66, v66
	v_rcp_f32_e32 v67, v67
	v_bitop3_b32 v197, v166, v219, s4 bitop3:0x36
	s_movk_i32 s4, 0xa0
	v_mul_f32_e32 v74, v2, v66
	v_mul_f32_e32 v50, v50, v66
	v_mul_f32_e32 v34, v34, v66
	v_mul_f32_e32 v18, v18, v66
	v_mul_f32_e32 v66, v3, v67
	v_rcp_f32_e32 v2, v68
	v_rcp_f32_e32 v3, v69
	v_mul_f32_e32 v51, v51, v67
	v_mul_f32_e32 v35, v35, v67
	v_mul_f32_e32 v19, v19, v67
	v_mul_f32_e32 v67, v4, v2
	v_mul_f32_e32 v52, v52, v2
	v_mul_f32_e32 v36, v36, v2
	v_mul_f32_e32 v20, v20, v2
	v_mul_f32_e32 v68, v5, v3
	s_waitcnt lgkmcnt(0)
	v_rcp_f32_e32 v2, v70
	v_mul_f32_e32 v53, v53, v3
	v_mul_f32_e32 v37, v37, v3
	v_mul_f32_e32 v21, v21, v3
	v_rcp_f32_e32 v3, v71
	v_mul_f32_e32 v69, v6, v2
	v_mul_f32_e32 v54, v54, v2
	v_mul_f32_e32 v38, v38, v2
	v_mul_f32_e32 v22, v22, v2
	v_mul_f32_e32 v70, v7, v3
	v_mul_f32_e32 v55, v55, v3
	v_mul_f32_e32 v39, v39, v3
	v_mul_f32_e32 v23, v23, v3
	ds_read_b128 v[2:5], v207 offset:64
	v_rcp_f32_e32 v6, v72
	v_rcp_f32_e32 v72, v73
	v_bitop3_b32 v198, v166, v219, s4 bitop3:0x36
	s_movk_i32 s4, 0xc0
	v_mul_f32_e32 v71, v8, v6
	v_mul_f32_e32 v56, v56, v6
	v_mul_f32_e32 v40, v40, v6
	v_mul_f32_e32 v24, v24, v6
	v_mul_f32_e32 v73, v9, v72
	ds_read_b128 v[6:9], v207 offset:96
	s_waitcnt lgkmcnt(1)
	v_rcp_f32_e32 v2, v2
	v_rcp_f32_e32 v3, v3
	s_waitcnt lgkmcnt(0)
	s_barrier
	v_mul_f32_e32 v10, v10, v2
	v_mul_f32_e32 v58, v58, v2
	v_mul_f32_e32 v42, v42, v2
	v_mul_f32_e32 v26, v26, v2
	v_mul_f32_e32 v11, v11, v3
	v_rcp_f32_e32 v2, v4
	v_mul_f32_e32 v59, v59, v3
	v_mul_f32_e32 v43, v43, v3
	v_mul_f32_e32 v27, v27, v3
	v_rcp_f32_e32 v3, v5
	v_mul_f32_e32 v12, v12, v2
	v_mul_f32_e32 v60, v60, v2
	v_mul_f32_e32 v44, v44, v2
	v_mul_f32_e32 v28, v28, v2
	v_mul_f32_e32 v13, v13, v3
	v_rcp_f32_e32 v2, v6
	v_mul_f32_e32 v6, v61, v3
	v_mul_f32_e32 v45, v45, v3
	v_mul_f32_e32 v29, v29, v3
	v_rcp_f32_e32 v3, v7
	v_mul_f32_e32 v14, v14, v2
	v_mul_f32_e32 v7, v62, v2
	v_mul_f32_e32 v46, v46, v2
	v_mul_f32_e32 v30, v30, v2
	v_mul_f32_e32 v15, v15, v3
	v_rcp_f32_e32 v2, v8
	v_mul_f32_e32 v8, v63, v3
	v_mul_f32_e32 v47, v47, v3
	v_mul_f32_e32 v31, v31, v3
	v_rcp_f32_e32 v3, v9
	v_mul_f32_e32 v16, v16, v2
	v_mul_f32_e32 v9, v64, v2
	v_mul_f32_e32 v48, v48, v2
	v_mul_f32_e32 v32, v32, v2
	v_mul_f32_e32 v17, v17, v3
	v_mul_f32_e32 v61, v65, v3
	v_mul_f32_e32 v49, v49, v3
	v_mul_f32_e32 v33, v33, v3
	v_cvt_pk_bf16_f32 v2, v74, v66
	v_cvt_pk_bf16_f32 v3, v67, v68
	v_cvt_pk_bf16_f32 v4, v69, v70
	v_cvt_pk_bf16_f32 v5, v71, v73
	ds_write_b128 v200, v[2:5]
	v_cvt_pk_bf16_f32 v2, v10, v11
	v_cvt_pk_bf16_f32 v3, v12, v13
	v_cvt_pk_bf16_f32 v4, v14, v15
	v_cvt_pk_bf16_f32 v5, v16, v17
	v_mul_f32_e32 v57, v57, v72
	ds_write_b128 v200, v[2:5] offset:8192
	v_cvt_pk_bf16_f32 v2, v50, v51
	v_cvt_pk_bf16_f32 v3, v52, v53
	v_cvt_pk_bf16_f32 v4, v54, v55
	v_cvt_pk_bf16_f32 v5, v56, v57
	ds_write_b128 v200, v[2:5] offset:16384
	v_cvt_pk_bf16_f32 v2, v58, v59
	v_cvt_pk_bf16_f32 v3, v60, v6
	v_cvt_pk_bf16_f32 v4, v7, v8
	v_cvt_pk_bf16_f32 v5, v9, v61
	v_mul_f32_e32 v41, v41, v72
	ds_write_b128 v200, v[2:5] offset:24576
	v_cvt_pk_bf16_f32 v2, v34, v35
	v_cvt_pk_bf16_f32 v3, v36, v37
	v_cvt_pk_bf16_f32 v4, v38, v39
	v_cvt_pk_bf16_f32 v5, v40, v41
	ds_write_b128 v200, v[2:5] offset:32768
	v_cvt_pk_bf16_f32 v2, v42, v43
	v_cvt_pk_bf16_f32 v3, v44, v45
	v_cvt_pk_bf16_f32 v4, v46, v47
	v_cvt_pk_bf16_f32 v5, v48, v49
	v_mul_f32_e32 v25, v25, v72
	ds_write_b128 v200, v[2:5] offset:40960
	v_cvt_pk_bf16_f32 v2, v18, v19
	v_cvt_pk_bf16_f32 v3, v20, v21
	v_cvt_pk_bf16_f32 v4, v22, v23
	v_cvt_pk_bf16_f32 v5, v24, v25
	ds_write_b128 v200, v[2:5] offset:49152
	v_cvt_pk_bf16_f32 v2, v26, v27
	v_cvt_pk_bf16_f32 v3, v28, v29
	v_cvt_pk_bf16_f32 v4, v30, v31
	v_cvt_pk_bf16_f32 v5, v32, v33
	global_load_dwordx4 v[6:9], v[182:183], off
	global_load_dwordx4 v[10:13], v[184:185], off
	global_load_dwordx4 v[14:17], v[168:169], off offset:128
	global_load_dwordx4 v[110:113], v[178:179], off offset:128
	global_load_dwordx4 v[106:109], v[178:179], off offset:160
	global_load_dwordx4 v[102:105], v[178:179], off offset:192
	global_load_dwordx4 v[98:101], v[178:179], off offset:224
	ds_write_b128 v200, v[2:5] offset:57344
	v_mov_b32_e32 v2, 0x80
	v_lshl_or_b32 v58, v217, 1, v2
	v_bitop3_b32 v2, v58, v220, v221 bitop3:0xde
	v_add_u32_e32 v179, 0, v2
	v_add_u32_e32 v182, v218, v197
	s_waitcnt vmcnt(0)
	s_waitcnt vmcnt(6)
	ds_write_b128 v215, v[6:9]
	s_waitcnt vmcnt(5)
	ds_write_b128 v216, v[10:13]
	s_waitcnt vmcnt(4)
	ds_write_b128 v179, v[14:17] offset:32768
	s_waitcnt lgkmcnt(0)
	s_barrier
; #define SWAIT() do { if constexpr (MODE == 1) asm volatile("s_waitcnt vmcnt(3)" ::: "memory"); else asm volatile("s_waitcnt vmcnt(4)" ::: "memory"); } while (0)
; #define MASK(P0, P1, jt) do { if (MODE == 0 && (jt) >= 4) { const int kr_ = kr0 + (jt) - 4; const bool rv_ = (kr_ >= r0w) && (kr_ < r0w + 8); int br_ = kr_ - qR + 7; br_ = br_ < 0 ? 0 : (br_ > 14 ? 14 : br_); \
;     na_mask(P0, P1, rv_, biasL + 64 + br_ * 32 + (4 * hi - qc + 15), 4 * hi - cs); } } while (0)
; template <int MODE>
; __device__ __forceinline__ void partialSM(f32x16& p0, f32x16& p1, float& m_reg, float& mn, float& alpha) {
;     constexpr float SCALE = Cfg<MODE>::SCALE, C = SCALE * 1.4426950408889634f;
;     float pmax = p0[0];
; #pragma unroll
;     for (int r = 1; r < 16; ++r) pmax = fmaxf(pmax, p0[r]);
; #pragma unroll
;     for (int r = 0; r < 16; ++r) pmax = fmaxf(pmax, p1[r]);
;     { auto rr = __builtin_amdgcn_permlane32_swap(__float_as_uint(pmax), __float_as_uint(pmax), false, false);
;       pmax = fmaxf(__uint_as_float(rr[0]), __uint_as_float(rr[1])); }
;     if (__builtin_expect(__all(pmax - m_reg <= THR / SCALE), 1)) { mn = m_reg; alpha = 1.f; }
;     else { mn = fmaxf(m_reg, pmax); alpha = __builtin_amdgcn_exp2f((m_reg - mn) * C); m_reg = mn; }
;     const float mnC = -mn * C;
; #pragma unroll
;     for (int r = 0; r < 16; ++r) p0[r] = fmaf(p0[r], C, mnC);
; #pragma unroll
;     for (int r = 0; r < 16; ++r) p1[r] = fmaf(p1[r], C, mnC);
; #pragma unroll
;     for (int r = 0; r < 16; ++r) p0[r] = __builtin_amdgcn_exp2f(p0[r]);
; }
; template <int MODE>
; __device__ __forceinline__ void attn_pass(const bf16_t* __restrict__ Qb, const bf16_t* __restrict__ Kh, const bf16_t* __restrict__ Vh, const int NT, const int kr0, const int g4, const int map,
;                                           LAS unsigned char* lds, f32x16 (&o)[4]) {
;     ...
;     SLOAD(SE, 0); asm volatile("s_waitcnt vmcnt(0)" ::: "memory"); SWRITE(0, SE); __syncthreads();
;     qkt<MODE>(pA0, pA1, K_lds, qr, Qs, r32, hi, cbase); MASK(pA0, pA1, 0); partialSM<MODE>(pA0, pA1, m_reg, mnA, alA);
;     SLOAD(SO, 1); if (2 < NT) SLOAD(SE, 2);
;     SWAIT(); SWRITE(1, SO); __syncthreads();
	ds_read_b128 v[2:5], v182 offset:32768
	ds_read_b128 v[6:9], v182 offset:40960
	s_waitcnt vmcnt(3) lgkmcnt(1)
	v_mfma_f32_32x32x16_bf16 v[34:49], v[2:5], v[110:113], 0
	v_add_u32_e32 v184, v218, v198
	v_bitop3_b32 v196, v166, v219, s4 bitop3:0x36
	v_add_u32_e32 v183, v218, v196
	s_movk_i32 s4, 0xe0
	v_bitop3_b32 v194, v166, v219, s4 bitop3:0x36
	v_add_u32_e32 v185, v218, v194
	s_mov_b32 s4, 0x40000
	s_waitcnt lgkmcnt(0)
	v_mfma_f32_32x32x16_bf16 v[18:33], v[6:9], v[110:113], 0
	ds_read_b128 v[2:5], v184 offset:32768
	ds_read_b128 v[6:9], v184 offset:40960
	ds_read_b128 v[50:53], v185 offset:40960
	v_mov_b32_e32 v59, 0
	v_lshl_add_u64 v[58:59], v[180:181], 0, v[58:59]
	s_mov_b32 s7, 0x42800000
	s_mov_b32 s65, s64
	s_mov_b32 s66, s64
	s_waitcnt vmcnt(2) lgkmcnt(2)
	v_mfma_f32_32x32x16_bf16 v[34:49], v[2:5], v[106:109], v[34:49]
	ds_read_b128 v[2:5], v183 offset:32768
	s_mov_b32 s67, s64
	s_mov_b32 s68, s64
	s_mov_b32 s69, s64
	s_mov_b32 s70, s64
	s_mov_b32 s71, s64
	s_mov_b32 s72, s64
	s_waitcnt lgkmcnt(2)
	v_mfma_f32_32x32x16_bf16 v[18:33], v[6:9], v[106:109], v[18:33]
	ds_read_b128 v[6:9], v183 offset:40960
	s_mov_b32 s73, s64
	s_mov_b32 s74, s64
	s_mov_b32 s75, s64
	s_mov_b32 s76, s64
	s_mov_b32 s77, s64
	s_mov_b32 s78, s64
	s_waitcnt vmcnt(1) lgkmcnt(1)
	v_mfma_f32_32x32x16_bf16 v[34:49], v[2:5], v[102:105], v[34:49]
	ds_read_b128 v[2:5], v185 offset:32768
	s_mov_b32 s79, s64
	s_mov_b32 s44, 0x3e38aa3b
	v_mov_b32_e32 v178, 0
	s_mov_b32 s6, 1
	s_mov_b32 s43, 0x39560000
	s_mov_b32 s57, 0x38460000
	s_waitcnt lgkmcnt(1)
	v_mfma_f32_32x32x16_bf16 v[18:33], v[6:9], v[102:105], v[18:33]
	s_mov_b64 s[46:47], 0x40000
	s_waitcnt vmcnt(0) lgkmcnt(0)
	v_mfma_f32_32x32x16_bf16 v[34:49], v[2:5], v[98:101], v[34:49]
	v_mov_b64_e32 v[2:3], s[64:65]
	v_mov_b64_e32 v[16:17], s[78:79]
	v_mov_b64_e32 v[4:5], s[66:67]
	v_mov_b64_e32 v[6:7], s[68:69]
	v_mov_b64_e32 v[8:9], s[70:71]
	v_mov_b64_e32 v[10:11], s[72:73]
	v_mov_b64_e32 v[12:13], s[74:75]
	v_mfma_f32_32x32x16_bf16 v[18:33], v[50:53], v[98:101], v[18:33]
	s_nop 3
	v_max_f32_e32 v50, v34, v35
	v_max3_f32 v50, v50, v36, v37
	v_max3_f32 v50, v50, v38, v39
	v_max3_f32 v50, v50, v40, v41
	v_max3_f32 v50, v50, v42, v43
	v_max3_f32 v50, v50, v44, v45
	v_max3_f32 v50, v50, v46, v47
	v_max3_f32 v50, v50, v48, v49
	v_max3_f32 v62, v50, v18, v19
	v_max3_f32 v62, v62, v20, v21
	v_max3_f32 v62, v62, v22, v23
	v_max3_f32 v62, v62, v24, v25
	v_max3_f32 v64, v62, v26, v27
	v_add_co_u32_e32 v62, vcc, s4, v168
	global_load_dwordx4 v[50:53], v[190:191], off
	global_load_dwordx4 v[54:57], v[192:193], off
	v_addc_co_u32_e32 v63, vcc, 0, v169, vcc
	global_load_dwordx4 v[58:61], v[58:59], off
	s_nop 0
	global_load_dwordx4 v[122:125], v[62:63], off offset:128
	global_load_dwordx4 v[118:121], v[186:187], off
	global_load_dwordx4 v[114:117], v[188:189], off
	v_max3_f32 v62, v64, v28, v29
	v_max3_f32 v62, v62, v30, v31
	v_max3_f32 v62, v62, v32, v33
	v_mov_b32_e32 v63, v62
	s_nop 1
	v_permlane32_swap_b32_e32 v62, v63
	v_max_f32_e32 v62, v62, v63
	v_add_f32_e32 v63, 0x7149f2ca, v62
	v_max_f32_e32 v62, 0xf149f2ca, v62
	v_cmp_ge_f32_e32 vcc, s7, v63
	v_sub_f32_e32 v63, 0xf149f2ca, v62
	v_mul_f32_e32 v63, 0x3e38aa3b, v63
	s_cmp_eq_u64 vcc, exec
	v_exp_f32_e32 v63, v63
	v_mov_b32_e32 v64, 0xf149f2ca
	s_cselect_b64 vcc, -1, 0
	v_cndmask_b32_e32 v140, v62, v64, vcc
	v_mul_f32_e32 v62, 0xbe38aa3b, v140
	v_cndmask_b32_e64 v180, v63, 1.0, vcc
	v_mov_b32_e32 v63, v62
	v_fmamk_f32 v34, v34, 0x3e38aa3b, v62
	v_fmamk_f32 v35, v35, 0x3e38aa3b, v62
	v_fmamk_f32 v36, v36, 0x3e38aa3b, v62
	v_fmamk_f32 v37, v37, 0x3e38aa3b, v62
	v_fmamk_f32 v38, v38, 0x3e38aa3b, v62
	v_fmamk_f32 v39, v39, 0x3e38aa3b, v62
	v_fmamk_f32 v40, v40, 0x3e38aa3b, v62
	v_fmamk_f32 v41, v41, 0x3e38aa3b, v62
	v_fmamk_f32 v42, v42, 0x3e38aa3b, v62
	v_fmamk_f32 v43, v43, 0x3e38aa3b, v62
	v_fmamk_f32 v44, v44, 0x3e38aa3b, v62
	v_fmamk_f32 v45, v45, 0x3e38aa3b, v62
	v_fmamk_f32 v46, v46, 0x3e38aa3b, v62
	v_fmamk_f32 v47, v47, 0x3e38aa3b, v62
	v_fmamk_f32 v48, v48, 0x3e38aa3b, v62
	v_fmac_f32_e32 v63, 0x3e38aa3b, v49
	v_exp_f32_e32 v167, v34
	v_exp_f32_e32 v169, v35
	v_exp_f32_e32 v153, v36
	v_exp_f32_e32 v168, v37
	v_exp_f32_e32 v151, v38
	v_exp_f32_e32 v166, v39
	v_exp_f32_e32 v150, v40
	v_exp_f32_e32 v152, v41
	v_exp_f32_e32 v147, v42
	v_exp_f32_e32 v149, v43
	v_exp_f32_e32 v145, v44
	v_exp_f32_e32 v148, v45
	v_exp_f32_e32 v143, v46
	v_exp_f32_e32 v146, v47
	v_exp_f32_e32 v142, v48
	v_exp_f32_e32 v144, v63
	s_waitcnt vmcnt(3)
	v_mov_b64_e32 v[14:15], s[76:77]
	v_pk_fma_f32 v[134:135], v[32:33], s[44:45], v[62:63] op_sel_hi:[1,0,0]
	v_pk_fma_f32 v[136:137], v[30:31], s[44:45], v[62:63] op_sel_hi:[1,0,0]
	v_pk_fma_f32 v[138:139], v[28:29], s[44:45], v[62:63] op_sel_hi:[1,0,0]
	v_pk_fma_f32 v[126:127], v[26:27], s[44:45], v[62:63] op_sel_hi:[1,0,0]
	v_pk_fma_f32 v[128:129], v[24:25], s[44:45], v[62:63] op_sel_hi:[1,0,0]
	v_pk_fma_f32 v[130:131], v[22:23], s[44:45], v[62:63] op_sel_hi:[1,0,0]
	v_pk_fma_f32 v[66:67], v[20:21], s[44:45], v[62:63] op_sel_hi:[1,0,0]
	v_pk_fma_f32 v[132:133], v[18:19], s[44:45], v[62:63] op_sel_hi:[1,0,0]
	s_waitcnt vmcnt(5)
	ds_write_b128 v215, v[50:53] offset:16384
	s_waitcnt vmcnt(4)
	ds_write_b128 v216, v[54:57] offset:16384
	s_waitcnt vmcnt(3)
	ds_write_b128 v179, v[58:61] offset:49152
	v_mov_b64_e32 v[64:65], v[16:17]
	v_mov_b64_e32 v[48:49], v[16:17]
	v_mov_b64_e32 v[32:33], v[16:17]
	s_mov_b32 s45, 0x39570000
	v_mov_b64_e32 v[62:63], v[14:15]
	v_mov_b64_e32 v[60:61], v[12:13]
	v_mov_b64_e32 v[58:59], v[10:11]
	v_mov_b64_e32 v[56:57], v[8:9]
	v_mov_b64_e32 v[54:55], v[6:7]
	v_mov_b64_e32 v[52:53], v[4:5]
	v_mov_b64_e32 v[50:51], v[2:3]
	v_mov_b64_e32 v[46:47], v[14:15]
	v_mov_b64_e32 v[44:45], v[12:13]
	v_mov_b64_e32 v[42:43], v[10:11]
	v_mov_b64_e32 v[40:41], v[8:9]
	v_mov_b64_e32 v[38:39], v[6:7]
	v_mov_b64_e32 v[36:37], v[4:5]
	v_mov_b64_e32 v[34:35], v[2:3]
	v_mov_b64_e32 v[30:31], v[14:15]
	v_mov_b64_e32 v[28:29], v[12:13]
	v_mov_b64_e32 v[26:27], v[10:11]
	v_mov_b64_e32 v[24:25], v[8:9]
	v_mov_b64_e32 v[22:23], v[6:7]
	v_mov_b64_e32 v[20:21], v[4:5]
	v_mov_b64_e32 v[18:19], v[2:3]
	s_waitcnt lgkmcnt(0)
	s_barrier
; #define LAS __attribute__((address_space(3)))
; #define SBAR() __builtin_amdgcn_sched_barrier(0)
; __device__ __forceinline__ void finishSM(f32x16& p0, f32x16& p1, float alpha, float& l_reg, bf16x8& pa0, bf16x8& pa1, bf16x8& pa2, bf16x8& pa3) {
; #pragma unroll
;     for (int r = 0; r < 16; ++r) p1[r] = __builtin_amdgcn_exp2f(p1[r]);
;     float ps = 0;
; #pragma unroll
;     for (int r = 0; r < 16; ++r) ps += p0[r];
; #pragma unroll
;     for (int r = 0; r < 16; ++r) ps += p1[r];
;     { auto rr = __builtin_amdgcn_permlane32_swap(__float_as_uint(ps), __float_as_uint(ps), false, false);
;       ps = __uint_as_float(rr[0]) + __uint_as_float(rr[1]); }
;     l_reg = l_reg * alpha + ps;
;     ...
;     PK4(p0, 0, pa0); PK4(p0, 8, pa1); PK4(p1, 0, pa2); PK4(p1, 8, pa3);
;     ...
; }
; template <int MODE>
; __device__ __forceinline__ void qkt(f32x16& p0, f32x16& p1, const LAS unsigned char* Ks, const bf16x8* qr, const LAS unsigned char* Qs, int r32, int hi, int cbase) {
;     p0 = f32x16{}; p1 = f32x16{};
; #pragma unroll
;     for (int d0 = 0; d0 < Cfg<MODE>::ND; ++d0) { const int cb = cbase + (d0 * 16 + hi * 8) * 2;
;         const bf16x8 b0 = *(const LAS bf16x8*)(Ks + KSWZ(r32, cb));
;         const bf16x8 b1 = *(const LAS bf16x8*)(Ks + KSWZ(32 + r32, cb));
;         bf16x8 q; if constexpr (MODE == 0) q = *(const LAS bf16x8*)(Qs + KSWZ(r32, cb)); else q = qr[d0];
;         p0 = __builtin_amdgcn_mfma_f32_32x32x16_bf16(b0, q, p0, 0, 0, 0);
;         p1 = __builtin_amdgcn_mfma_f32_32x32x16_bf16(b1, q, p1, 0, 0, 0); }
; template <int MODE>
; __device__ __forceinline__ void attn_pass(const bf16_t* __restrict__ Qb, const bf16_t* __restrict__ Kh, const bf16_t* __restrict__ Vh, const int NT, const int kr0, const int g4, const int map,
;                                           LAS unsigned char* lds, f32x16 (&o)[4]) {
;     ...
;         SBAR(); qkt<MODE>(pB0, pB1, K_lds + SHM_K, qr, Qs, r32, hi, cbase); MASK(pB0, pB1, j);
;         finishSM(pA0, pA1, alA, l_reg, pa0, pa1, pa2, pa3); SBAR();
;         SLOAD(SO, j + 2 < NT ? j + 2 : NT - 1); SBAR();
;         pv_d0(o, vb0, pa0, pa1, pa2, pa3); partialSM<MODE>(pB0, pB1, m_reg, mnB, alB);
.LBB0_431:
	v_add_f32_e32 v181, 0, v167
	ds_read_b128 v[68:71], v182 offset:49152
	ds_read_b128 v[72:75], v182 offset:57344
	ds_read_b128 v[186:189], v184 offset:49152
	ds_read_b128 v[190:193], v184 offset:57344
	ds_read_b128 v[218:221], v183 offset:49152
	ds_read_b128 v[222:225], v183 offset:57344
	v_add_f32_e32 v181, v169, v181
	s_waitcnt lgkmcnt(5)
	v_mfma_f32_32x32x16_bf16 v[82:97], v[68:71], v[110:113], 0
	v_exp_f32_e32 v141, v66
	v_exp_f32_e32 v201, v67
	v_add_f32_e32 v181, v153, v181
	v_add_f32_e32 v181, v168, v181
	v_add_f32_e32 v181, v151, v181
	v_add_f32_e32 v181, v166, v181
	v_add_f32_e32 v181, v150, v181
	s_waitcnt lgkmcnt(4)
	v_mfma_f32_32x32x16_bf16 v[66:81], v[72:75], v[110:113], 0
	v_add_f32_e32 v181, v152, v181
	v_add_f32_e32 v181, v147, v181
	v_add_f32_e32 v181, v149, v181
	v_add_f32_e32 v181, v145, v181
	v_add_f32_e32 v181, v148, v181
	v_exp_f32_e32 v132, v132
	v_add_f32_e32 v181, v143, v181
	s_waitcnt lgkmcnt(3)
	v_mfma_f32_32x32x16_bf16 v[82:97], v[186:189], v[106:109], v[82:97]
	v_exp_f32_e32 v133, v133
	v_add_f32_e32 v181, v146, v181
	v_add_f32_e32 v181, v142, v181
	v_add_f32_e32 v181, v144, v181
	v_exp_f32_e32 v130, v130
	v_add_f32_e32 v181, v132, v181
	v_exp_f32_e32 v131, v131
	s_waitcnt lgkmcnt(2)
	v_mfma_f32_32x32x16_bf16 v[66:81], v[190:193], v[106:109], v[66:81]
	v_add_f32_e32 v181, v133, v181
	v_exp_f32_e32 v128, v128
	v_add_f32_e32 v181, v141, v181
	v_exp_f32_e32 v129, v129
	v_add_f32_e32 v181, v201, v181
	v_exp_f32_e32 v126, v126
	v_add_f32_e32 v181, v130, v181
	s_waitcnt lgkmcnt(1)
	v_mfma_f32_32x32x16_bf16 v[82:97], v[218:221], v[102:105], v[82:97]
	ds_read_b128 v[226:229], v185 offset:49152
	ds_read_b128 v[230:233], v185 offset:57344
	v_exp_f32_e32 v127, v127
	v_add_f32_e32 v181, v131, v181
	v_exp_f32_e32 v138, v138
	v_add_f32_e32 v181, v128, v181
	v_exp_f32_e32 v139, v139
	v_add_f32_e32 v181, v129, v181
	s_waitcnt lgkmcnt(2)
	v_mfma_f32_32x32x16_bf16 v[66:81], v[222:225], v[102:105], v[66:81]
	v_exp_f32_e32 v136, v136
	v_add_f32_e32 v181, v126, v181
	v_exp_f32_e32 v137, v137
	v_add_f32_e32 v181, v127, v181
	v_exp_f32_e32 v134, v134
	v_add_f32_e32 v181, v138, v181
	v_exp_f32_e32 v135, v135
	s_waitcnt lgkmcnt(1)
	v_mfma_f32_32x32x16_bf16 v[82:97], v[226:229], v[98:101], v[82:97]
	v_add_f32_e32 v181, v139, v181
	v_add_f32_e32 v181, v136, v181
	v_add_f32_e32 v181, v137, v181
	v_add_f32_e32 v181, v134, v181
	v_add_f32_e32 v181, v135, v181
	v_mov_b32_e32 v186, v181
	s_nop 1
	v_permlane32_swap_b32_e32 v181, v186
	s_waitcnt lgkmcnt(0)
	v_mfma_f32_32x32x16_bf16 v[66:81], v[230:233], v[98:101], v[66:81]
	v_cvt_pk_bf16_f32 v188, v167, v169
	v_cvt_pk_bf16_f32 v189, v153, v168
	v_cvt_pk_bf16_f32 v190, v151, v166
	v_cvt_pk_bf16_f32 v191, v150, v152
	v_cvt_pk_bf16_f32 v150, v147, v149
	v_cvt_pk_bf16_f32 v151, v145, v148
	v_cvt_pk_bf16_f32 v152, v143, v146
	v_cvt_pk_bf16_f32 v153, v142, v144
	v_cvt_pk_bf16_f32 v142, v132, v133
	v_cvt_pk_bf16_f32 v143, v141, v201
	v_cvt_pk_bf16_f32 v144, v130, v131
	v_cvt_pk_bf16_f32 v145, v128, v129
	v_cvt_pk_bf16_f32 v146, v126, v127
	v_cvt_pk_bf16_f32 v147, v138, v139
	v_cvt_pk_bf16_f32 v148, v136, v137
	v_cvt_pk_bf16_f32 v149, v134, v135
	s_nop 0
	v_permlane32_swap_b32_e32 v188, v190
	v_permlane32_swap_b32_e32 v189, v191
	v_permlane32_swap_b32_e32 v150, v152
	v_permlane32_swap_b32_e32 v151, v153
	v_permlane32_swap_b32_e32 v142, v144
	v_permlane32_swap_b32_e32 v143, v145
	v_permlane32_swap_b32_e32 v146, v148
	v_permlane32_swap_b32_e32 v147, v149
	v_lshl_add_u64 v[166:167], v[164:165], 0, s[20:21]
	v_add_co_u32_e32 v126, vcc, s43, v166
	v_lshl_add_u64 v[168:169], v[162:163], 0, s[20:21]
	s_nop 0
	v_addc_co_u32_e32 v127, vcc, 0, v167, vcc
	v_add_co_u32_e32 v130, vcc, s45, v166
	s_nop 1
	v_addc_co_u32_e32 v131, vcc, 0, v167, vcc
	v_add_co_u32_e32 v134, vcc, s57, v168
	global_load_dwordx4 v[126:129], v[126:127], off
	s_nop 0
	global_load_dwordx4 v[130:133], v[130:131], off
	v_addc_co_u32_e32 v135, vcc, 0, v169, vcc
	global_load_dwordx4 v[134:137], v[134:135], off offset:128
	ds_read_b64_tr_b16 v[218:219], v175 offset:0
	ds_read_b64_tr_b16 v[220:221], v175 offset:0x800
	ds_read_b64_tr_b16 v[222:223], v175 offset:0x1000
	ds_read_b64_tr_b16 v[224:225], v175 offset:0x1800
	ds_read_b64_tr_b16 v[226:227], v175 offset:0x2000
	ds_read_b64_tr_b16 v[228:229], v175 offset:0x2800
	ds_read_b64_tr_b16 v[230:231], v175 offset:0x3000
	ds_read_b64_tr_b16 v[232:233], v175 offset:0x3800
	s_waitcnt lgkmcnt(0)
	s_nop 0
	v_mfma_f32_32x32x16_bf16 v[2:17], v[188:191], v[218:221], v[2:17]
	ds_read_b64_tr_b16 v[218:219], v175 offset:0x200
	ds_read_b64_tr_b16 v[220:221], v175 offset:0xa00
	v_mfma_f32_32x32x16_bf16 v[2:17], v[150:153], v[222:225], v[2:17]
	ds_read_b64_tr_b16 v[222:223], v175 offset:0x1200
	ds_read_b64_tr_b16 v[224:225], v175 offset:0x1a00
	v_mfma_f32_32x32x16_bf16 v[2:17], v[142:145], v[226:229], v[2:17]
	ds_read_b64_tr_b16 v[226:227], v175 offset:0x2200
	ds_read_b64_tr_b16 v[228:229], v175 offset:0x2a00
	ds_read_b64_tr_b16 v[234:235], v175 offset:0x3200
	ds_read_b64_tr_b16 v[236:237], v175 offset:0x3a00
	v_mfma_f32_32x32x16_bf16 v[2:17], v[146:149], v[230:233], v[2:17]
	s_waitcnt lgkmcnt(0)
; #define SWAIT() do { if constexpr (MODE == 1) asm volatile("s_waitcnt vmcnt(3)" ::: "memory"); else asm volatile("s_waitcnt vmcnt(4)" ::: "memory"); } while (0)
; #define RESC(a) do { if (__any((a) < 1.f)) { if (hi == 0) al_l[r32] = (a); asm volatile("s_waitcnt lgkmcnt(0)" ::: "memory"); \
;     _Pragma("unroll") for (int d = 0; d < 4; ++d) _Pragma("unroll") for (int r = 0; r < 16; ++r) o[d][r] *= al_l[crow(r, hi)]; } } while (0)
; template <int MODE>
; __device__ __forceinline__ void partialSM(f32x16& p0, f32x16& p1, float& m_reg, float& mn, float& alpha) {
;     constexpr float SCALE = Cfg<MODE>::SCALE, C = SCALE * 1.4426950408889634f;
;     float pmax = p0[0];
; #pragma unroll
;     for (int r = 1; r < 16; ++r) pmax = fmaxf(pmax, p0[r]);
; #pragma unroll
;     for (int r = 0; r < 16; ++r) pmax = fmaxf(pmax, p1[r]);
;     { auto rr = __builtin_amdgcn_permlane32_swap(__float_as_uint(pmax), __float_as_uint(pmax), false, false);
;       pmax = fmaxf(__uint_as_float(rr[0]), __uint_as_float(rr[1])); }
;     if (__builtin_expect(__all(pmax - m_reg <= THR / SCALE), 1)) { mn = m_reg; alpha = 1.f; }
;     else { mn = fmaxf(m_reg, pmax); alpha = __builtin_amdgcn_exp2f((m_reg - mn) * C); m_reg = mn; }
; template <int MODE>
; __device__ __forceinline__ void attn_pass(const bf16_t* __restrict__ Qb, const bf16_t* __restrict__ Kh, const bf16_t* __restrict__ Vh, const int NT, const int kr0, const int g4, const int map,
;                                           LAS unsigned char* lds, f32x16 (&o)[4]) {
;     ...
;         pv_d0(o, vb0, pa0, pa1, pa2, pa3); partialSM<MODE>(pB0, pB1, m_reg, mnB, alB);
;         __syncthreads(); SWAIT(); SWRITE(0, SE);
;         RESC(alB); __syncthreads();
	v_mfma_f32_32x32x16_bf16 v[50:65], v[188:191], v[218:221], v[50:65]
	ds_read_b64_tr_b16 v[218:219], v175 offset:0x400
	ds_read_b64_tr_b16 v[220:221], v175 offset:0xc00
	v_mfma_f32_32x32x16_bf16 v[50:65], v[150:153], v[222:225], v[50:65]
	ds_read_b64_tr_b16 v[222:223], v175 offset:0x1400
	ds_read_b64_tr_b16 v[224:225], v175 offset:0x1c00
	v_mfma_f32_32x32x16_bf16 v[50:65], v[142:145], v[226:229], v[50:65]
	ds_read_b64_tr_b16 v[226:227], v175 offset:0x2400
	ds_read_b64_tr_b16 v[228:229], v175 offset:0x2c00
	ds_read_b64_tr_b16 v[230:231], v175 offset:0x3400
	ds_read_b64_tr_b16 v[232:233], v175 offset:0x3c00
	v_mfma_f32_32x32x16_bf16 v[50:65], v[146:149], v[234:237], v[50:65]
	s_waitcnt lgkmcnt(0)
	v_mfma_f32_32x32x16_bf16 v[34:49], v[188:191], v[218:221], v[34:49]
	ds_read_b64_tr_b16 v[218:219], v175 offset:0x600
	ds_read_b64_tr_b16 v[220:221], v175 offset:0xe00
	v_mfma_f32_32x32x16_bf16 v[34:49], v[150:153], v[222:225], v[34:49]
	ds_read_b64_tr_b16 v[222:223], v175 offset:0x1600
	ds_read_b64_tr_b16 v[224:225], v175 offset:0x1e00
	v_mfma_f32_32x32x16_bf16 v[34:49], v[142:145], v[226:229], v[34:49]
	ds_read_b64_tr_b16 v[226:227], v175 offset:0x2600
	ds_read_b64_tr_b16 v[228:229], v175 offset:0x2e00
	ds_read_b64_tr_b16 v[234:235], v175 offset:0x3600
	ds_read_b64_tr_b16 v[236:237], v175 offset:0x3e00
	v_mfma_f32_32x32x16_bf16 v[34:49], v[146:149], v[230:233], v[34:49]
	s_waitcnt lgkmcnt(0)
	v_mfma_f32_32x32x16_bf16 v[18:33], v[188:191], v[218:221], v[18:33]
	v_max_f32_e32 v138, v82, v83
	v_max3_f32 v138, v138, v84, v85
	v_max3_f32 v138, v138, v86, v87
	v_max3_f32 v138, v138, v88, v89
	v_max3_f32 v138, v138, v90, v91
	v_max3_f32 v138, v138, v92, v93
	v_mfma_f32_32x32x16_bf16 v[18:33], v[150:153], v[222:225], v[18:33]
	v_max3_f32 v138, v138, v94, v95
	v_max3_f32 v138, v138, v96, v97
	v_max3_f32 v138, v138, v66, v67
	v_max3_f32 v138, v138, v68, v69
	v_max3_f32 v138, v138, v70, v71
	v_max3_f32 v138, v138, v72, v73
	v_max3_f32 v138, v138, v74, v75
	v_max3_f32 v138, v138, v76, v77
	v_mfma_f32_32x32x16_bf16 v[18:33], v[142:145], v[226:229], v[18:33]
	v_max3_f32 v138, v138, v78, v79
	v_max3_f32 v138, v138, v80, v81
	v_mov_b32_e32 v139, v138
	s_nop 1
	v_permlane32_swap_b32_e32 v138, v139
	v_max_f32_e32 v138, v138, v139
	v_sub_f32_e32 v139, v138, v140
	v_max_f32_e32 v138, v140, v138
	v_mfma_f32_32x32x16_bf16 v[18:33], v[146:149], v[234:237], v[18:33]
	v_sub_f32_e32 v141, v140, v138
	v_mul_f32_e32 v141, 0x3e38aa3b, v141
	v_exp_f32_e32 v141, v141
	v_cmp_ge_f32_e32 vcc, s7, v139
	s_cmp_eq_u64 vcc, exec
	s_cselect_b64 s[4:5], -1, 0
	s_barrier
	s_waitcnt vmcnt(3)
	v_cndmask_b32_e64 v187, v141, 1.0, s[4:5]
	v_cmp_gt_f32_e32 vcc, 1.0, v187
	s_waitcnt vmcnt(3)
	ds_write_b128 v215, v[114:117]
	ds_write_b128 v216, v[118:121]
	ds_write_b128 v179, v[122:125] offset:32768
	s_cbranch_vccz .LBB0_435
	s_and_saveexec_b64 s[48:49], s[0:1]
	ds_write_b32 v171, v187 offset:128
	s_or_b64 exec, exec, s[48:49]
	s_waitcnt lgkmcnt(0)
	ds_read_b128 v[142:145], v207 offset:224
	ds_read_b128 v[146:149], v207 offset:192
	ds_read_b128 v[150:153], v207 offset:160
	ds_read_b128 v[188:191], v207 offset:128
	s_waitcnt lgkmcnt(3)
	v_pk_mul_f32 v[16:17], v[16:17], v[144:145]
	s_waitcnt lgkmcnt(2)
	v_pk_mul_f32 v[12:13], v[12:13], v[148:149]
	s_waitcnt lgkmcnt(1)
	v_pk_mul_f32 v[8:9], v[8:9], v[152:153]
	s_waitcnt lgkmcnt(0)
	v_pk_mul_f32 v[4:5], v[4:5], v[190:191]
	v_pk_mul_f32 v[14:15], v[14:15], v[142:143]
	v_pk_mul_f32 v[10:11], v[10:11], v[146:147]
	v_pk_mul_f32 v[6:7], v[6:7], v[150:151]
	v_pk_mul_f32 v[2:3], v[2:3], v[188:189]
	v_pk_mul_f32 v[64:65], v[64:65], v[144:145]
	v_pk_mul_f32 v[60:61], v[60:61], v[148:149]
	v_pk_mul_f32 v[56:57], v[56:57], v[152:153]
	v_pk_mul_f32 v[52:53], v[52:53], v[190:191]
	v_pk_mul_f32 v[62:63], v[62:63], v[142:143]
	v_pk_mul_f32 v[58:59], v[58:59], v[146:147]
	v_pk_mul_f32 v[54:55], v[54:55], v[150:151]
	v_pk_mul_f32 v[50:51], v[50:51], v[188:189]
	v_pk_mul_f32 v[48:49], v[48:49], v[144:145]
	v_pk_mul_f32 v[44:45], v[44:45], v[148:149]
	v_pk_mul_f32 v[40:41], v[40:41], v[152:153]
	v_pk_mul_f32 v[36:37], v[36:37], v[190:191]
	v_pk_mul_f32 v[46:47], v[46:47], v[142:143]
	v_pk_mul_f32 v[42:43], v[42:43], v[146:147]
	v_pk_mul_f32 v[38:39], v[38:39], v[150:151]
	v_pk_mul_f32 v[34:35], v[34:35], v[188:189]
	v_pk_mul_f32 v[32:33], v[32:33], v[144:145]
	v_pk_mul_f32 v[28:29], v[28:29], v[148:149]
	v_pk_mul_f32 v[24:25], v[24:25], v[152:153]
	v_pk_mul_f32 v[20:21], v[20:21], v[190:191]
	v_pk_mul_f32 v[30:31], v[30:31], v[142:143]
	v_pk_mul_f32 v[26:27], v[26:27], v[146:147]
	v_pk_mul_f32 v[22:23], v[22:23], v[150:151]
	v_pk_mul_f32 v[18:19], v[18:19], v[188:189]

; #define SWAIT() do { if constexpr (MODE == 1) asm volatile("s_waitcnt vmcnt(3)" ::: "memory"); else asm volatile("s_waitcnt vmcnt(4)" ::: "memory"); } while (0)
; #define RESC(a) do { if (__any((a) < 1.f)) { if (hi == 0) al_l[r32] = (a); asm volatile("s_waitcnt lgkmcnt(0)" ::: "memory"); \
;     _Pragma("unroll") for (int d = 0; d < 4; ++d) _Pragma("unroll") for (int r = 0; r < 16; ++r) o[d][r] *= al_l[crow(r, hi)]; } } while (0)
; template <int MODE>
; __device__ __forceinline__ void partialSM(f32x16& p0, f32x16& p1, float& m_reg, float& mn, float& alpha) {
;     constexpr float SCALE = Cfg<MODE>::SCALE, C = SCALE * 1.4426950408889634f;
;     float pmax = p0[0];
; #pragma unroll
;     for (int r = 1; r < 16; ++r) pmax = fmaxf(pmax, p0[r]);
; #pragma unroll
;     for (int r = 0; r < 16; ++r) pmax = fmaxf(pmax, p1[r]);
;     { auto rr = __builtin_amdgcn_permlane32_swap(__float_as_uint(pmax), __float_as_uint(pmax), false, false);
;       pmax = fmaxf(__uint_as_float(rr[0]), __uint_as_float(rr[1])); }
;     if (__builtin_expect(__all(pmax - m_reg <= THR / SCALE), 1)) { mn = m_reg; alpha = 1.f; }
;     else { mn = fmaxf(m_reg, pmax); alpha = __builtin_amdgcn_exp2f((m_reg - mn) * C); m_reg = mn; }
; template <int MODE>
; __device__ __forceinline__ void attn_pass(const bf16_t* __restrict__ Qb, const bf16_t* __restrict__ Kh, const bf16_t* __restrict__ Vh, const int NT, const int kr0, const int g4, const int map,
;                                           LAS unsigned char* lds, f32x16 (&o)[4]) {
;     ...
;         pv_d0(o, vb0 + SHM_V, pa0, pa1, pa2, pa3); partialSM<MODE>(pA0, pA1, m_reg, mnA, alA);
;         __syncthreads(); SWAIT(); SWRITE(1, SO);
;         RESC(alA); __syncthreads();
.LBB0_437:
	ds_read_b64_tr_b16 v[166:167], v173 offset:0
	ds_read_b64_tr_b16 v[168:169], v173 offset:0x800
	ds_read_b64_tr_b16 v[218:219], v173 offset:0x1000
	ds_read_b64_tr_b16 v[220:221], v173 offset:0x1800
	ds_read_b64_tr_b16 v[222:223], v173 offset:0x2000
	ds_read_b64_tr_b16 v[224:225], v173 offset:0x2800
	ds_read_b64_tr_b16 v[226:227], v173 offset:0x3000
	ds_read_b64_tr_b16 v[228:229], v173 offset:0x3800
	s_waitcnt lgkmcnt(0)
	s_nop 0
	v_mfma_f32_32x32x16_bf16 v[2:17], v[138:141], v[166:169], v[2:17]
	ds_read_b64_tr_b16 v[166:167], v173 offset:0x200
	ds_read_b64_tr_b16 v[168:169], v173 offset:0xa00
	v_mfma_f32_32x32x16_bf16 v[2:17], v[142:145], v[218:221], v[2:17]
	ds_read_b64_tr_b16 v[218:219], v173 offset:0x1200
	ds_read_b64_tr_b16 v[220:221], v173 offset:0x1a00
	v_mfma_f32_32x32x16_bf16 v[2:17], v[150:153], v[222:225], v[2:17]
	ds_read_b64_tr_b16 v[222:223], v173 offset:0x2200
	ds_read_b64_tr_b16 v[224:225], v173 offset:0x2a00
	ds_read_b64_tr_b16 v[230:231], v173 offset:0x3200
	ds_read_b64_tr_b16 v[232:233], v173 offset:0x3a00
	v_mfma_f32_32x32x16_bf16 v[2:17], v[146:149], v[226:229], v[2:17]
	s_waitcnt lgkmcnt(0)
	v_mfma_f32_32x32x16_bf16 v[50:65], v[138:141], v[166:169], v[50:65]
	ds_read_b64_tr_b16 v[166:167], v173 offset:0x400
	ds_read_b64_tr_b16 v[168:169], v173 offset:0xc00
	v_mfma_f32_32x32x16_bf16 v[50:65], v[142:145], v[218:221], v[50:65]
	ds_read_b64_tr_b16 v[218:219], v173 offset:0x1400
	ds_read_b64_tr_b16 v[220:221], v173 offset:0x1c00
	v_mfma_f32_32x32x16_bf16 v[50:65], v[150:153], v[222:225], v[50:65]
	ds_read_b64_tr_b16 v[222:223], v173 offset:0x2400
	ds_read_b64_tr_b16 v[224:225], v173 offset:0x2c00
	ds_read_b64_tr_b16 v[226:227], v173 offset:0x3400
	ds_read_b64_tr_b16 v[228:229], v173 offset:0x3c00
	v_mfma_f32_32x32x16_bf16 v[50:65], v[146:149], v[230:233], v[50:65]
	s_waitcnt lgkmcnt(0)
	v_mfma_f32_32x32x16_bf16 v[34:49], v[138:141], v[166:169], v[34:49]
	ds_read_b64_tr_b16 v[166:167], v173 offset:0x600
	ds_read_b64_tr_b16 v[168:169], v173 offset:0xe00
	v_mfma_f32_32x32x16_bf16 v[34:49], v[142:145], v[218:221], v[34:49]
	ds_read_b64_tr_b16 v[218:219], v173 offset:0x1600
	ds_read_b64_tr_b16 v[220:221], v173 offset:0x1e00
	v_mfma_f32_32x32x16_bf16 v[34:49], v[150:153], v[222:225], v[34:49]
	ds_read_b64_tr_b16 v[222:223], v173 offset:0x2600
	ds_read_b64_tr_b16 v[224:225], v173 offset:0x2e00
	ds_read_b64_tr_b16 v[230:231], v173 offset:0x3600
	ds_read_b64_tr_b16 v[232:233], v173 offset:0x3e00
	v_mfma_f32_32x32x16_bf16 v[34:49], v[146:149], v[226:229], v[34:49]
	s_waitcnt lgkmcnt(0)
	v_mfma_f32_32x32x16_bf16 v[18:33], v[138:141], v[166:169], v[18:33]
	v_max_f32_e32 v191, v82, v83
	v_max3_f32 v191, v191, v84, v85
	v_max3_f32 v191, v191, v86, v87
	v_max3_f32 v138, v191, v88, v89
	v_max3_f32 v138, v138, v90, v91
	v_max3_f32 v138, v138, v92, v93
	v_mfma_f32_32x32x16_bf16 v[18:33], v[142:145], v[218:221], v[18:33]
	v_max3_f32 v138, v138, v94, v95
	v_max3_f32 v138, v138, v96, v97
	v_max3_f32 v138, v138, v66, v67
	v_max3_f32 v138, v138, v68, v69
	v_max3_f32 v138, v138, v70, v71
	v_max3_f32 v138, v138, v72, v73
	v_max3_f32 v138, v138, v74, v75
	v_max3_f32 v138, v138, v76, v77
	v_mfma_f32_32x32x16_bf16 v[18:33], v[150:153], v[222:225], v[18:33]
	v_max3_f32 v138, v138, v78, v79
	v_max3_f32 v138, v138, v80, v81
	v_mov_b32_e32 v139, v138
	s_nop 1
	v_permlane32_swap_b32_e32 v138, v139
	v_max_f32_e32 v138, v138, v139
	v_sub_f32_e32 v139, v138, v188
	v_max_f32_e32 v138, v188, v138
	v_mfma_f32_32x32x16_bf16 v[18:33], v[146:149], v[230:233], v[18:33]
	v_sub_f32_e32 v140, v188, v138
	v_mul_f32_e32 v140, 0x3e38aa3b, v140
	v_exp_f32_e32 v140, v140
	v_cmp_ge_f32_e32 vcc, s7, v139
	s_cmp_eq_u64 vcc, exec
	s_cselect_b64 s[4:5], -1, 0
	s_barrier
	s_waitcnt vmcnt(3)
	v_cndmask_b32_e64 v141, v140, 1.0, s[4:5]
	v_cmp_gt_f32_e32 vcc, 1.0, v141
	s_waitcnt vmcnt(3)
	ds_write_b128 v215, v[126:129] offset:16384
	s_waitcnt vmcnt(3)
	ds_write_b128 v216, v[130:133] offset:16384
	s_waitcnt vmcnt(3)
	ds_write_b128 v179, v[134:137] offset:49152
	s_cbranch_vccz .LBB0_441
	s_and_saveexec_b64 s[52:53], s[0:1]
	ds_write_b32 v171, v141 offset:128
	s_or_b64 exec, exec, s[52:53]
	s_waitcnt lgkmcnt(0)
	ds_read_b128 v[126:129], v207 offset:224
	ds_read_b128 v[130:133], v207 offset:192
	ds_read_b128 v[134:137], v207 offset:160
	ds_read_b128 v[142:145], v207 offset:128
	s_waitcnt lgkmcnt(3)
	v_pk_mul_f32 v[16:17], v[16:17], v[128:129]
	s_waitcnt lgkmcnt(2)
	v_pk_mul_f32 v[12:13], v[12:13], v[132:133]
	s_waitcnt lgkmcnt(1)
	v_pk_mul_f32 v[8:9], v[8:9], v[136:137]
	s_waitcnt lgkmcnt(0)
	v_pk_mul_f32 v[4:5], v[4:5], v[144:145]
	v_pk_mul_f32 v[14:15], v[14:15], v[126:127]
	v_pk_mul_f32 v[10:11], v[10:11], v[130:131]
	v_pk_mul_f32 v[6:7], v[6:7], v[134:135]
	v_pk_mul_f32 v[2:3], v[2:3], v[142:143]
	v_pk_mul_f32 v[64:65], v[64:65], v[128:129]
	v_pk_mul_f32 v[60:61], v[60:61], v[132:133]
	v_pk_mul_f32 v[56:57], v[56:57], v[136:137]
	v_pk_mul_f32 v[52:53], v[52:53], v[144:145]
	v_pk_mul_f32 v[62:63], v[62:63], v[126:127]
	v_pk_mul_f32 v[58:59], v[58:59], v[130:131]
	v_pk_mul_f32 v[54:55], v[54:55], v[134:135]
	v_pk_mul_f32 v[50:51], v[50:51], v[142:143]
	v_pk_mul_f32 v[48:49], v[48:49], v[128:129]
	v_pk_mul_f32 v[44:45], v[44:45], v[132:133]
	v_pk_mul_f32 v[40:41], v[40:41], v[136:137]
	v_pk_mul_f32 v[36:37], v[36:37], v[144:145]
	v_pk_mul_f32 v[46:47], v[46:47], v[126:127]
	v_pk_mul_f32 v[42:43], v[42:43], v[130:131]
	v_pk_mul_f32 v[38:39], v[38:39], v[134:135]
	v_pk_mul_f32 v[34:35], v[34:35], v[142:143]
	v_pk_mul_f32 v[32:33], v[32:33], v[128:129]
	v_pk_mul_f32 v[28:29], v[28:29], v[132:133]
	v_pk_mul_f32 v[24:25], v[24:25], v[136:137]
	v_pk_mul_f32 v[20:21], v[20:21], v[144:145]
	v_pk_mul_f32 v[30:31], v[30:31], v[126:127]
	v_pk_mul_f32 v[26:27], v[26:27], v[130:131]
	v_pk_mul_f32 v[22:23], v[22:23], v[134:135]
	v_pk_mul_f32 v[18:19], v[18:19], v[142:143]

; #define LAS __attribute__((address_space(3)))
; #define SBAR() __builtin_amdgcn_sched_barrier(0)
; #define MASK(P0, P1, jt) do { if (MODE == 0 && (jt) >= 4) { const int kr_ = kr0 + (jt) - 4; const bool rv_ = (kr_ >= r0w) && (kr_ < r0w + 8); int br_ = kr_ - qR + 7; br_ = br_ < 0 ? 0 : (br_ > 14 ? 14 : br_); \
;     na_mask(P0, P1, rv_, biasL + 64 + br_ * 32 + (4 * hi - qc + 15), 4 * hi - cs); } } while (0)
; __device__ __forceinline__ void finishSM(f32x16& p0, f32x16& p1, float alpha, float& l_reg, bf16x8& pa0, bf16x8& pa1, bf16x8& pa2, bf16x8& pa3) {
; #pragma unroll
;     for (int r = 0; r < 16; ++r) p1[r] = __builtin_amdgcn_exp2f(p1[r]);
;     float ps = 0;
; #pragma unroll
;     for (int r = 0; r < 16; ++r) ps += p0[r];
; #pragma unroll
;     for (int r = 0; r < 16; ++r) ps += p1[r];
;     { auto rr = __builtin_amdgcn_permlane32_swap(__float_as_uint(ps), __float_as_uint(ps), false, false);
;       ps = __uint_as_float(rr[0]) + __uint_as_float(rr[1]); }
;     l_reg = l_reg * alpha + ps;
;     ...
;     PK4(p0, 0, pa0); PK4(p0, 8, pa1); PK4(p1, 0, pa2); PK4(p1, 8, pa3);
;     ...
; }
; template <int MODE>
; __device__ __forceinline__ void qkt(f32x16& p0, f32x16& p1, const LAS unsigned char* Ks, const bf16x8* qr, const LAS unsigned char* Qs, int r32, int hi, int cbase) {
;     p0 = f32x16{}; p1 = f32x16{};
; #pragma unroll
;     for (int d0 = 0; d0 < Cfg<MODE>::ND; ++d0) { const int cb = cbase + (d0 * 16 + hi * 8) * 2;
;         const bf16x8 b0 = *(const LAS bf16x8*)(Ks + KSWZ(r32, cb));
;         const bf16x8 b1 = *(const LAS bf16x8*)(Ks + KSWZ(32 + r32, cb));
;         bf16x8 q; if constexpr (MODE == 0) q = *(const LAS bf16x8*)(Qs + KSWZ(r32, cb)); else q = qr[d0];
;         p0 = __builtin_amdgcn_mfma_f32_32x32x16_bf16(b0, q, p0, 0, 0, 0);
;         p1 = __builtin_amdgcn_mfma_f32_32x32x16_bf16(b1, q, p1, 0, 0, 0); }
; template <int MODE>
; __device__ __forceinline__ void attn_pass(const bf16_t* __restrict__ Qb, const bf16_t* __restrict__ Kh, const bf16_t* __restrict__ Vh, const int NT, const int kr0, const int g4, const int map,
;                                           LAS unsigned char* lds, f32x16 (&o)[4]) {
;     ...
;     SBAR(); qkt<MODE>(pB0, pB1, K_lds + SHM_K, qr, Qs, r32, hi, cbase); MASK(pB0, pB1, NT - 1);
;     finishSM(pA0, pA1, alA, l_reg, pa0, pa1, pa2, pa3); SBAR();
;     pv_d0(o, vb0, pa0, pa1, pa2, pa3); partialSM<MODE>(pB0, pB1, m_reg, mnB, alB);
.LBB0_443:
	ds_read_b128 v[68:71], v182 offset:49152
	ds_read_b128 v[72:75], v182 offset:57344
	ds_read_b128 v[114:117], v184 offset:49152
	ds_read_b128 v[118:121], v184 offset:57344
	ds_read_b128 v[122:125], v183 offset:49152
	ds_read_b128 v[162:165], v183 offset:57344
	s_waitcnt lgkmcnt(5)
	v_mfma_f32_32x32x16_bf16 v[82:97], v[68:71], v[110:113], 0
	v_exp_f32_e32 v179, v66
	v_exp_f32_e32 v180, v67
	v_exp_f32_e32 v132, v132
	v_exp_f32_e32 v133, v133
	v_exp_f32_e32 v130, v130
	ds_read_b128 v[186:189], v185 offset:49152
	ds_read_b128 v[190:193], v185 offset:57344
	s_waitcnt lgkmcnt(6)
	v_mfma_f32_32x32x16_bf16 v[66:81], v[72:75], v[110:113], 0
	v_exp_f32_e32 v112, v129
	v_add_f32_e32 v129, 0, v167
	v_add_f32_e32 v129, v169, v129
	v_add_f32_e32 v129, v153, v129
	v_exp_f32_e32 v110, v131
	v_exp_f32_e32 v111, v128
	v_exp_f32_e32 v113, v126
	s_waitcnt lgkmcnt(5)
	v_mfma_f32_32x32x16_bf16 v[82:97], v[114:117], v[106:109], v[82:97]
	v_exp_f32_e32 v126, v127
	v_exp_f32_e32 v127, v138
	v_exp_f32_e32 v128, v139
	v_exp_f32_e32 v114, v136
	v_exp_f32_e32 v115, v137
	v_exp_f32_e32 v116, v134
	v_exp_f32_e32 v117, v135
	s_waitcnt lgkmcnt(4)
	v_mfma_f32_32x32x16_bf16 v[66:81], v[118:121], v[106:109], v[66:81]
	v_add_f32_e32 v106, v168, v129
	v_add_f32_e32 v106, v151, v106
	v_add_f32_e32 v106, v166, v106
	v_add_f32_e32 v106, v150, v106
	v_add_f32_e32 v106, v152, v106
	v_add_f32_e32 v106, v147, v106
	v_add_f32_e32 v106, v149, v106
	v_add_f32_e32 v106, v145, v106
	v_add_f32_e32 v106, v148, v106
	v_add_f32_e32 v106, v143, v106
	v_add_f32_e32 v106, v146, v106
	v_add_f32_e32 v106, v142, v106
	v_add_f32_e32 v106, v144, v106
	v_add_f32_e32 v106, v132, v106
	s_waitcnt lgkmcnt(3)
	v_mfma_f32_32x32x16_bf16 v[82:97], v[122:125], v[102:105], v[82:97]
	s_waitcnt lgkmcnt(2)
	v_mfma_f32_32x32x16_bf16 v[66:81], v[162:165], v[102:105], v[66:81]
	v_add_f32_e32 v102, v133, v106
	v_add_f32_e32 v102, v179, v102
	v_add_f32_e32 v102, v180, v102
	v_add_f32_e32 v102, v130, v102
	v_add_f32_e32 v102, v110, v102
	v_add_f32_e32 v102, v111, v102
	v_add_f32_e32 v102, v112, v102
	v_add_f32_e32 v102, v113, v102
	v_add_f32_e32 v102, v126, v102
	s_waitcnt lgkmcnt(1)
	v_mfma_f32_32x32x16_bf16 v[82:97], v[186:189], v[98:101], v[82:97]
	v_add_f32_e32 v102, v127, v102
	v_add_f32_e32 v102, v128, v102
	v_add_f32_e32 v102, v114, v102
	v_add_f32_e32 v102, v115, v102
	v_add_f32_e32 v102, v116, v102
	s_waitcnt lgkmcnt(0)
	v_mfma_f32_32x32x16_bf16 v[66:81], v[190:193], v[98:101], v[66:81]
	v_add_f32_e32 v98, v117, v102
	v_mov_b32_e32 v99, v98
	v_cvt_pk_bf16_f32 v100, v167, v169
	v_cvt_pk_bf16_f32 v101, v153, v168
	v_cvt_pk_bf16_f32 v102, v151, v166
	v_cvt_pk_bf16_f32 v103, v150, v152
	s_nop 1
	v_permlane32_swap_b32_e32 v98, v99
	v_permlane32_swap_b32_e32 v100, v102
	v_permlane32_swap_b32_e32 v101, v103
	v_cvt_pk_bf16_f32 v104, v147, v149
	v_cvt_pk_bf16_f32 v105, v145, v148
	v_cvt_pk_bf16_f32 v106, v143, v146
	v_cvt_pk_bf16_f32 v107, v142, v144
	v_cvt_pk_bf16_f32 v108, v132, v133
	v_cvt_pk_bf16_f32 v109, v179, v180
	v_cvt_pk_bf16_f32 v110, v130, v110
	v_cvt_pk_bf16_f32 v111, v111, v112
	v_cvt_pk_bf16_f32 v112, v113, v126
	v_cvt_pk_bf16_f32 v113, v127, v128
	v_cvt_pk_bf16_f32 v114, v114, v115
	v_cvt_pk_bf16_f32 v115, v116, v117
	s_nop 0
	v_permlane32_swap_b32_e32 v104, v106
	v_permlane32_swap_b32_e32 v105, v107
	v_permlane32_swap_b32_e32 v108, v110
	v_permlane32_swap_b32_e32 v109, v111
	v_permlane32_swap_b32_e32 v112, v114
	v_permlane32_swap_b32_e32 v113, v115
	ds_read_b64_tr_b16 v[116:117], v175 offset:0
	ds_read_b64_tr_b16 v[118:119], v175 offset:0x800
	ds_read_b64_tr_b16 v[120:121], v175 offset:0x1000
	ds_read_b64_tr_b16 v[122:123], v175 offset:0x1800
	ds_read_b64_tr_b16 v[124:125], v175 offset:0x2000
	ds_read_b64_tr_b16 v[126:127], v175 offset:0x2800
	ds_read_b64_tr_b16 v[128:129], v175 offset:0x3000
	ds_read_b64_tr_b16 v[130:131], v175 offset:0x3800
	s_waitcnt lgkmcnt(0)
	s_nop 0
	v_mfma_f32_32x32x16_bf16 v[2:17], v[100:103], v[116:119], v[2:17]
	ds_read_b64_tr_b16 v[116:117], v175 offset:0x200
	ds_read_b64_tr_b16 v[118:119], v175 offset:0xa00
	v_mfma_f32_32x32x16_bf16 v[2:17], v[104:107], v[120:123], v[2:17]
	ds_read_b64_tr_b16 v[120:121], v175 offset:0x1200
	ds_read_b64_tr_b16 v[122:123], v175 offset:0x1a00
	v_mfma_f32_32x32x16_bf16 v[2:17], v[108:111], v[124:127], v[2:17]
	ds_read_b64_tr_b16 v[124:125], v175 offset:0x2200
	ds_read_b64_tr_b16 v[126:127], v175 offset:0x2a00
	ds_read_b64_tr_b16 v[132:133], v175 offset:0x3200
	ds_read_b64_tr_b16 v[134:135], v175 offset:0x3a00
	v_mfma_f32_32x32x16_bf16 v[2:17], v[112:115], v[128:131], v[2:17]
	s_waitcnt lgkmcnt(0)
; #define RESC(a) do { if (__any((a) < 1.f)) { if (hi == 0) al_l[r32] = (a); asm volatile("s_waitcnt lgkmcnt(0)" ::: "memory"); \
;     _Pragma("unroll") for (int d = 0; d < 4; ++d) _Pragma("unroll") for (int r = 0; r < 16; ++r) o[d][r] *= al_l[crow(r, hi)]; } } while (0)
; template <int MODE>
; __device__ __forceinline__ void partialSM(f32x16& p0, f32x16& p1, float& m_reg, float& mn, float& alpha) {
;     constexpr float SCALE = Cfg<MODE>::SCALE, C = SCALE * 1.4426950408889634f;
;     float pmax = p0[0];
; #pragma unroll
;     for (int r = 1; r < 16; ++r) pmax = fmaxf(pmax, p0[r]);
; #pragma unroll
;     for (int r = 0; r < 16; ++r) pmax = fmaxf(pmax, p1[r]);
;     { auto rr = __builtin_amdgcn_permlane32_swap(__float_as_uint(pmax), __float_as_uint(pmax), false, false);
;       pmax = fmaxf(__uint_as_float(rr[0]), __uint_as_float(rr[1])); }
;     if (__builtin_expect(__all(pmax - m_reg <= THR / SCALE), 1)) { mn = m_reg; alpha = 1.f; }
;     else { mn = fmaxf(m_reg, pmax); alpha = __builtin_amdgcn_exp2f((m_reg - mn) * C); m_reg = mn; }
;     const float mnC = -mn * C;
; #pragma unroll
;     for (int r = 0; r < 16; ++r) p0[r] = fmaf(p0[r], C, mnC);
; #pragma unroll
;     for (int r = 0; r < 16; ++r) p1[r] = fmaf(p1[r], C, mnC);
; #pragma unroll
;     for (int r = 0; r < 16; ++r) p0[r] = __builtin_amdgcn_exp2f(p0[r]);
; }
; template <int MODE>
; __device__ __forceinline__ void attn_pass(const bf16_t* __restrict__ Qb, const bf16_t* __restrict__ Kh, const bf16_t* __restrict__ Vh, const int NT, const int kr0, const int g4, const int map,
;                                           LAS unsigned char* lds, f32x16 (&o)[4]) {
;     ...
;     pv_d0(o, vb0, pa0, pa1, pa2, pa3); partialSM<MODE>(pB0, pB1, m_reg, mnB, alB);
;     __syncthreads(); RESC(alB);
	v_mfma_f32_32x32x16_bf16 v[50:65], v[100:103], v[116:119], v[50:65]
	ds_read_b64_tr_b16 v[116:117], v175 offset:0x400
	ds_read_b64_tr_b16 v[118:119], v175 offset:0xc00
	v_mfma_f32_32x32x16_bf16 v[50:65], v[104:107], v[120:123], v[50:65]
	ds_read_b64_tr_b16 v[120:121], v175 offset:0x1400
	ds_read_b64_tr_b16 v[122:123], v175 offset:0x1c00
	v_mfma_f32_32x32x16_bf16 v[50:65], v[108:111], v[124:127], v[50:65]
	ds_read_b64_tr_b16 v[124:125], v175 offset:0x2400
	ds_read_b64_tr_b16 v[126:127], v175 offset:0x2c00
	ds_read_b64_tr_b16 v[128:129], v175 offset:0x3400
	ds_read_b64_tr_b16 v[130:131], v175 offset:0x3c00
	v_mfma_f32_32x32x16_bf16 v[50:65], v[112:115], v[132:135], v[50:65]
	s_waitcnt lgkmcnt(0)
	v_mfma_f32_32x32x16_bf16 v[34:49], v[100:103], v[116:119], v[34:49]
	ds_read_b64_tr_b16 v[116:117], v175 offset:0x600
	ds_read_b64_tr_b16 v[118:119], v175 offset:0xe00
	v_mfma_f32_32x32x16_bf16 v[34:49], v[104:107], v[120:123], v[34:49]
	ds_read_b64_tr_b16 v[120:121], v175 offset:0x1600
	ds_read_b64_tr_b16 v[122:123], v175 offset:0x1e00
	v_mfma_f32_32x32x16_bf16 v[34:49], v[108:111], v[124:127], v[34:49]
	ds_read_b64_tr_b16 v[124:125], v175 offset:0x2600
	ds_read_b64_tr_b16 v[126:127], v175 offset:0x2e00
	ds_read_b64_tr_b16 v[132:133], v175 offset:0x3600
	ds_read_b64_tr_b16 v[134:135], v175 offset:0x3e00
	v_mfma_f32_32x32x16_bf16 v[34:49], v[112:115], v[128:131], v[34:49]
	s_waitcnt lgkmcnt(0)
	v_mfma_f32_32x32x16_bf16 v[18:33], v[100:103], v[116:119], v[18:33]
	v_max_f32_e32 v128, v82, v83
	v_max3_f32 v128, v128, v84, v85
	v_max3_f32 v128, v128, v86, v87
	v_max3_f32 v100, v128, v88, v89
	v_max3_f32 v100, v100, v90, v91
	v_max3_f32 v100, v100, v92, v93
	v_mfma_f32_32x32x16_bf16 v[18:33], v[104:107], v[120:123], v[18:33]
	v_max3_f32 v100, v100, v94, v95
	v_max3_f32 v100, v100, v96, v97
	v_max3_f32 v100, v100, v66, v67
	v_max3_f32 v100, v100, v68, v69
	v_max3_f32 v100, v100, v70, v71
	v_max3_f32 v100, v100, v72, v73
	v_max3_f32 v100, v100, v74, v75
	v_max3_f32 v100, v100, v76, v77
	v_mfma_f32_32x32x16_bf16 v[18:33], v[108:111], v[124:127], v[18:33]
	v_max3_f32 v100, v100, v78, v79
	v_max3_f32 v100, v100, v80, v81
	v_mov_b32_e32 v101, v100
	s_nop 1
	v_permlane32_swap_b32_e32 v100, v101
	v_max_f32_e32 v100, v100, v101
	v_max_f32_e32 v102, v140, v100
	v_sub_f32_e32 v101, v100, v140
	v_mfma_f32_32x32x16_bf16 v[18:33], v[112:115], v[132:135], v[18:33]
	v_sub_f32_e32 v100, v140, v102
	s_mov_b32 s4, 0x42800000
	v_mul_f32_e32 v100, 0x3e38aa3b, v100
	v_exp_f32_e32 v100, v100
	v_cmp_ge_f32_e32 vcc, s4, v101
	s_cmp_eq_u64 vcc, exec
	s_cselect_b64 vcc, -1, 0
	v_cndmask_b32_e32 v101, v102, v140, vcc
	v_cndmask_b32_e64 v100, v100, 1.0, vcc
	v_mul_f32_e32 v101, 0xbe38aa3b, v101
	v_fmamk_f32 v82, v82, 0x3e38aa3b, v101
	v_fmamk_f32 v83, v83, 0x3e38aa3b, v101
	v_fmamk_f32 v84, v84, 0x3e38aa3b, v101
	v_fmamk_f32 v85, v85, 0x3e38aa3b, v101
	v_fmamk_f32 v86, v86, 0x3e38aa3b, v101
	v_fmamk_f32 v87, v87, 0x3e38aa3b, v101
	v_fmamk_f32 v88, v88, 0x3e38aa3b, v101
	v_fmamk_f32 v89, v89, 0x3e38aa3b, v101
	v_fmamk_f32 v90, v90, 0x3e38aa3b, v101
	v_fmamk_f32 v91, v91, 0x3e38aa3b, v101
	v_fmamk_f32 v92, v92, 0x3e38aa3b, v101
	v_fmamk_f32 v93, v93, 0x3e38aa3b, v101
	v_fmamk_f32 v94, v94, 0x3e38aa3b, v101
	v_fmamk_f32 v95, v95, 0x3e38aa3b, v101
	v_fmamk_f32 v96, v96, 0x3e38aa3b, v101
	v_fmamk_f32 v97, v97, 0x3e38aa3b, v101
	v_cmp_gt_f32_e32 vcc, 1.0, v100
	s_barrier
	s_cbranch_vccz .LBB0_447
	s_and_saveexec_b64 s[4:5], s[0:1]
	ds_write_b32 v171, v100 offset:128
	s_or_b64 exec, exec, s[4:5]
	s_waitcnt lgkmcnt(0)
	ds_read_b128 v[102:105], v207 offset:224
	ds_read_b128 v[106:109], v207 offset:192
	ds_read_b128 v[110:113], v207 offset:160
	ds_read_b128 v[114:117], v207 offset:128
	s_waitcnt lgkmcnt(3)
	v_pk_mul_f32 v[16:17], v[16:17], v[104:105]
	s_waitcnt lgkmcnt(2)
	v_pk_mul_f32 v[12:13], v[12:13], v[108:109]
	s_waitcnt lgkmcnt(1)
	v_pk_mul_f32 v[8:9], v[8:9], v[112:113]
	s_waitcnt lgkmcnt(0)
	v_pk_mul_f32 v[4:5], v[4:5], v[116:117]
	v_pk_mul_f32 v[14:15], v[14:15], v[102:103]
	v_pk_mul_f32 v[10:11], v[10:11], v[106:107]
	v_pk_mul_f32 v[6:7], v[6:7], v[110:111]
	v_pk_mul_f32 v[2:3], v[2:3], v[114:115]
	v_pk_mul_f32 v[64:65], v[64:65], v[104:105]
	v_pk_mul_f32 v[60:61], v[60:61], v[108:109]
	v_pk_mul_f32 v[56:57], v[56:57], v[112:113]
	v_pk_mul_f32 v[52:53], v[52:53], v[116:117]
	v_pk_mul_f32 v[62:63], v[62:63], v[102:103]
	v_pk_mul_f32 v[58:59], v[58:59], v[106:107]
	v_pk_mul_f32 v[54:55], v[54:55], v[110:111]
	v_pk_mul_f32 v[50:51], v[50:51], v[114:115]
	v_pk_mul_f32 v[48:49], v[48:49], v[104:105]
	v_pk_mul_f32 v[44:45], v[44:45], v[108:109]
	v_pk_mul_f32 v[40:41], v[40:41], v[112:113]
	v_pk_mul_f32 v[36:37], v[36:37], v[116:117]
	v_pk_mul_f32 v[46:47], v[46:47], v[102:103]
	v_pk_mul_f32 v[42:43], v[42:43], v[106:107]
	v_pk_mul_f32 v[38:39], v[38:39], v[110:111]
	v_pk_mul_f32 v[34:35], v[34:35], v[114:115]
	v_pk_mul_f32 v[32:33], v[32:33], v[104:105]
	v_pk_mul_f32 v[28:29], v[28:29], v[108:109]
	v_pk_mul_f32 v[24:25], v[24:25], v[112:113]
	v_pk_mul_f32 v[20:21], v[20:21], v[116:117]
	v_pk_mul_f32 v[30:31], v[30:31], v[102:103]
	v_pk_mul_f32 v[26:27], v[26:27], v[106:107]
	v_pk_mul_f32 v[22:23], v[22:23], v[110:111]
	v_pk_mul_f32 v[18:19], v[18:19], v[114:115]

; #define LAS __attribute__((address_space(3)))
; __device__ __forceinline__ int v_st(int k, int c) { const int kk = (k & ~0xC) | ((k & 4) << 1) | ((k & 8) >> 1); return ((kk >> 3) * 4 + (c >> 5)) * 512 + ((kk & 7) * 32 + (c & 31)) * 2; }
; __device__ __forceinline__ int v_rd_base(int lane) { return ((lane & 3) << 3) | (((lane >> 2) & 3) << 6) | (((lane >> 4) & 1) << 5) | (((lane >> 5) & 1) << 8); }
; #define MASK(P0, P1, jt) do { if (MODE == 0 && (jt) >= 4) { const int kr_ = kr0 + (jt) - 4; const bool rv_ = (kr_ >= r0w) && (kr_ < r0w + 8); int br_ = kr_ - qR + 7; br_ = br_ < 0 ? 0 : (br_ > 14 ? 14 : br_); \
;     na_mask(P0, P1, rv_, biasL + 64 + br_ * 32 + (4 * hi - qc + 15), 4 * hi - cs); } } while (0)
; template <int MODE>
; __device__ __forceinline__ void attn_pass(const bf16_t* __restrict__ Qb, const bf16_t* __restrict__ Kh, const bf16_t* __restrict__ Vh, const int NT, const int kr0, const int g4, const int map,
;                                           LAS unsigned char* lds, f32x16 (&o)[4]) {
;     ...
;     const bf16_t* Qw = Qb + (long)(wid * QBLK + r32) * LDK + hi * 8;
;     LAS unsigned char* Qs = lds + OFF_Q + wid * (QBLK * 256);
; #pragma unroll
;     for (int d0 = 0; d0 < ND; ++d0) { qr[d0] = *(const bf16x8*)(Qw + d0 * 16); if constexpr (MODE == 0) *(LAS bf16x8*)(Qs + KSWZ(r32, (d0 * 16 + hi * 8) * 2)) = qr[d0]; }
;     const int cbase = MODE == 1 ? map * 128 : 0;
;     const int sr = tid >> 4, sc = (tid & 15) * 8, vst0 = v_st(sr, sc), vst1 = v_st(32 + sr, sc);
;     const int vb0 = (int)(uintptr_t)V_lds + v_rd_base(lane);
;     const int qR = g4 * 4 + (wid >> 1), qc = 32 * (wid & 1) + r32, cs = qc < 8 ? 0 : (qc > 56 ? 48 : qc - 8);
;     const int r0w = qR < 4 ? 0 : (qR > 60 ? 56 : qR - 4);
;     struct { bf16x8 vs0, vs1, ks0, ks1; } sr_[2];
;     ...
;     const int kr1 = tid >> 3, kc1 = map * 64 + (tid & 7) * 8;
;     ...
;     f32x16 pA0, pA1, pB0, pB1; float mnA, mnB, alA, alB; bf16x8 pa0, pa1, pa2, pa3;
;     constexpr int SE = 0, SO = 1;
;     SLOAD(SE, 0); asm volatile("s_waitcnt vmcnt(0)" ::: "memory"); SWRITE(0, SE); __syncthreads();
;     qkt<MODE>(pA0, pA1, K_lds, qr, Qs, r32, hi, cbase); MASK(pA0, pA1, 0); partialSM<MODE>(pA0, pA1, m_reg, mnA, alA);
.LBB0_459:
	s_or_b64 exec, exec, s[4:5]
	s_lshl_b32 s6, s38, 1
	s_add_u32 s4, s82, s24
	s_addc_u32 s5, s83, s25
	s_add_u32 s4, s4, s6
	s_addc_u32 s5, s5, 0
	s_add_u32 s24, s4, 0x36200000
	s_addc_u32 s25, s5, 0
	s_add_u32 s38, s4, 0x37300000
	s_addc_u32 s39, s5, 0
	s_lshl_b64 s[4:5], s[40:41], 1
	s_add_u32 s4, s82, s4
	s_addc_u32 s5, s83, s5
	v_mov_b32_e32 v177, 0
	s_add_u32 s4, s4, s6
	v_lshrrev_b32_e32 v51, 6, v0
	v_lshlrev_b32_e32 v2, 1, v214
	s_addc_u32 s5, s5, 0
	v_lshl_or_b32 v2, v51, 16, v2
	v_mov_b32_e32 v3, v177
	v_lshl_add_u64 v[2:3], s[4:5], 0, v[2:3]
	v_lshlrev_b32_e32 v4, 1, v160
	v_mov_b32_e32 v5, v177
	v_lshl_add_u64 v[2:3], v[2:3], 0, v[4:5]
	s_mov_b64 s[4:5], 0x3a600000
	v_lshlrev_b32_e32 v34, 10, v174
	v_lshl_add_u64 v[30:31], v[2:3], 0, s[4:5]
	s_mov_b32 s4, 0x3a600000
	v_or_b32_e32 v66, v34, v156
	v_add_co_u32_e32 v26, vcc, s4, v2
	v_lshlrev_b32_e32 v70, 1, v66
	v_or_b32_e32 v154, 0x408000, v66
	v_addc_co_u32_e32 v27, vcc, 0, v3, vcc
	v_or_b32_e32 v42, 0x800000, v70
	v_mov_b32_e32 v43, v177
	v_lshlrev_b64 v[44:45], 1, v[154:155]
	s_waitcnt lgkmcnt(0)
	s_barrier
	global_load_dwordx4 v[2:5], v[30:31], off offset:32
	global_load_dwordx4 v[6:9], v[30:31], off offset:64
	global_load_dwordx4 v[10:13], v[30:31], off offset:96
	global_load_dwordx4 v[14:17], v[30:31], off offset:128
	global_load_dwordx4 v[18:21], v[30:31], off offset:160
	global_load_dwordx4 v[22:25], v[30:31], off offset:192
	s_nop 0
	global_load_dwordx4 v[26:29], v[26:27], off
	s_nop 0
	global_load_dwordx4 v[30:33], v[30:31], off offset:224
	v_lshl_add_u64 v[34:35], s[38:39], 0, v[42:43]
	v_lshl_add_u64 v[38:39], s[38:39], 0, v[44:45]
	v_lshl_add_u64 v[42:43], s[24:25], 0, v[42:43]
	v_lshl_add_u64 v[46:47], s[24:25], 0, v[44:45]
	global_load_dwordx4 v[34:37], v[34:35], off
	s_nop 0
	global_load_dwordx4 v[38:41], v[38:39], off
	s_nop 0
	global_load_dwordx4 v[42:45], v[42:43], off
	s_nop 0
	global_load_dwordx4 v[46:49], v[46:47], off
	v_lshlrev_b32_e32 v190, 1, v156
	v_lshlrev_b32_e32 v52, 8, v174
	v_and_b32_e32 v53, 0x70, v0
	v_lshlrev_b32_e32 v54, 8, v176
	v_and_b32_e32 v56, 48, v190
	v_bitop3_b32 v52, v190, v52, v53 bitop3:0xde
	v_bitop3_b32 v53, v190, v54, v53 bitop3:0xde
	v_or_b32_e32 v54, v161, v56
	s_add_i32 s4, 0, 0x11800
	v_add_u32_e32 v199, 0, v54
	v_lshl_add_u32 v54, v51, 13, s4
	v_add_u32_e32 v51, v54, v157
	v_or_b32_e32 v55, v213, v157
	v_or_b32_e32 v56, v210, v56
	v_add_u32_e32 v192, 0, v52
	v_add_u32_e32 v52, v51, v213
	v_add_u32_e32 v193, 0, v53
	v_add_u32_e32 v200, 0, v56
	v_add_u32_e32 v53, v51, v209
	v_add_u32_e32 v56, v51, v211
	v_add_u32_e32 v57, v51, v212
	v_add_u32_e32 v58, v51, v197
	v_add_u32_e32 v59, v51, v198
	v_add_u32_e32 v60, v51, v196
	v_add_u32_e32 v51, v51, v194
	v_add_u32_e32 v201, 0, v55
	v_add_u32_e32 v202, v54, v55
	v_and_or_b32 v75, v50, 32, v172
	v_cmp_lt_u32_e32 vcc, 7, v75
	v_lshrrev_b32_e32 v74, 7, v0
	v_add_u32_e32 v191, s21, v74
	s_mov_b32 s7, 0x42b504f3
	v_or_b32_e32 v154, 0x418000, v66
	v_mov_b32_e32 v219, 0xf149f2ca
	v_mov_b32_e32 v71, v177
	s_mov_b32 s40, 0
	s_mov_b32 s41, s40
	s_mov_b32 s42, s40
	s_mov_b32 s43, s40
	s_mov_b32 s44, s40
	s_mov_b32 s45, s40
	s_mov_b32 s46, s40
	s_mov_b32 s47, s40
	s_mov_b32 s48, s40
	s_mov_b32 s49, s40
	s_mov_b32 s50, s40
	s_mov_b32 s51, s40
	s_mov_b32 s52, s40
	s_mov_b32 s53, s40
	s_mov_b32 s54, s40
	s_mov_b32 s55, s40
	s_waitcnt vmcnt(5)
	ds_write_b128 v52, v[26:29]
	ds_write_b128 v53, v[2:5]
	ds_write_b128 v56, v[6:9]
	ds_write_b128 v57, v[10:13]
	ds_write_b128 v58, v[14:17]
	ds_write_b128 v59, v[18:21]
	ds_write_b128 v60, v[22:25]
	s_waitcnt vmcnt(4)
	ds_write_b128 v51, v[30:33]
	s_waitcnt vmcnt(0)
	s_waitcnt vmcnt(3)
	ds_write_b128 v199, v[34:37]
	s_waitcnt vmcnt(2)
	ds_write_b128 v200, v[38:41]
	s_waitcnt vmcnt(1)
	ds_write_b128 v192, v[42:45] offset:32768
	s_waitcnt vmcnt(0)
	ds_write_b128 v193, v[46:49] offset:32768
	s_waitcnt lgkmcnt(0)
	s_barrier
	ds_read_b128 v[2:5], v201 offset:32768
	ds_read_b128 v[10:13], v195 offset:40960
	ds_read_b128 v[6:9], v202
	s_waitcnt lgkmcnt(0)
	v_mfma_f32_32x32x16_bf16 v[34:49], v[2:5], v[6:9], 0
	ds_read_b128 v[2:5], v204 offset:40960
	v_or_b32_e32 v14, v209, v157
	v_add_u32_e32 v203, 0, v14
	v_add_u32_e32 v209, v54, v14
	v_or_b32_e32 v14, v211, v157
	v_add_u32_e32 v210, 0, v14
	v_add_u32_e32 v211, v54, v14
	s_waitcnt lgkmcnt(0)
	v_mfma_f32_32x32x16_bf16 v[18:33], v[2:5], v[6:9], 0
	ds_read_b128 v[2:5], v203 offset:32768
	ds_read_b128 v[6:9], v209
	v_or_b32_e32 v14, v212, v157
	v_add_u32_e32 v212, 0, v14
	v_add_u32_e32 v213, v54, v14
	v_or_b32_e32 v14, v197, v157
	v_add_u32_e32 v197, 0, v14
	s_waitcnt lgkmcnt(0)
	v_mfma_f32_32x32x16_bf16 v[34:49], v[2:5], v[6:9], v[34:49]
	ds_read_b128 v[2:5], v210 offset:32768
	v_add_u32_e32 v214, v54, v14
	v_or_b32_e32 v51, v198, v157
	v_add_u32_e32 v198, 0, v51
	v_add_u32_e32 v215, v54, v51
	v_or_b32_e32 v58, 0x820000, v70
	v_mov_b32_e32 v59, v177
	v_mfma_f32_32x32x16_bf16 v[18:33], v[10:13], v[6:9], v[18:33]
	ds_read_b128 v[6:9], v211
	ds_read_b128 v[10:13], v206 offset:40960
	v_lshlrev_b64 v[60:61], 1, v[154:155]
	v_lshl_add_u64 v[62:63], s[24:25], 0, v[60:61]
	v_or_b32_e32 v154, 0x428000, v66
	v_or_b32_e32 v70, 0x840000, v70
	v_lshl_add_u64 v[72:73], s[24:25], 0, v[70:71]
	s_waitcnt lgkmcnt(1)
	v_mfma_f32_32x32x16_bf16 v[34:49], v[2:5], v[6:9], v[34:49]
	ds_read_b128 v[2:5], v205 offset:40960
	s_mov_b64 s[4:5], 0x36200000
	v_lshlrev_b32_e32 v187, 2, v208
	v_sub_u32_e32 v208, v187, v75
	s_mov_b32 s6, 1
	v_lshl_add_u32 v222, v208, 2, 0
	v_mov_b32_e32 v188, v177
	s_waitcnt lgkmcnt(0)
	v_mfma_f32_32x32x16_bf16 v[18:33], v[2:5], v[6:9], v[18:33]
	ds_read_b128 v[2:5], v212 offset:32768
	ds_read_b128 v[6:9], v213
	s_waitcnt lgkmcnt(0)
; #define SWAIT() do { if constexpr (MODE == 1) asm volatile("s_waitcnt vmcnt(3)" ::: "memory"); else asm volatile("s_waitcnt vmcnt(4)" ::: "memory"); } while (0)
; template <int MODE>
; __device__ __forceinline__ void partialSM(f32x16& p0, f32x16& p1, float& m_reg, float& mn, float& alpha) {
;     constexpr float SCALE = Cfg<MODE>::SCALE, C = SCALE * 1.4426950408889634f;
;     float pmax = p0[0];
; #pragma unroll
;     for (int r = 1; r < 16; ++r) pmax = fmaxf(pmax, p0[r]);
; #pragma unroll
;     for (int r = 0; r < 16; ++r) pmax = fmaxf(pmax, p1[r]);
;     { auto rr = __builtin_amdgcn_permlane32_swap(__float_as_uint(pmax), __float_as_uint(pmax), false, false);
;       pmax = fmaxf(__uint_as_float(rr[0]), __uint_as_float(rr[1])); }
;     if (__builtin_expect(__all(pmax - m_reg <= THR / SCALE), 1)) { mn = m_reg; alpha = 1.f; }
;     else { mn = fmaxf(m_reg, pmax); alpha = __builtin_amdgcn_exp2f((m_reg - mn) * C); m_reg = mn; }
;     const float mnC = -mn * C;
; #pragma unroll
;     for (int r = 0; r < 16; ++r) p0[r] = fmaf(p0[r], C, mnC);
; #pragma unroll
;     for (int r = 0; r < 16; ++r) p1[r] = fmaf(p1[r], C, mnC);
; #pragma unroll
;     for (int r = 0; r < 16; ++r) p0[r] = __builtin_amdgcn_exp2f(p0[r]);
; }
; template <int MODE>
; __device__ __forceinline__ void attn_pass(const bf16_t* __restrict__ Qb, const bf16_t* __restrict__ Kh, const bf16_t* __restrict__ Vh, const int NT, const int kr0, const int g4, const int map,
;                                           LAS unsigned char* lds, f32x16 (&o)[4]) {
;     ...
;     const int qR = g4 * 4 + (wid >> 1), qc = 32 * (wid & 1) + r32, cs = qc < 8 ? 0 : (qc > 56 ? 48 : qc - 8);
;     const int r0w = qR < 4 ? 0 : (qR > 60 ? 56 : qR - 4);
;     struct { bf16x8 vs0, vs1, ks0, ks1; } sr_[2];
;     ...
;     const int kr1 = tid >> 3, kc1 = map * 64 + (tid & 7) * 8;
;     ...
;     f32x16 pA0, pA1, pB0, pB1; float mnA, mnB, alA, alB; bf16x8 pa0, pa1, pa2, pa3;
;     constexpr int SE = 0, SO = 1;
;     SLOAD(SE, 0); asm volatile("s_waitcnt vmcnt(0)" ::: "memory"); SWRITE(0, SE); __syncthreads();
;     qkt<MODE>(pA0, pA1, K_lds, qr, Qs, r32, hi, cbase); MASK(pA0, pA1, 0); partialSM<MODE>(pA0, pA1, m_reg, mnA, alA);
;     SLOAD(SO, 1); if (2 < NT) SLOAD(SE, 2);
;     SWAIT(); SWRITE(1, SO); __syncthreads();
	v_mfma_f32_32x32x16_bf16 v[34:49], v[2:5], v[6:9], v[34:49]
	ds_read_b128 v[2:5], v197 offset:32768
	v_mfma_f32_32x32x16_bf16 v[18:33], v[10:13], v[6:9], v[18:33]
	ds_read_b128 v[6:9], v214
	ds_read_b128 v[10:13], v182 offset:40960
	s_waitcnt lgkmcnt(1)
	v_mfma_f32_32x32x16_bf16 v[34:49], v[2:5], v[6:9], v[34:49]
	ds_read_b128 v[2:5], v198 offset:32768
	ds_read_b128 v[14:17], v184 offset:40960
	s_waitcnt lgkmcnt(2)
	v_mfma_f32_32x32x16_bf16 v[18:33], v[10:13], v[6:9], v[18:33]
	ds_read_b128 v[6:9], v215
	v_min_u32_e32 v10, 56, v75
	v_or_b32_e32 v11, v196, v157
	v_add_u32_e32 v216, 0, v11
	v_add_u32_e32 v217, v54, v11
	s_waitcnt lgkmcnt(0)
	v_mfma_f32_32x32x16_bf16 v[34:49], v[2:5], v[6:9], v[34:49]
	v_add_u32_e32 v2, -8, v10
	v_cndmask_b32_e32 v76, 0, v2, vcc
	ds_read_b128 v[2:5], v216 offset:32768
	v_min_u32_e32 v10, 60, v191
	v_add_u32_e32 v10, -4, v10
	v_cmp_lt_u32_e32 vcc, 3, v191
	v_sub_u32_e32 v189, v187, v76
	v_mfma_f32_32x32x16_bf16 v[18:33], v[14:17], v[6:9], v[18:33]
	ds_read_b128 v[6:9], v217
	v_cndmask_b32_e32 v196, 0, v10, vcc
	ds_read_b128 v[10:13], v183 offset:40960
	v_or_b32_e32 v14, v194, v157
	v_add_u32_e32 v194, 0, v14
	v_add_u32_e32 v218, v54, v14
	v_add_u32_e32 v221, 8, v196
	s_waitcnt lgkmcnt(1)
	v_mfma_f32_32x32x16_bf16 v[34:49], v[2:5], v[6:9], v[34:49]
	ds_read_b128 v[2:5], v194 offset:32768
	ds_read_b128 v[50:53], v185 offset:40960
	ds_read_b128 v[54:57], v218
	s_waitcnt lgkmcnt(3)
	v_mfma_f32_32x32x16_bf16 v[18:33], v[10:13], v[6:9], v[18:33]
	s_waitcnt lgkmcnt(0)
	v_mfma_f32_32x32x16_bf16 v[34:49], v[2:5], v[54:57], v[34:49]
	v_mov_b64_e32 v[2:3], s[40:41]
	v_mov_b64_e32 v[4:5], s[42:43]
	v_mov_b64_e32 v[6:7], s[44:45]
	v_mov_b64_e32 v[8:9], s[46:47]
	v_mov_b64_e32 v[10:11], s[48:49]
	v_mov_b64_e32 v[12:13], s[50:51]
	v_mov_b64_e32 v[14:15], s[52:53]
	v_mfma_f32_32x32x16_bf16 v[18:33], v[50:53], v[54:57], v[18:33]
	s_nop 3
	v_max_f32_e32 v50, v34, v35
	v_max3_f32 v50, v50, v36, v37
	v_max3_f32 v50, v50, v38, v39
	v_max3_f32 v50, v50, v40, v41
	v_max3_f32 v50, v50, v42, v43
	v_max3_f32 v50, v50, v44, v45
	v_max3_f32 v50, v50, v46, v47
	v_max3_f32 v50, v50, v48, v49
	v_max3_f32 v50, v50, v18, v19
	v_max3_f32 v50, v50, v20, v21
	v_max3_f32 v50, v50, v22, v23
	v_max3_f32 v50, v50, v24, v25
	v_max3_f32 v50, v50, v26, v27
	v_max3_f32 v67, v50, v28, v29
	v_max3_f32 v67, v67, v30, v31
	v_max3_f32 v67, v67, v32, v33
	v_mov_b32_e32 v68, v67
	s_nop 1
	v_permlane32_swap_b32_e32 v67, v68
	v_max_f32_e32 v67, v67, v68
	v_add_f32_e32 v68, 0x7149f2ca, v67
	v_cmp_ge_f32_e32 vcc, s7, v68
	s_cmp_eq_u64 vcc, exec
	v_max_f32_e32 v67, 0xf149f2ca, v67
	v_lshl_add_u64 v[50:51], s[38:39], 0, v[58:59]
	v_lshl_add_u64 v[54:55], s[38:39], 0, v[60:61]
	v_lshl_add_u64 v[58:59], s[24:25], 0, v[58:59]
	v_sub_f32_e32 v68, 0xf149f2ca, v67
	s_cselect_b64 vcc, -1, 0
	global_load_dwordx4 v[50:53], v[50:51], off
	s_nop 0
	global_load_dwordx4 v[54:57], v[54:55], off
	s_nop 0
	global_load_dwordx4 v[58:61], v[58:59], off
	s_nop 0
	global_load_dwordx4 v[62:65], v[62:63], off
	v_mul_f32_e32 v68, 0x3e0293ee, v68
	v_cndmask_b32_e32 v164, v67, v219, vcc
	v_lshlrev_b64 v[66:67], 1, v[154:155]
	v_exp_f32_e32 v77, v68
	v_lshl_add_u64 v[68:69], s[24:25], 0, v[66:67]
	v_lshl_add_u64 v[66:67], s[38:39], 0, v[66:67]
	global_load_dwordx4 v[142:145], v[68:69], off
	global_load_dwordx4 v[138:141], v[72:73], off
	v_lshl_add_u64 v[68:69], s[38:39], 0, v[70:71]
	global_load_dwordx4 v[134:137], v[66:67], off
	global_load_dwordx4 v[130:133], v[68:69], off
	v_mul_f32_e32 v66, 0xbe0293ee, v164
	v_mov_b32_e32 v67, v66
	v_mov_b64_e32 v[16:17], s[54:55]
	s_mov_b32 s40, 0x3e0293ee
	v_fmac_f32_e32 v67, 0x3e0293ee, v49
	v_pk_fma_f32 v[160:161], v[32:33], s[40:41], v[66:67] op_sel_hi:[1,0,0]
	v_pk_fma_f32 v[162:163], v[30:31], s[40:41], v[66:67] op_sel_hi:[1,0,0]
	v_pk_fma_f32 v[146:147], v[28:29], s[40:41], v[66:67] op_sel_hi:[1,0,0]
	v_pk_fma_f32 v[148:149], v[26:27], s[40:41], v[66:67] op_sel_hi:[1,0,0]
	v_pk_fma_f32 v[150:151], v[24:25], s[40:41], v[66:67] op_sel_hi:[1,0,0]
	v_pk_fma_f32 v[152:153], v[22:23], s[40:41], v[66:67] op_sel_hi:[1,0,0]
	v_pk_fma_f32 v[154:155], v[20:21], s[40:41], v[66:67] op_sel_hi:[1,0,0]
	v_pk_fma_f32 v[156:157], v[18:19], s[40:41], v[66:67] op_sel_hi:[1,0,0]
	s_lshl_b32 s41, s57, 6
	s_ashr_i32 s42, s41, 31
	v_mov_b32_e32 v19, s42
	v_or_b32_e32 v18, s41, v174
	s_add_u32 s42, s20, s56
	v_lshlrev_b64 v[18:19], 11, v[18:19]
	s_addc_u32 s43, 0, s3
	v_lshl_add_u64 v[18:19], s[42:43], 0, v[18:19]
	v_fmamk_f32 v34, v34, 0x3e0293ee, v66
	v_fmamk_f32 v35, v35, 0x3e0293ee, v66
	v_fmamk_f32 v36, v36, 0x3e0293ee, v66
	v_fmamk_f32 v37, v37, 0x3e0293ee, v66
	v_fmamk_f32 v38, v38, 0x3e0293ee, v66
	v_fmamk_f32 v39, v39, 0x3e0293ee, v66
	v_fmamk_f32 v40, v40, 0x3e0293ee, v66
	v_fmamk_f32 v41, v41, 0x3e0293ee, v66
	v_fmamk_f32 v42, v42, 0x3e0293ee, v66
	v_fmamk_f32 v43, v43, 0x3e0293ee, v66
	v_fmamk_f32 v44, v44, 0x3e0293ee, v66
	v_fmamk_f32 v45, v45, 0x3e0293ee, v66
	v_fmamk_f32 v46, v46, 0x3e0293ee, v66
	v_fmamk_f32 v47, v47, 0x3e0293ee, v66
	v_fmamk_f32 v48, v48, 0x3e0293ee, v66
	v_lshl_add_u64 v[18:19], v[18:19], 0, v[158:159]
	v_exp_f32_e32 v234, v34
	v_exp_f32_e32 v236, v35
	v_exp_f32_e32 v232, v36
	v_exp_f32_e32 v235, v37
	v_exp_f32_e32 v230, v38
	v_exp_f32_e32 v233, v39
	v_exp_f32_e32 v229, v40
	v_exp_f32_e32 v231, v41
	v_exp_f32_e32 v226, v42
	v_exp_f32_e32 v228, v43
	v_exp_f32_e32 v168, v44
	v_exp_f32_e32 v227, v45
	v_exp_f32_e32 v166, v46
	v_exp_f32_e32 v169, v47
	v_exp_f32_e32 v165, v48
	v_exp_f32_e32 v167, v67
	v_lshl_add_u64 v[18:19], s[82:83], 0, v[18:19]
	s_waitcnt vmcnt(4)
	v_lshl_add_u64 v[180:181], v[18:19], 0, s[4:5]
	v_sub_u32_e32 v18, s57, v74
	s_waitcnt vmcnt(7)
	ds_write_b128 v199, v[50:53] offset:16384
	s_waitcnt vmcnt(6)
	ds_write_b128 v200, v[54:57] offset:16384
	s_waitcnt vmcnt(5)
	ds_write_b128 v192, v[58:61] offset:49152
	s_waitcnt vmcnt(4)
	ds_write_b128 v193, v[62:65] offset:49152
	v_subrev_u32_e32 v223, s21, v18
	v_mov_b64_e32 v[64:65], v[16:17]
	v_mov_b64_e32 v[48:49], v[16:17]
	v_mov_b64_e32 v[32:33], v[16:17]
	v_cndmask_b32_e64 v220, v77, 1.0, vcc
	s_sub_i32 s3, s41, 64
	s_movk_i32 s41, 0xffe0
	s_movk_i32 s46, 0xffd0
	s_movk_i32 s47, 0xffef
	s_mov_b64 s[20:21], 0x40000
	v_mov_b64_e32 v[62:63], v[14:15]
	v_mov_b64_e32 v[60:61], v[12:13]
	v_mov_b64_e32 v[58:59], v[10:11]
	v_mov_b64_e32 v[56:57], v[8:9]
	v_mov_b64_e32 v[54:55], v[6:7]
	v_mov_b64_e32 v[52:53], v[4:5]
	v_mov_b64_e32 v[50:51], v[2:3]
	v_mov_b64_e32 v[46:47], v[14:15]
	v_mov_b64_e32 v[44:45], v[12:13]
	v_mov_b64_e32 v[42:43], v[10:11]
	v_mov_b64_e32 v[40:41], v[8:9]
	v_mov_b64_e32 v[38:39], v[6:7]
	v_mov_b64_e32 v[36:37], v[4:5]
	v_mov_b64_e32 v[34:35], v[2:3]
	v_mov_b64_e32 v[30:31], v[14:15]
	v_mov_b64_e32 v[28:29], v[12:13]
	v_mov_b64_e32 v[26:27], v[10:11]
	v_mov_b64_e32 v[24:25], v[8:9]
	v_mov_b64_e32 v[22:23], v[6:7]
	v_mov_b64_e32 v[20:21], v[4:5]
	v_mov_b64_e32 v[18:19], v[2:3]
	s_waitcnt lgkmcnt(0)
	s_barrier

; #define SBAR() __builtin_amdgcn_sched_barrier(0)
; template <int MODE>
; __device__ __forceinline__ void partialSM(f32x16& p0, f32x16& p1, float& m_reg, float& mn, float& alpha) {
;     constexpr float SCALE = Cfg<MODE>::SCALE, C = SCALE * 1.4426950408889634f;
;     float pmax = p0[0];
; #pragma unroll
;     for (int r = 1; r < 16; ++r) pmax = fmaxf(pmax, p0[r]);
; #pragma unroll
;     for (int r = 0; r < 16; ++r) pmax = fmaxf(pmax, p1[r]);
;     { auto rr = __builtin_amdgcn_permlane32_swap(__float_as_uint(pmax), __float_as_uint(pmax), false, false);
;       pmax = fmaxf(__uint_as_float(rr[0]), __uint_as_float(rr[1])); }
;     if (__builtin_expect(__all(pmax - m_reg <= THR / SCALE), 1)) { mn = m_reg; alpha = 1.f; }
;     else { mn = fmaxf(m_reg, pmax); alpha = __builtin_amdgcn_exp2f((m_reg - mn) * C); m_reg = mn; }
;     const float mnC = -mn * C;
; #pragma unroll
;     for (int r = 0; r < 16; ++r) p0[r] = fmaf(p0[r], C, mnC);
; #pragma unroll
;     for (int r = 0; r < 16; ++r) p1[r] = fmaf(p1[r], C, mnC);
; #pragma unroll
;     for (int r = 0; r < 16; ++r) p0[r] = __builtin_amdgcn_exp2f(p0[r]);
; }
; __device__ __forceinline__ void finishSM(f32x16& p0, f32x16& p1, float alpha, float& l_reg, bf16x8& pa0, bf16x8& pa1, bf16x8& pa2, bf16x8& pa3) {
; #pragma unroll
;     for (int r = 0; r < 16; ++r) p1[r] = __builtin_amdgcn_exp2f(p1[r]);
;     float ps = 0;
; #pragma unroll
;     for (int r = 0; r < 16; ++r) ps += p0[r];
; #pragma unroll
;     for (int r = 0; r < 16; ++r) ps += p1[r];
;     { auto rr = __builtin_amdgcn_permlane32_swap(__float_as_uint(ps), __float_as_uint(ps), false, false);
;       ps = __uint_as_float(rr[0]) + __uint_as_float(rr[1]); }
;     l_reg = l_reg * alpha + ps;
;     ...
;     PK4(p0, 0, pa0); PK4(p0, 8, pa1); PK4(p1, 0, pa2); PK4(p1, 8, pa3);
; template <int MODE>
; __device__ __forceinline__ void attn_pass(const bf16_t* __restrict__ Qb, const bf16_t* __restrict__ Kh, const bf16_t* __restrict__ Vh, const int NT, const int kr0, const int g4, const int map,
;                                           LAS unsigned char* lds, f32x16 (&o)[4]) {
;     ...
;         finishSM(pA0, pA1, alA, l_reg, pa0, pa1, pa2, pa3); SBAR();
;         SLOAD(SO, j + 2 < NT ? j + 2 : NT - 1); SBAR();
;         pv_d0(o, vb0, pa0, pa1, pa2, pa3); partialSM<MODE>(pB0, pB1, m_reg, mnB, alB);
.LBB0_465:
	v_add_f32_e32 v68, 0, v234
	v_add_f32_e32 v68, v236, v68
	v_add_f32_e32 v68, v232, v68
	v_add_f32_e32 v68, v235, v68
	v_add_f32_e32 v68, v230, v68
	v_add_f32_e32 v68, v233, v68
	v_add_f32_e32 v68, v229, v68
	v_add_f32_e32 v68, v231, v68
	v_add_f32_e32 v68, v226, v68
	v_add_f32_e32 v68, v228, v68
	v_add_f32_e32 v68, v168, v68
	v_add_f32_e32 v68, v227, v68
	v_exp_f32_e32 v67, v156
	v_add_f32_e32 v68, v166, v68
	v_exp_f32_e32 v72, v157
	v_add_f32_e32 v68, v169, v68
	v_exp_f32_e32 v75, v154
	v_add_f32_e32 v68, v165, v68
	v_exp_f32_e32 v80, v155
	v_add_f32_e32 v68, v167, v68
	v_exp_f32_e32 v100, v152
	v_add_f32_e32 v68, v67, v68
	v_exp_f32_e32 v101, v153
	v_add_f32_e32 v68, v72, v68
	v_exp_f32_e32 v102, v150
	v_add_f32_e32 v68, v75, v68
	v_exp_f32_e32 v103, v151
	v_add_f32_e32 v68, v80, v68
	v_exp_f32_e32 v104, v148
	v_add_f32_e32 v68, v100, v68
	v_exp_f32_e32 v105, v149
	v_add_f32_e32 v68, v101, v68
	v_exp_f32_e32 v106, v146
	v_add_f32_e32 v68, v102, v68
	v_exp_f32_e32 v107, v147
	v_add_f32_e32 v68, v103, v68
	v_exp_f32_e32 v108, v162
	v_add_f32_e32 v68, v104, v68
	v_exp_f32_e32 v109, v163
	v_add_f32_e32 v68, v105, v68
	v_exp_f32_e32 v110, v160
	v_add_f32_e32 v68, v106, v68
	v_exp_f32_e32 v111, v161
	v_add_f32_e32 v68, v107, v68
	v_add_f32_e32 v68, v108, v68
	v_add_f32_e32 v68, v109, v68
	v_add_f32_e32 v68, v110, v68
	v_add_f32_e32 v113, v111, v68
	v_mov_b32_e32 v224, v113
	s_nop 1
	v_permlane32_swap_b32_e32 v113, v224
	v_cvt_pk_bf16_f32 v68, v234, v236
	v_cvt_pk_bf16_f32 v69, v232, v235
	v_cvt_pk_bf16_f32 v70, v230, v233
	v_cvt_pk_bf16_f32 v71, v229, v231
	v_cvt_pk_bf16_f32 v76, v226, v228
	v_cvt_pk_bf16_f32 v77, v168, v227
	v_cvt_pk_bf16_f32 v78, v166, v169
	v_cvt_pk_bf16_f32 v79, v165, v167
	v_cvt_pk_bf16_f32 v98, v67, v72
	v_cvt_pk_bf16_f32 v99, v75, v80
	v_cvt_pk_bf16_f32 v100, v100, v101
	v_cvt_pk_bf16_f32 v101, v102, v103
	v_cvt_pk_bf16_f32 v102, v104, v105
	v_cvt_pk_bf16_f32 v103, v106, v107
	v_cvt_pk_bf16_f32 v104, v108, v109
	v_cvt_pk_bf16_f32 v105, v110, v111
	s_nop 0
	v_permlane32_swap_b32_e32 v68, v70
	v_permlane32_swap_b32_e32 v69, v71
	v_permlane32_swap_b32_e32 v76, v78
	v_permlane32_swap_b32_e32 v77, v79
	v_permlane32_swap_b32_e32 v98, v100
	v_permlane32_swap_b32_e32 v99, v101
	v_permlane32_swap_b32_e32 v102, v104
	v_permlane32_swap_b32_e32 v103, v105
	s_cmp_gt_u32 s6, 1
	s_cselect_b32 s4, s3, 0x10c0
	s_ashr_i32 s5, s4, 31
	v_mov_b32_e32 v107, s5
	v_or_b32_e32 v106, s4, v174
	v_lshlrev_b64 v[106:107], 11, v[106:107]
	v_lshl_add_u64 v[110:111], v[176:177], 0, s[4:5]
	v_or_b32_e32 v106, v106, v190
	v_lshlrev_b64 v[110:111], 11, v[110:111]
	v_lshl_add_u64 v[108:109], s[38:39], 0, v[106:107]
	v_or_b32_e32 v110, v110, v190
	v_lshl_add_u64 v[106:107], s[24:25], 0, v[106:107]
	v_lshl_add_u64 v[114:115], s[38:39], 0, v[110:111]
	global_load_dwordx4 v[146:149], v[108:109], off
	global_load_dwordx4 v[150:153], v[114:115], off
	v_lshl_add_u64 v[108:109], s[24:25], 0, v[110:111]
	global_load_dwordx4 v[154:157], v[106:107], off
	global_load_dwordx4 v[158:161], v[108:109], off
	ds_read_b64_tr_b16 v[106:107], v175 offset:0
	ds_read_b64_tr_b16 v[108:109], v175 offset:0x800
	ds_read_b64_tr_b16 v[114:115], v175 offset:0x1000
	ds_read_b64_tr_b16 v[116:117], v175 offset:0x1800
	ds_read_b64_tr_b16 v[118:119], v175 offset:0x2000
	ds_read_b64_tr_b16 v[120:121], v175 offset:0x2800
	ds_read_b64_tr_b16 v[122:123], v175 offset:0x3000
	ds_read_b64_tr_b16 v[124:125], v175 offset:0x3800
	s_waitcnt lgkmcnt(0)
	s_nop 0
	v_mfma_f32_32x32x16_bf16 v[2:17], v[68:71], v[106:109], v[2:17]
	ds_read_b64_tr_b16 v[106:107], v175 offset:0x200
	ds_read_b64_tr_b16 v[108:109], v175 offset:0xa00
	v_mfma_f32_32x32x16_bf16 v[2:17], v[76:79], v[114:117], v[2:17]
	ds_read_b64_tr_b16 v[114:115], v175 offset:0x1200
	ds_read_b64_tr_b16 v[116:117], v175 offset:0x1a00
	v_mfma_f32_32x32x16_bf16 v[2:17], v[98:101], v[118:121], v[2:17]
	ds_read_b64_tr_b16 v[118:119], v175 offset:0x2200
	ds_read_b64_tr_b16 v[120:121], v175 offset:0x2a00
	ds_read_b64_tr_b16 v[126:127], v175 offset:0x3200
	ds_read_b64_tr_b16 v[128:129], v175 offset:0x3a00
	v_mfma_f32_32x32x16_bf16 v[2:17], v[102:105], v[122:125], v[2:17]
	s_waitcnt lgkmcnt(0)
	v_mfma_f32_32x32x16_bf16 v[50:65], v[68:71], v[106:109], v[50:65]
	ds_read_b64_tr_b16 v[106:107], v175 offset:0x400
	ds_read_b64_tr_b16 v[108:109], v175 offset:0xc00
	v_mfma_f32_32x32x16_bf16 v[50:65], v[76:79], v[114:117], v[50:65]
	ds_read_b64_tr_b16 v[114:115], v175 offset:0x1400
	ds_read_b64_tr_b16 v[116:117], v175 offset:0x1c00
	v_mfma_f32_32x32x16_bf16 v[50:65], v[98:101], v[118:121], v[50:65]
	ds_read_b64_tr_b16 v[118:119], v175 offset:0x2400
	ds_read_b64_tr_b16 v[120:121], v175 offset:0x2c00
	ds_read_b64_tr_b16 v[122:123], v175 offset:0x3400
	ds_read_b64_tr_b16 v[124:125], v175 offset:0x3c00
	v_mfma_f32_32x32x16_bf16 v[50:65], v[102:105], v[126:129], v[50:65]
	s_waitcnt lgkmcnt(0)
	v_mfma_f32_32x32x16_bf16 v[34:49], v[68:71], v[106:109], v[34:49]
	ds_read_b64_tr_b16 v[106:107], v175 offset:0x600
	ds_read_b64_tr_b16 v[108:109], v175 offset:0xe00
	v_mfma_f32_32x32x16_bf16 v[34:49], v[76:79], v[114:117], v[34:49]
	ds_read_b64_tr_b16 v[114:115], v175 offset:0x1600
	ds_read_b64_tr_b16 v[116:117], v175 offset:0x1e00
	v_mfma_f32_32x32x16_bf16 v[34:49], v[98:101], v[118:121], v[34:49]
	ds_read_b64_tr_b16 v[118:119], v175 offset:0x2600
	ds_read_b64_tr_b16 v[120:121], v175 offset:0x2e00
	ds_read_b64_tr_b16 v[126:127], v175 offset:0x3600
	ds_read_b64_tr_b16 v[128:129], v175 offset:0x3e00
	v_mfma_f32_32x32x16_bf16 v[34:49], v[102:105], v[122:125], v[34:49]
	s_waitcnt lgkmcnt(0)
	v_mfma_f32_32x32x16_bf16 v[18:33], v[68:71], v[106:109], v[18:33]
	v_max_f32_e32 v67, v82, v83
	v_max3_f32 v67, v67, v84, v85
	v_max3_f32 v67, v67, v86, v87
	v_max3_f32 v67, v67, v88, v89
	v_max3_f32 v67, v67, v90, v91
	v_max3_f32 v67, v67, v92, v93
	v_mfma_f32_32x32x16_bf16 v[18:33], v[76:79], v[114:117], v[18:33]
	v_max3_f32 v67, v67, v94, v95
	v_max3_f32 v67, v67, v96, v97
	v_max3_f32 v67, v67, v66, v237
	v_max3_f32 v67, v67, v238, v239
	v_max3_f32 v67, v67, v240, v241
	v_max3_f32 v67, v67, v242, v73
	v_max3_f32 v67, v67, v74, v243
	v_max3_f32 v67, v67, v244, v245
	v_mfma_f32_32x32x16_bf16 v[18:33], v[98:101], v[118:121], v[18:33]
	v_max3_f32 v67, v67, v246, v247
	v_max3_f32 v67, v67, v250, v81
	v_mov_b32_e32 v68, v67
	s_nop 1
	v_permlane32_swap_b32_e32 v67, v68
	v_max_f32_e32 v67, v67, v68
	v_sub_f32_e32 v68, v67, v164
	v_max_f32_e32 v67, v164, v67
	v_mfma_f32_32x32x16_bf16 v[18:33], v[102:105], v[126:129], v[18:33]
	v_sub_f32_e32 v69, v164, v67
	v_mul_f32_e32 v69, 0x3e0293ee, v69
	v_exp_f32_e32 v69, v69
	v_cmp_ge_f32_e32 vcc, s7, v68
	s_cmp_eq_u64 vcc, exec
	s_cselect_b64 s[4:5], -1, 0
	s_barrier
; #define SWAIT() do { if constexpr (MODE == 1) asm volatile("s_waitcnt vmcnt(3)" ::: "memory"); else asm volatile("s_waitcnt vmcnt(4)" ::: "memory"); } while (0)
; #define RESC(a) do { if (__any((a) < 1.f)) { if (hi == 0) al_l[r32] = (a); asm volatile("s_waitcnt lgkmcnt(0)" ::: "memory"); \
;     _Pragma("unroll") for (int d = 0; d < 4; ++d) _Pragma("unroll") for (int r = 0; r < 16; ++r) o[d][r] *= al_l[crow(r, hi)]; } } while (0)
; template <int MODE>
; __device__ __forceinline__ void attn_pass(const bf16_t* __restrict__ Qb, const bf16_t* __restrict__ Kh, const bf16_t* __restrict__ Vh, const int NT, const int kr0, const int g4, const int map,
;                                           LAS unsigned char* lds, f32x16 (&o)[4]) {
;     ...
;         __syncthreads(); SWAIT(); SWRITE(0, SE);
;         RESC(alB); __syncthreads();
	s_waitcnt vmcnt(4)
	v_cndmask_b32_e64 v225, v69, 1.0, s[4:5]
	v_cmp_gt_f32_e32 vcc, 1.0, v225
	s_waitcnt vmcnt(4)
	ds_write_b128 v199, v[130:133]
	ds_write_b128 v200, v[134:137]
	ds_write_b128 v192, v[138:141] offset:32768
	ds_write_b128 v193, v[142:145] offset:32768
	s_cbranch_vccz .LBB0_469
	s_and_saveexec_b64 s[42:43], s[0:1]
	ds_write_b32 v171, v225 offset:128
	s_or_b64 exec, exec, s[42:43]
	s_waitcnt lgkmcnt(0)
	ds_read_b128 v[68:71], v207 offset:224
	ds_read_b128 v[76:79], v207 offset:192
	ds_read_b128 v[98:101], v207 offset:160
	ds_read_b128 v[102:105], v207 offset:128
	s_waitcnt lgkmcnt(3)
	v_pk_mul_f32 v[16:17], v[16:17], v[70:71]
	s_waitcnt lgkmcnt(2)
	v_pk_mul_f32 v[12:13], v[12:13], v[78:79]
	s_waitcnt lgkmcnt(1)
	v_pk_mul_f32 v[8:9], v[8:9], v[100:101]
	s_waitcnt lgkmcnt(0)
	v_pk_mul_f32 v[4:5], v[4:5], v[104:105]
	v_pk_mul_f32 v[14:15], v[14:15], v[68:69]
	v_pk_mul_f32 v[10:11], v[10:11], v[76:77]
	v_pk_mul_f32 v[6:7], v[6:7], v[98:99]
	v_pk_mul_f32 v[2:3], v[2:3], v[102:103]
	v_pk_mul_f32 v[64:65], v[64:65], v[70:71]
	v_pk_mul_f32 v[60:61], v[60:61], v[78:79]
	v_pk_mul_f32 v[56:57], v[56:57], v[100:101]
	v_pk_mul_f32 v[52:53], v[52:53], v[104:105]
	v_pk_mul_f32 v[62:63], v[62:63], v[68:69]
	v_pk_mul_f32 v[58:59], v[58:59], v[76:77]
	v_pk_mul_f32 v[54:55], v[54:55], v[98:99]
	v_pk_mul_f32 v[50:51], v[50:51], v[102:103]
	v_pk_mul_f32 v[48:49], v[48:49], v[70:71]
	v_pk_mul_f32 v[44:45], v[44:45], v[78:79]
	v_pk_mul_f32 v[40:41], v[40:41], v[100:101]
	v_pk_mul_f32 v[36:37], v[36:37], v[104:105]
	v_pk_mul_f32 v[46:47], v[46:47], v[68:69]
	v_pk_mul_f32 v[42:43], v[42:43], v[76:77]
	v_pk_mul_f32 v[38:39], v[38:39], v[98:99]
	v_pk_mul_f32 v[34:35], v[34:35], v[102:103]
	v_pk_mul_f32 v[32:33], v[32:33], v[70:71]
	v_pk_mul_f32 v[28:29], v[28:29], v[78:79]
	v_pk_mul_f32 v[24:25], v[24:25], v[100:101]
	v_pk_mul_f32 v[20:21], v[20:21], v[104:105]
	v_pk_mul_f32 v[30:31], v[30:31], v[68:69]
	v_pk_mul_f32 v[26:27], v[26:27], v[76:77]
	v_pk_mul_f32 v[22:23], v[22:23], v[98:99]
	v_pk_mul_f32 v[18:19], v[18:19], v[102:103]

; #define SWAIT() do { if constexpr (MODE == 1) asm volatile("s_waitcnt vmcnt(3)" ::: "memory"); else asm volatile("s_waitcnt vmcnt(4)" ::: "memory"); } while (0)
; #define RESC(a) do { if (__any((a) < 1.f)) { if (hi == 0) al_l[r32] = (a); asm volatile("s_waitcnt lgkmcnt(0)" ::: "memory"); \
;     _Pragma("unroll") for (int d = 0; d < 4; ++d) _Pragma("unroll") for (int r = 0; r < 16; ++r) o[d][r] *= al_l[crow(r, hi)]; } } while (0)
; template <int MODE>
; __device__ __forceinline__ void partialSM(f32x16& p0, f32x16& p1, float& m_reg, float& mn, float& alpha) {
;     constexpr float SCALE = Cfg<MODE>::SCALE, C = SCALE * 1.4426950408889634f;
;     float pmax = p0[0];
; #pragma unroll
;     for (int r = 1; r < 16; ++r) pmax = fmaxf(pmax, p0[r]);
; #pragma unroll
;     for (int r = 0; r < 16; ++r) pmax = fmaxf(pmax, p1[r]);
;     { auto rr = __builtin_amdgcn_permlane32_swap(__float_as_uint(pmax), __float_as_uint(pmax), false, false);
;       pmax = fmaxf(__uint_as_float(rr[0]), __uint_as_float(rr[1])); }
;     if (__builtin_expect(__all(pmax - m_reg <= THR / SCALE), 1)) { mn = m_reg; alpha = 1.f; }
;     else { mn = fmaxf(m_reg, pmax); alpha = __builtin_amdgcn_exp2f((m_reg - mn) * C); m_reg = mn; }
; template <int MODE>
; __device__ __forceinline__ void attn_pass(const bf16_t* __restrict__ Qb, const bf16_t* __restrict__ Kh, const bf16_t* __restrict__ Vh, const int NT, const int kr0, const int g4, const int map,
;                                           LAS unsigned char* lds, f32x16 (&o)[4]) {
;     ...
;         pv_d0(o, vb0 + SHM_V, pa0, pa1, pa2, pa3); partialSM<MODE>(pA0, pA1, m_reg, mnA, alA);
;         __syncthreads(); SWAIT(); SWRITE(1, SO);
;         RESC(alA); __syncthreads();
.LBB0_477:
	ds_read_b64_tr_b16 v[228:229], v173 offset:0
	ds_read_b64_tr_b16 v[230:231], v173 offset:0x800
	ds_read_b64_tr_b16 v[232:233], v173 offset:0x1000
	ds_read_b64_tr_b16 v[234:235], v173 offset:0x1800
	ds_read_b64_tr_b16 v[236:237], v173 offset:0x2000
	ds_read_b64_tr_b16 v[238:239], v173 offset:0x2800
	ds_read_b64_tr_b16 v[240:241], v173 offset:0x3000
	ds_read_b64_tr_b16 v[242:243], v173 offset:0x3800
	s_waitcnt lgkmcnt(0)
	s_nop 0
	v_mfma_f32_32x32x16_bf16 v[2:17], v[68:71], v[228:231], v[2:17]
	ds_read_b64_tr_b16 v[228:229], v173 offset:0x200
	ds_read_b64_tr_b16 v[230:231], v173 offset:0xa00
	v_mfma_f32_32x32x16_bf16 v[2:17], v[76:79], v[232:235], v[2:17]
	ds_read_b64_tr_b16 v[232:233], v173 offset:0x1200
	ds_read_b64_tr_b16 v[234:235], v173 offset:0x1a00
	v_mfma_f32_32x32x16_bf16 v[2:17], v[166:169], v[236:239], v[2:17]
	ds_read_b64_tr_b16 v[236:237], v173 offset:0x2200
	ds_read_b64_tr_b16 v[238:239], v173 offset:0x2a00
	ds_read_b64_tr_b16 v[244:245], v173 offset:0x3200
	ds_read_b64_tr_b16 v[246:247], v173 offset:0x3a00
	v_mfma_f32_32x32x16_bf16 v[2:17], v[162:165], v[240:243], v[2:17]
	s_waitcnt lgkmcnt(0)
	v_mfma_f32_32x32x16_bf16 v[50:65], v[68:71], v[228:231], v[50:65]
	ds_read_b64_tr_b16 v[228:229], v173 offset:0x400
	ds_read_b64_tr_b16 v[230:231], v173 offset:0xc00
	v_mfma_f32_32x32x16_bf16 v[50:65], v[76:79], v[232:235], v[50:65]
	ds_read_b64_tr_b16 v[232:233], v173 offset:0x1400
	ds_read_b64_tr_b16 v[234:235], v173 offset:0x1c00
	v_mfma_f32_32x32x16_bf16 v[50:65], v[166:169], v[236:239], v[50:65]
	ds_read_b64_tr_b16 v[236:237], v173 offset:0x2400
	ds_read_b64_tr_b16 v[238:239], v173 offset:0x2c00
	ds_read_b64_tr_b16 v[240:241], v173 offset:0x3400
	ds_read_b64_tr_b16 v[242:243], v173 offset:0x3c00
	v_mfma_f32_32x32x16_bf16 v[50:65], v[162:165], v[244:247], v[50:65]
	s_waitcnt lgkmcnt(0)
	v_mfma_f32_32x32x16_bf16 v[34:49], v[68:71], v[228:231], v[34:49]
	ds_read_b64_tr_b16 v[228:229], v173 offset:0x600
	ds_read_b64_tr_b16 v[230:231], v173 offset:0xe00
	v_mfma_f32_32x32x16_bf16 v[34:49], v[76:79], v[232:235], v[34:49]
	ds_read_b64_tr_b16 v[232:233], v173 offset:0x1600
	ds_read_b64_tr_b16 v[234:235], v173 offset:0x1e00
	v_mfma_f32_32x32x16_bf16 v[34:49], v[166:169], v[236:239], v[34:49]
	ds_read_b64_tr_b16 v[236:237], v173 offset:0x2600
	ds_read_b64_tr_b16 v[238:239], v173 offset:0x2e00
	ds_read_b64_tr_b16 v[244:245], v173 offset:0x3600
	ds_read_b64_tr_b16 v[246:247], v173 offset:0x3e00
	v_mfma_f32_32x32x16_bf16 v[34:49], v[162:165], v[240:243], v[34:49]
	s_waitcnt lgkmcnt(0)
	v_mfma_f32_32x32x16_bf16 v[18:33], v[68:71], v[228:231], v[18:33]
	v_max_f32_e32 v75, v82, v83
	v_max3_f32 v75, v75, v84, v85
	v_max3_f32 v75, v75, v86, v87
	v_max3_f32 v68, v75, v88, v89
	v_max3_f32 v68, v68, v90, v91
	v_max3_f32 v68, v68, v92, v93
	v_mfma_f32_32x32x16_bf16 v[18:33], v[76:79], v[232:235], v[18:33]
	v_max3_f32 v68, v68, v94, v95
	v_max3_f32 v68, v68, v96, v97
	v_max3_f32 v66, v68, v66, v99
	v_max3_f32 v66, v66, v100, v101
	v_max3_f32 v66, v66, v102, v103
	v_max3_f32 v66, v66, v104, v73
	v_max3_f32 v66, v66, v74, v107
	v_max3_f32 v66, v66, v108, v109
	v_mfma_f32_32x32x16_bf16 v[18:33], v[166:169], v[236:239], v[18:33]
	v_max3_f32 v66, v66, v110, v111
	v_max3_f32 v66, v66, v112, v81
	v_mov_b32_e32 v68, v66
	s_nop 1
	v_permlane32_swap_b32_e32 v66, v68
	v_max_f32_e32 v66, v66, v68
	v_sub_f32_e32 v68, v66, v226
	v_max_f32_e32 v66, v226, v66
	v_mfma_f32_32x32x16_bf16 v[18:33], v[162:165], v[244:247], v[18:33]
	v_sub_f32_e32 v69, v226, v66
	v_mul_f32_e32 v69, 0x3e0293ee, v69
	v_exp_f32_e32 v69, v69
	v_cmp_ge_f32_e32 vcc, s7, v68
	s_cmp_eq_u64 vcc, exec
	s_cselect_b64 s[4:5], -1, 0
	s_barrier
	s_waitcnt vmcnt(4)
	v_cndmask_b32_e64 v98, v69, 1.0, s[4:5]
	v_cmp_gt_f32_e32 vcc, 1.0, v98
	s_waitcnt vmcnt(4)
	ds_write_b128 v199, v[146:149] offset:16384
	s_waitcnt vmcnt(4)
	ds_write_b128 v200, v[150:153] offset:16384
	s_waitcnt vmcnt(4)
	ds_write_b128 v192, v[154:157] offset:49152
	s_waitcnt vmcnt(4)
	ds_write_b128 v193, v[158:161] offset:49152
	s_cbranch_vccz .LBB0_481
	s_and_saveexec_b64 s[44:45], s[0:1]
	ds_write_b32 v171, v98 offset:128
	s_or_b64 exec, exec, s[44:45]
	s_waitcnt lgkmcnt(0)
	ds_read_b128 v[68:71], v207 offset:224
	ds_read_b128 v[74:77], v207 offset:192
	ds_read_b128 v[100:103], v207 offset:160
	ds_read_b128 v[104:107], v207 offset:128
	s_waitcnt lgkmcnt(3)
	v_pk_mul_f32 v[16:17], v[16:17], v[70:71]
	s_waitcnt lgkmcnt(2)
	v_pk_mul_f32 v[12:13], v[12:13], v[76:77]
	s_waitcnt lgkmcnt(1)
	v_pk_mul_f32 v[8:9], v[8:9], v[102:103]
	s_waitcnt lgkmcnt(0)
	v_pk_mul_f32 v[4:5], v[4:5], v[106:107]
	v_pk_mul_f32 v[14:15], v[14:15], v[68:69]
	v_pk_mul_f32 v[10:11], v[10:11], v[74:75]
	v_pk_mul_f32 v[6:7], v[6:7], v[100:101]
	v_pk_mul_f32 v[2:3], v[2:3], v[104:105]
	v_pk_mul_f32 v[64:65], v[64:65], v[70:71]
	v_pk_mul_f32 v[60:61], v[60:61], v[76:77]
	v_pk_mul_f32 v[56:57], v[56:57], v[102:103]
	v_pk_mul_f32 v[52:53], v[52:53], v[106:107]
	v_pk_mul_f32 v[62:63], v[62:63], v[68:69]
	v_pk_mul_f32 v[58:59], v[58:59], v[74:75]
	v_pk_mul_f32 v[54:55], v[54:55], v[100:101]
	v_pk_mul_f32 v[50:51], v[50:51], v[104:105]
	v_pk_mul_f32 v[48:49], v[48:49], v[70:71]
	v_pk_mul_f32 v[44:45], v[44:45], v[76:77]
	v_pk_mul_f32 v[40:41], v[40:41], v[102:103]
	v_pk_mul_f32 v[36:37], v[36:37], v[106:107]
	v_pk_mul_f32 v[46:47], v[46:47], v[68:69]
	v_pk_mul_f32 v[42:43], v[42:43], v[74:75]
	v_pk_mul_f32 v[38:39], v[38:39], v[100:101]
	v_pk_mul_f32 v[34:35], v[34:35], v[104:105]
	v_pk_mul_f32 v[32:33], v[32:33], v[70:71]
	v_pk_mul_f32 v[28:29], v[28:29], v[76:77]
	v_pk_mul_f32 v[24:25], v[24:25], v[102:103]
	v_pk_mul_f32 v[20:21], v[20:21], v[106:107]
	v_pk_mul_f32 v[30:31], v[30:31], v[68:69]
	v_pk_mul_f32 v[26:27], v[26:27], v[74:75]
	v_pk_mul_f32 v[22:23], v[22:23], v[100:101]
	v_pk_mul_f32 v[18:19], v[18:19], v[104:105]

; #define SBAR() __builtin_amdgcn_sched_barrier(0)
; template <int MODE>
; __device__ __forceinline__ void partialSM(f32x16& p0, f32x16& p1, float& m_reg, float& mn, float& alpha) {
;     constexpr float SCALE = Cfg<MODE>::SCALE, C = SCALE * 1.4426950408889634f;
;     float pmax = p0[0];
; #pragma unroll
;     for (int r = 1; r < 16; ++r) pmax = fmaxf(pmax, p0[r]);
; #pragma unroll
;     for (int r = 0; r < 16; ++r) pmax = fmaxf(pmax, p1[r]);
;     { auto rr = __builtin_amdgcn_permlane32_swap(__float_as_uint(pmax), __float_as_uint(pmax), false, false);
;       pmax = fmaxf(__uint_as_float(rr[0]), __uint_as_float(rr[1])); }
;     if (__builtin_expect(__all(pmax - m_reg <= THR / SCALE), 1)) { mn = m_reg; alpha = 1.f; }
;     else { mn = fmaxf(m_reg, pmax); alpha = __builtin_amdgcn_exp2f((m_reg - mn) * C); m_reg = mn; }
;     const float mnC = -mn * C;
; #pragma unroll
;     for (int r = 0; r < 16; ++r) p0[r] = fmaf(p0[r], C, mnC);
; #pragma unroll
;     for (int r = 0; r < 16; ++r) p1[r] = fmaf(p1[r], C, mnC);
; #pragma unroll
;     for (int r = 0; r < 16; ++r) p0[r] = __builtin_amdgcn_exp2f(p0[r]);
; }
; __device__ __forceinline__ void finishSM(f32x16& p0, f32x16& p1, float alpha, float& l_reg, bf16x8& pa0, bf16x8& pa1, bf16x8& pa2, bf16x8& pa3) {
; #pragma unroll
;     for (int r = 0; r < 16; ++r) p1[r] = __builtin_amdgcn_exp2f(p1[r]);
;     float ps = 0;
; #pragma unroll
;     for (int r = 0; r < 16; ++r) ps += p0[r];
; #pragma unroll
;     for (int r = 0; r < 16; ++r) ps += p1[r];
;     { auto rr = __builtin_amdgcn_permlane32_swap(__float_as_uint(ps), __float_as_uint(ps), false, false);
;       ps = __uint_as_float(rr[0]) + __uint_as_float(rr[1]); }
;     l_reg = l_reg * alpha + ps;
;     ...
;     PK4(p0, 0, pa0); PK4(p0, 8, pa1); PK4(p1, 0, pa2); PK4(p1, 8, pa3);
; template <int MODE>
; __device__ __forceinline__ void attn_pass(const bf16_t* __restrict__ Qb, const bf16_t* __restrict__ Kh, const bf16_t* __restrict__ Vh, const int NT, const int kr0, const int g4, const int map,
;                                           LAS unsigned char* lds, f32x16 (&o)[4]) {
;     ...
;     SBAR(); qkt<MODE>(pB0, pB1, K_lds + SHM_K, qr, Qs, r32, hi, cbase); MASK(pB0, pB1, NT - 1);
;     finishSM(pA0, pA1, alA, l_reg, pa0, pa1, pa2, pa3); SBAR();
;     pv_d0(o, vb0, pa0, pa1, pa2, pa3); partialSM<MODE>(pB0, pB1, m_reg, mnB, alB);
;     __syncthreads(); RESC(alB);
.LBB0_485:
	s_or_b64 exec, exec, s[4:5]
	s_nop 7
	v_add_f32_e32 v66, 0, v234
	v_add_f32_e32 v66, v236, v66
	v_add_f32_e32 v66, v232, v66
	v_add_f32_e32 v66, v235, v66
	v_add_f32_e32 v66, v230, v66
	v_add_f32_e32 v66, v233, v66
	v_add_f32_e32 v66, v229, v66
	v_add_f32_e32 v66, v231, v66
	v_add_f32_e32 v66, v226, v66
	v_add_f32_e32 v66, v228, v66
	v_add_f32_e32 v66, v168, v66
	v_add_f32_e32 v66, v227, v66
	v_exp_f32_e32 v76, v156
	v_add_f32_e32 v66, v166, v66
	v_exp_f32_e32 v77, v157
	v_add_f32_e32 v66, v169, v66
	v_exp_f32_e32 v78, v154
	v_add_f32_e32 v66, v165, v66
	v_exp_f32_e32 v79, v155
	v_add_f32_e32 v66, v167, v66
	v_exp_f32_e32 v80, v152
	v_add_f32_e32 v66, v76, v66
	v_exp_f32_e32 v81, v153
	v_add_f32_e32 v66, v77, v66
	v_exp_f32_e32 v82, v150
	v_add_f32_e32 v66, v78, v66
	v_exp_f32_e32 v83, v151
	v_add_f32_e32 v66, v79, v66
	v_exp_f32_e32 v84, v148
	v_add_f32_e32 v66, v80, v66
	v_exp_f32_e32 v85, v149
	v_add_f32_e32 v66, v81, v66
	v_exp_f32_e32 v86, v146
	v_add_f32_e32 v66, v82, v66
	v_exp_f32_e32 v87, v147
	v_add_f32_e32 v66, v83, v66
	v_exp_f32_e32 v88, v162
	v_add_f32_e32 v66, v84, v66
	v_exp_f32_e32 v89, v163
	v_add_f32_e32 v66, v85, v66
	v_exp_f32_e32 v90, v160
	v_add_f32_e32 v66, v86, v66
	v_exp_f32_e32 v91, v161
	v_add_f32_e32 v66, v87, v66
	v_add_f32_e32 v66, v88, v66
	v_add_f32_e32 v66, v89, v66
	v_add_f32_e32 v66, v90, v66
	v_add_f32_e32 v66, v91, v66
	v_mov_b32_e32 v67, v66
	v_cvt_pk_bf16_f32 v68, v234, v236
	v_cvt_pk_bf16_f32 v69, v232, v235
	v_cvt_pk_bf16_f32 v70, v230, v233
	v_cvt_pk_bf16_f32 v71, v229, v231
	v_cvt_pk_bf16_f32 v72, v226, v228
	v_cvt_pk_bf16_f32 v73, v168, v227
	v_cvt_pk_bf16_f32 v74, v166, v169
	v_cvt_pk_bf16_f32 v75, v165, v167
	v_cvt_pk_bf16_f32 v76, v76, v77
	v_cvt_pk_bf16_f32 v77, v78, v79
	v_cvt_pk_bf16_f32 v78, v80, v81
	v_cvt_pk_bf16_f32 v79, v82, v83
	v_cvt_pk_bf16_f32 v80, v84, v85
	v_cvt_pk_bf16_f32 v81, v86, v87
	v_cvt_pk_bf16_f32 v82, v88, v89
	v_cvt_pk_bf16_f32 v83, v90, v91
	s_nop 1
	v_permlane32_swap_b32_e32 v66, v67
	v_permlane32_swap_b32_e32 v68, v70
	v_permlane32_swap_b32_e32 v69, v71
	v_permlane32_swap_b32_e32 v72, v74
	v_permlane32_swap_b32_e32 v73, v75
	v_permlane32_swap_b32_e32 v76, v78
	v_permlane32_swap_b32_e32 v77, v79
	v_permlane32_swap_b32_e32 v80, v82
	v_permlane32_swap_b32_e32 v81, v83
	ds_read_b64_tr_b16 v[84:85], v175 offset:0
	ds_read_b64_tr_b16 v[86:87], v175 offset:0x800
	ds_read_b64_tr_b16 v[88:89], v175 offset:0x1000
	ds_read_b64_tr_b16 v[90:91], v175 offset:0x1800
	ds_read_b64_tr_b16 v[92:93], v175 offset:0x2000
	ds_read_b64_tr_b16 v[94:95], v175 offset:0x2800
	ds_read_b64_tr_b16 v[132:133], v175 offset:0x3000
	ds_read_b64_tr_b16 v[134:135], v175 offset:0x3800
	s_waitcnt lgkmcnt(0)
	s_nop 0
	v_mfma_f32_32x32x16_bf16 v[2:17], v[68:71], v[84:87], v[2:17]
	ds_read_b64_tr_b16 v[84:85], v175 offset:0x200
	ds_read_b64_tr_b16 v[86:87], v175 offset:0xa00
	v_mfma_f32_32x32x16_bf16 v[2:17], v[72:75], v[88:91], v[2:17]
	ds_read_b64_tr_b16 v[88:89], v175 offset:0x1200
	ds_read_b64_tr_b16 v[90:91], v175 offset:0x1a00
	v_mfma_f32_32x32x16_bf16 v[2:17], v[76:79], v[92:95], v[2:17]
	ds_read_b64_tr_b16 v[92:93], v175 offset:0x2200
	ds_read_b64_tr_b16 v[94:95], v175 offset:0x2a00
	ds_read_b64_tr_b16 v[136:137], v175 offset:0x3200
	ds_read_b64_tr_b16 v[138:139], v175 offset:0x3a00
	v_mfma_f32_32x32x16_bf16 v[2:17], v[80:83], v[132:135], v[2:17]
	s_waitcnt lgkmcnt(0)
	v_mfma_f32_32x32x16_bf16 v[50:65], v[68:71], v[84:87], v[50:65]
	ds_read_b64_tr_b16 v[84:85], v175 offset:0x400
	ds_read_b64_tr_b16 v[86:87], v175 offset:0xc00
	v_mfma_f32_32x32x16_bf16 v[50:65], v[72:75], v[88:91], v[50:65]
	ds_read_b64_tr_b16 v[88:89], v175 offset:0x1400
	ds_read_b64_tr_b16 v[90:91], v175 offset:0x1c00
	v_mfma_f32_32x32x16_bf16 v[50:65], v[76:79], v[92:95], v[50:65]
	ds_read_b64_tr_b16 v[92:93], v175 offset:0x2400
	ds_read_b64_tr_b16 v[94:95], v175 offset:0x2c00
	ds_read_b64_tr_b16 v[132:133], v175 offset:0x3400
	ds_read_b64_tr_b16 v[134:135], v175 offset:0x3c00
	v_mfma_f32_32x32x16_bf16 v[50:65], v[80:83], v[136:139], v[50:65]
	s_waitcnt lgkmcnt(0)
	v_mfma_f32_32x32x16_bf16 v[34:49], v[68:71], v[84:87], v[34:49]
	ds_read_b64_tr_b16 v[84:85], v175 offset:0x600
	ds_read_b64_tr_b16 v[86:87], v175 offset:0xe00
	v_mfma_f32_32x32x16_bf16 v[34:49], v[72:75], v[88:91], v[34:49]
	ds_read_b64_tr_b16 v[88:89], v175 offset:0x1600
	ds_read_b64_tr_b16 v[90:91], v175 offset:0x1e00
	v_mfma_f32_32x32x16_bf16 v[34:49], v[76:79], v[92:95], v[34:49]
	ds_read_b64_tr_b16 v[92:93], v175 offset:0x2600
	ds_read_b64_tr_b16 v[94:95], v175 offset:0x2e00
	ds_read_b64_tr_b16 v[136:137], v175 offset:0x3600
	ds_read_b64_tr_b16 v[138:139], v175 offset:0x3e00
	v_mfma_f32_32x32x16_bf16 v[34:49], v[80:83], v[132:135], v[34:49]
	s_waitcnt lgkmcnt(0)
	v_mfma_f32_32x32x16_bf16 v[18:33], v[68:71], v[84:87], v[18:33]
	v_max_f32_e32 v96, v110, v111
	v_max3_f32 v96, v96, v114, v118
	v_max3_f32 v96, v96, v119, v120
	v_max3_f32 v68, v96, v121, v122
	v_max3_f32 v68, v68, v123, v124
	v_max3_f32 v68, v68, v125, v126
	v_mfma_f32_32x32x16_bf16 v[18:33], v[72:75], v[88:91], v[18:33]
	v_max3_f32 v68, v68, v127, v128
	v_max3_f32 v68, v68, v129, v130
	v_max3_f32 v68, v68, v99, v100
	v_max3_f32 v68, v68, v101, v102
	v_max3_f32 v68, v68, v103, v104
	v_max3_f32 v68, v68, v105, v106
	v_max3_f32 v68, v68, v107, v108
	v_max3_f32 v68, v68, v109, v112
	v_mfma_f32_32x32x16_bf16 v[18:33], v[76:79], v[92:95], v[18:33]
	v_max3_f32 v68, v68, v113, v116
	v_max3_f32 v68, v68, v117, v115
	v_mov_b32_e32 v69, v68
	s_nop 1
	v_permlane32_swap_b32_e32 v68, v69
	v_max_f32_e32 v68, v68, v69
	v_max_f32_e32 v70, v164, v68
	v_sub_f32_e32 v69, v68, v164
	v_mfma_f32_32x32x16_bf16 v[18:33], v[80:83], v[136:139], v[18:33]
	v_sub_f32_e32 v68, v164, v70
	s_mov_b32 s3, 0x42b504f3
	v_mul_f32_e32 v68, 0x3e0293ee, v68
	v_exp_f32_e32 v68, v68
	v_cmp_ge_f32_e32 vcc, s3, v69
	s_cmp_eq_u64 vcc, exec
	s_cselect_b64 vcc, -1, 0
	v_cndmask_b32_e32 v69, v70, v164, vcc
	v_cndmask_b32_e64 v68, v68, 1.0, vcc
	v_mul_f32_e32 v69, 0xbe0293ee, v69
	v_fmamk_f32 v70, v110, 0x3e0293ee, v69
	v_fmamk_f32 v71, v111, 0x3e0293ee, v69
	v_fmamk_f32 v72, v114, 0x3e0293ee, v69
	v_fmamk_f32 v73, v118, 0x3e0293ee, v69
	v_fmamk_f32 v74, v119, 0x3e0293ee, v69
	v_fmamk_f32 v75, v120, 0x3e0293ee, v69
	v_fmamk_f32 v76, v121, 0x3e0293ee, v69
	v_fmamk_f32 v77, v122, 0x3e0293ee, v69
	v_fmamk_f32 v78, v123, 0x3e0293ee, v69
	v_fmamk_f32 v79, v124, 0x3e0293ee, v69
	v_fmamk_f32 v80, v125, 0x3e0293ee, v69
	v_fmamk_f32 v81, v126, 0x3e0293ee, v69
	v_fmamk_f32 v82, v127, 0x3e0293ee, v69
	v_fmamk_f32 v83, v128, 0x3e0293ee, v69
	v_fmamk_f32 v84, v129, 0x3e0293ee, v69
	v_fmamk_f32 v85, v130, 0x3e0293ee, v69
	v_cmp_gt_f32_e32 vcc, 1.0, v68
	s_barrier
; #define RESC(a) do { if (__any((a) < 1.f)) { if (hi == 0) al_l[r32] = (a); asm volatile("s_waitcnt lgkmcnt(0)" ::: "memory"); \
;     _Pragma("unroll") for (int d = 0; d < 4; ++d) _Pragma("unroll") for (int r = 0; r < 16; ++r) o[d][r] *= al_l[crow(r, hi)]; } } while (0)
; template <int MODE>
; __device__ __forceinline__ void attn_pass(const bf16_t* __restrict__ Qb, const bf16_t* __restrict__ Kh, const bf16_t* __restrict__ Vh, const int NT, const int kr0, const int g4, const int map,
;                                           LAS unsigned char* lds, f32x16 (&o)[4]) {
;     ...
;     __syncthreads(); RESC(alB);
	s_cbranch_vccz .LBB0_489
	s_and_saveexec_b64 s[4:5], s[0:1]
	ds_write_b32 v171, v68 offset:128
	s_or_b64 exec, exec, s[4:5]
	s_waitcnt lgkmcnt(0)
	v_lshl_add_u32 v110, v187, 2, v1
	ds_read_b128 v[86:89], v110 offset:224
	ds_read_b128 v[90:93], v110 offset:192
	ds_read_b128 v[94:97], v110 offset:160
	ds_read_b128 v[118:121], v110 offset:128
	s_waitcnt lgkmcnt(3)
	v_pk_mul_f32 v[16:17], v[16:17], v[88:89]
	s_waitcnt lgkmcnt(2)
	v_pk_mul_f32 v[12:13], v[12:13], v[92:93]
	s_waitcnt lgkmcnt(1)
	v_pk_mul_f32 v[8:9], v[8:9], v[96:97]
	s_waitcnt lgkmcnt(0)
	v_pk_mul_f32 v[4:5], v[4:5], v[120:121]
	v_pk_mul_f32 v[14:15], v[14:15], v[86:87]
	v_pk_mul_f32 v[10:11], v[10:11], v[90:91]
	v_pk_mul_f32 v[6:7], v[6:7], v[94:95]
	v_pk_mul_f32 v[2:3], v[2:3], v[118:119]
	v_pk_mul_f32 v[64:65], v[64:65], v[88:89]
	v_pk_mul_f32 v[60:61], v[60:61], v[92:93]
	v_pk_mul_f32 v[56:57], v[56:57], v[96:97]
	v_pk_mul_f32 v[52:53], v[52:53], v[120:121]
	v_pk_mul_f32 v[62:63], v[62:63], v[86:87]
	v_pk_mul_f32 v[58:59], v[58:59], v[90:91]
	v_pk_mul_f32 v[54:55], v[54:55], v[94:95]
	v_pk_mul_f32 v[50:51], v[50:51], v[118:119]
	v_pk_mul_f32 v[48:49], v[48:49], v[88:89]
	v_pk_mul_f32 v[44:45], v[44:45], v[92:93]
	v_pk_mul_f32 v[40:41], v[40:41], v[96:97]
	v_pk_mul_f32 v[36:37], v[36:37], v[120:121]
	v_pk_mul_f32 v[46:47], v[46:47], v[86:87]
	v_pk_mul_f32 v[42:43], v[42:43], v[90:91]
	v_pk_mul_f32 v[38:39], v[38:39], v[94:95]
	v_pk_mul_f32 v[34:35], v[34:35], v[118:119]
	v_pk_mul_f32 v[32:33], v[32:33], v[88:89]
	v_pk_mul_f32 v[28:29], v[28:29], v[92:93]
	v_pk_mul_f32 v[24:25], v[24:25], v[96:97]
	v_pk_mul_f32 v[20:21], v[20:21], v[120:121]
	v_pk_mul_f32 v[30:31], v[30:31], v[86:87]
	v_pk_mul_f32 v[26:27], v[26:27], v[90:91]
	v_pk_mul_f32 v[22:23], v[22:23], v[94:95]
	v_pk_mul_f32 v[18:19], v[18:19], v[118:119]
